# write-through stores also for attention Y, residual stream (out-proj epilogues), conv Y and bf16 weight copies
# baseline (speedup 1.0000x reference)
; __device__ __forceinline__ void na_unit(int u, const f16* Z, f16* Y, const float* rpb, LAS unsigned char* lds) {
;     ...
;     const float linv = 1.f / (l + __shfl_xor(l, 32));
;     f16* yr = Y + (size_t)qrow * DM + 64 * head;
; #pragma unroll
;     for (int dt = 0; dt < 2; ++dt)
; #pragma unroll
;         for (int rp = 0; rp < 2; ++rp) { u32x2 w[2];
; #pragma unroll
;             for (int z = 0; z < 2; ++z) { const int rg = 2 * rp + z; w[z].x = pkh(o[dt][4 * rg] * linv, o[dt][4 * rg + 1] * linv); w[z].y = pkh(o[dt][4 * rg + 2] * linv, o[dt][4 * rg + 3] * linv); }
;             store_pair16(yr + 32 * dt + 16 * rp, w[0], w[1], hh); }
;     __syncthreads();
.LBB0_546:
	v_and_b32_e32 v6, 64, v215
	v_xor_b32_e32 v5, 32, v215
	v_add_u32_e32 v6, 64, v6
	v_cmp_lt_i32_e32 vcc, v5, v6
	v_lshlrev_b32_e32 v4, 3, v171
	v_readlane_b32 s76, v250, 23
	v_cndmask_b32_e32 v5, v215, v5, vcc
	v_lshlrev_b32_e32 v5, 2, v5
	ds_bpermute_b32 v5, v5, v84
	v_readlane_b32 s77, v250, 24
	v_readlane_b32 s33, v250, 53
	s_mov_b64 s[34:35], 0x800
	s_waitcnt lgkmcnt(0)
	v_add_f32_e32 v5, v84, v5
	v_div_scale_f32 v6, s[0:1], v5, v5, 1.0
	v_rcp_f32_e32 v7, v6
	v_readlane_b32 s0, v250, 14
	v_readlane_b32 s1, v250, 15
	v_fma_f32 v8, -v6, v7, 1.0
	v_fmac_f32_e32 v7, v8, v7
	v_div_scale_f32 v8, vcc, 1.0, v5, 1.0
	v_mul_f32_e32 v9, v8, v7
	v_fma_f32 v10, -v6, v9, v8
	v_fmac_f32_e32 v9, v10, v7
	v_fma_f32 v6, -v6, v9, v8
	v_div_fmas_f32 v6, v6, v7, v9
	v_div_fixup_f32 v10, v6, v5, 1.0
	v_lshlrev_b64 v[6:7], 11, v[2:3]
	v_lshl_add_u64 v[6:7], s[0:1], 0, v[6:7]
	v_readlane_b32 s0, v250, 54
	v_readlane_b32 s1, v250, 55
	v_lshlrev_b32_e32 v2, 1, v4
	v_mul_f32_e32 v4, v53, v10
	v_lshl_add_u64 v[6:7], s[0:1], 1, v[6:7]
	v_lshl_add_u64 v[8:9], v[6:7], 0, v[2:3]
	v_mul_f32_e32 v2, v52, v10
	v_cvt_pk_f16_f32 v4, v2, v4
	v_mul_f32_e32 v2, v54, v10
	v_mul_f32_e32 v5, v55, v10
	v_cvt_pk_f16_f32 v5, v2, v5
	v_mul_f32_e32 v2, v56, v10
	v_mul_f32_e32 v6, v57, v10
	v_cvt_pk_f16_f32 v6, v2, v6
	v_mul_f32_e32 v2, v58, v10
	v_mul_f32_e32 v7, v59, v10
	v_cvt_pk_f16_f32 v7, v2, v7
	v_permlane32_swap_b32_e32 v4, v6
	s_nop 0
	v_permlane32_swap_b32_e32 v5, v7
	global_store_dwordx4 v[8:9], v[4:7], off sc0 sc1
	v_mul_f32_e32 v2, v60, v10
	s_mov_b64 s[0:1], 0
	v_mul_f32_e32 v4, v61, v10
	v_cvt_pk_f16_f32 v4, v2, v4
	v_mul_f32_e32 v2, v62, v10
	v_mul_f32_e32 v5, v63, v10
	v_cvt_pk_f16_f32 v5, v2, v5
	v_mul_f32_e32 v2, v64, v10
	v_mul_f32_e32 v6, v65, v10
	v_cvt_pk_f16_f32 v6, v2, v6
	v_mul_f32_e32 v2, v66, v10
	v_mul_f32_e32 v7, v67, v10
	v_cvt_pk_f16_f32 v7, v2, v7
	v_permlane32_swap_b32_e32 v4, v6
	s_nop 0
	v_permlane32_swap_b32_e32 v5, v7
	global_store_dwordx4 v[8:9], v[4:7], off offset:32 sc0 sc1
	v_mul_f32_e32 v2, v68, v10
	s_nop 0
	v_mul_f32_e32 v4, v69, v10
	v_cvt_pk_f16_f32 v4, v2, v4
	v_mul_f32_e32 v2, v70, v10
	v_mul_f32_e32 v5, v71, v10
	v_cvt_pk_f16_f32 v5, v2, v5
	v_mul_f32_e32 v2, v72, v10
	v_mul_f32_e32 v6, v73, v10
	v_cvt_pk_f16_f32 v6, v2, v6
	v_mul_f32_e32 v2, v74, v10
	v_mul_f32_e32 v7, v75, v10
	v_cvt_pk_f16_f32 v7, v2, v7
	v_permlane32_swap_b32_e32 v4, v6
	s_nop 0
	v_permlane32_swap_b32_e32 v5, v7
	global_store_dwordx4 v[8:9], v[4:7], off offset:64 sc0 sc1
	v_mul_f32_e32 v2, v76, v10
	s_nop 0
	v_mul_f32_e32 v4, v77, v10
	v_cvt_pk_f16_f32 v4, v2, v4
	v_mul_f32_e32 v2, v78, v10
	v_mul_f32_e32 v5, v79, v10
	v_cvt_pk_f16_f32 v5, v2, v5
	v_mul_f32_e32 v2, v80, v10
	v_mul_f32_e32 v6, v81, v10
	v_cvt_pk_f16_f32 v6, v2, v6
	v_mul_f32_e32 v2, v82, v10
	v_mul_f32_e32 v7, v83, v10
	v_cvt_pk_f16_f32 v7, v2, v7
	v_permlane32_swap_b32_e32 v4, v6
	s_nop 0
	v_permlane32_swap_b32_e32 v5, v7
	global_store_dwordx4 v[8:9], v[4:7], off offset:96 sc0 sc1
	s_barrier

; __device__ __forceinline__ void diff_unit(int u, const f16* Z, f16* Y, const float* subln, float lam, LAS unsigned char* lds) {
;     ...
;     if (map == 0) {
;         float ss = 0.f;
; #pragma unroll
;         for (int dt = 0; dt < 4; ++dt)
; #pragma unroll
;             for (int r = 0; r < 16; ++r) { const float d = o[dt][r] * linv - lam * cb[(dt * 16 + r) * 64 + lane]; o[dt][r] = d; ss += d * d; }
;         ss += __shfl_xor(ss, 32);
.LBB0_574:
	s_cmpk_gt_u32 s11, 0xff
	s_waitcnt lgkmcnt(0)
	s_barrier
	s_cbranch_scc1 .LBB0_576
	ds_read2st64_b32 v[132:133], v2 offset1:1
	ds_read2st64_b32 v[126:127], v2 offset0:2 offset1:3
	ds_read2st64_b32 v[116:117], v2 offset0:4 offset1:5
	ds_read2st64_b32 v[108:109], v2 offset0:6 offset1:7
	ds_read2st64_b32 v[136:137], v2 offset0:8 offset1:9
	ds_read2st64_b32 v[140:141], v2 offset0:10 offset1:11
	ds_read2st64_b32 v[144:145], v2 offset0:12 offset1:13
	ds_read2st64_b32 v[146:147], v2 offset0:14 offset1:15
	ds_read2st64_b32 v[124:125], v2 offset0:16 offset1:17
	ds_read2st64_b32 v[130:131], v2 offset0:18 offset1:19
	ds_read2st64_b32 v[138:139], v2 offset0:20 offset1:21
	ds_read2st64_b32 v[142:143], v2 offset0:22 offset1:23
	ds_read2st64_b32 v[112:113], v2 offset0:24 offset1:25
	ds_read2st64_b32 v[118:119], v2 offset0:26 offset1:27
	ds_read2st64_b32 v[128:129], v2 offset0:28 offset1:29
	ds_read2st64_b32 v[134:135], v2 offset0:30 offset1:31
	ds_read2st64_b32 v[102:103], v2 offset0:32 offset1:33
	ds_read2st64_b32 v[106:107], v2 offset0:34 offset1:35
	ds_read2st64_b32 v[114:115], v2 offset0:36 offset1:37
	ds_read2st64_b32 v[122:123], v2 offset0:38 offset1:39
	ds_read2st64_b32 v[96:97], v2 offset0:40 offset1:41
	ds_read2st64_b32 v[100:101], v2 offset0:42 offset1:43
	ds_read2st64_b32 v[104:105], v2 offset0:44 offset1:45
	ds_read2st64_b32 v[110:111], v2 offset0:46 offset1:47
	ds_read2st64_b32 v[88:89], v2 offset0:48 offset1:49
	ds_read2st64_b32 v[90:91], v2 offset0:50 offset1:51
	ds_read2st64_b32 v[94:95], v2 offset0:52 offset1:53
	ds_read2st64_b32 v[98:99], v2 offset0:54 offset1:55
	ds_read2st64_b32 v[86:87], v2 offset0:56 offset1:57
	ds_read2st64_b32 v[4:5], v2 offset0:58 offset1:59
	v_readlane_b32 s0, v250, 14
	v_readlane_b32 s1, v250, 15
	s_lshl_b32 s86, s10, 1
	s_waitcnt lgkmcnt(0)
	v_pk_mul_f32 v[4:5], v[198:199], v[4:5]
	s_nop 0
	v_pk_fma_f32 v[12:13], v[28:29], v[82:83], v[4:5] op_sel_hi:[1,0,1] neg_lo:[0,0,1] neg_hi:[0,0,1]
	ds_read2st64_b32 v[4:5], v2 offset0:60 offset1:61
	v_pk_mul_f32 v[84:85], v[12:13], v[12:13]
	s_waitcnt lgkmcnt(0)
	v_pk_mul_f32 v[4:5], v[198:199], v[4:5]
	s_nop 0
	v_pk_fma_f32 v[14:15], v[30:31], v[82:83], v[4:5] op_sel_hi:[1,0,1] neg_lo:[0,0,1] neg_hi:[0,0,1]
	ds_read2st64_b32 v[4:5], v2 offset0:62 offset1:63
	v_pk_mul_f32 v[30:31], v[198:199], v[108:109]
	v_lshlrev_b32_e32 v2, 1, v202
	v_pk_mul_f32 v[92:93], v[14:15], v[14:15]
	s_waitcnt lgkmcnt(0)
	v_pk_mul_f32 v[4:5], v[198:199], v[4:5]
	s_nop 0
	v_pk_fma_f32 v[28:29], v[32:33], v[82:83], v[4:5] op_sel_hi:[1,0,1] neg_lo:[0,0,1] neg_hi:[0,0,1]
	v_lshlrev_b32_e32 v83, 2, v216
	v_pk_fma_f32 v[108:109], v[72:73], v[82:83], v[30:31] op_sel_hi:[1,0,1] neg_lo:[0,0,1] neg_hi:[0,0,1]
	v_pk_mul_f32 v[30:31], v[198:199], v[116:117]
	v_lshlrev_b64 v[4:5], 11, v[200:201]
	v_pk_fma_f32 v[116:117], v[70:71], v[82:83], v[30:31] op_sel_hi:[1,0,1] neg_lo:[0,0,1] neg_hi:[0,0,1]
	v_pk_mul_f32 v[30:31], v[198:199], v[126:127]
	v_lshl_add_u64 v[4:5], s[0:1], 0, v[4:5]
	v_pk_fma_f32 v[126:127], v[68:69], v[82:83], v[30:31] op_sel_hi:[1,0,1] neg_lo:[0,0,1] neg_hi:[0,0,1]
	v_pk_mul_f32 v[30:31], v[198:199], v[132:133]
	v_lshl_add_u64 v[4:5], v[4:5], 0, s[86:87]
	v_pk_fma_f32 v[132:133], v[66:67], v[82:83], v[30:31] op_sel_hi:[1,0,1] neg_lo:[0,0,1] neg_hi:[0,0,1]
	v_lshl_add_u64 v[16:17], v[4:5], 0, v[2:3]
	v_pk_mul_f32 v[154:155], v[132:133], v[132:133]
	v_pk_mul_f32 v[152:153], v[126:127], v[126:127]
	v_add_f32_e32 v2, v154, v155
	v_pk_mul_f32 v[30:31], v[198:199], v[146:147]
	v_add_f32_e32 v2, v2, v152
	v_pk_mul_f32 v[150:151], v[116:117], v[116:117]
	v_pk_fma_f32 v[70:71], v[80:81], v[82:83], v[30:31] op_sel_hi:[1,0,1] neg_lo:[0,0,1] neg_hi:[0,0,1]
	v_pk_mul_f32 v[30:31], v[198:199], v[144:145]
	v_add_f32_e32 v2, v2, v153
	v_pk_fma_f32 v[72:73], v[78:79], v[82:83], v[30:31] op_sel_hi:[1,0,1] neg_lo:[0,0,1] neg_hi:[0,0,1]
	v_pk_mul_f32 v[30:31], v[198:199], v[140:141]
	v_add_f32_e32 v2, v2, v150
	v_pk_mul_f32 v[148:149], v[108:109], v[108:109]
	v_pk_fma_f32 v[78:79], v[76:77], v[82:83], v[30:31] op_sel_hi:[1,0,1] neg_lo:[0,0,1] neg_hi:[0,0,1]
	v_pk_mul_f32 v[30:31], v[198:199], v[136:137]
	v_add_f32_e32 v2, v2, v151
	v_pk_fma_f32 v[80:81], v[74:75], v[82:83], v[30:31] op_sel_hi:[1,0,1] neg_lo:[0,0,1] neg_hi:[0,0,1]
	v_add_f32_e32 v2, v2, v148
	v_pk_mul_f32 v[136:137], v[80:81], v[80:81]
	v_add_f32_e32 v2, v2, v149
	v_add_f32_e32 v2, v2, v136
	v_pk_mul_f32 v[140:141], v[78:79], v[78:79]
	v_add_f32_e32 v2, v2, v137
	v_pk_mul_f32 v[30:31], v[198:199], v[142:143]
	v_add_f32_e32 v2, v2, v140
	v_pk_mul_f32 v[144:145], v[72:73], v[72:73]
	v_pk_fma_f32 v[66:67], v[56:57], v[82:83], v[30:31] op_sel_hi:[1,0,1] neg_lo:[0,0,1] neg_hi:[0,0,1]
	v_pk_mul_f32 v[30:31], v[198:199], v[138:139]
	v_add_f32_e32 v2, v2, v141
	v_pk_fma_f32 v[68:69], v[54:55], v[82:83], v[30:31] op_sel_hi:[1,0,1] neg_lo:[0,0,1] neg_hi:[0,0,1]
	v_pk_mul_f32 v[30:31], v[198:199], v[130:131]
	v_add_f32_e32 v2, v2, v144
	v_pk_mul_f32 v[146:147], v[70:71], v[70:71]
	v_pk_fma_f32 v[74:75], v[52:53], v[82:83], v[30:31] op_sel_hi:[1,0,1] neg_lo:[0,0,1] neg_hi:[0,0,1]
	v_pk_mul_f32 v[30:31], v[198:199], v[124:125]
	v_add_f32_e32 v2, v2, v145
	v_pk_fma_f32 v[76:77], v[50:51], v[82:83], v[30:31] op_sel_hi:[1,0,1] neg_lo:[0,0,1] neg_hi:[0,0,1]
	v_add_f32_e32 v2, v2, v146
	v_pk_mul_f32 v[124:125], v[76:77], v[76:77]
	v_add_f32_e32 v2, v2, v147
	v_add_f32_e32 v2, v2, v124
	v_pk_mul_f32 v[130:131], v[74:75], v[74:75]
	v_add_f32_e32 v2, v2, v125
	v_pk_mul_f32 v[30:31], v[198:199], v[134:135]
	v_add_f32_e32 v2, v2, v130
	v_readlane_b32 s0, v251, 12
	v_pk_mul_f32 v[138:139], v[68:69], v[68:69]
; __device__ __forceinline__ void diff_unit(int u, const f16* Z, f16* Y, const float* subln, float lam, LAS unsigned char* lds) {
;     ...
;         for (int dt = 0; dt < 4; ++dt)
; #pragma unroll
;             for (int r = 0; r < 16; ++r) { const float d = o[dt][r] * linv - lam * cb[(dt * 16 + r) * 64 + lane]; o[dt][r] = d; ss += d * d; }
;         ss += __shfl_xor(ss, 32);
;         const float rstd = 0.8f / sqrtf(ss * (1.f / 128.f) + EPS);
;         f16* yr = Y + (size_t)qrow * DM + 512 + 128 * h;
; #pragma unroll
;         for (int dt = 0; dt < 4; ++dt)
; #pragma unroll
;             for (int rp = 0; rp < 2; ++rp) { u32x2 w[2];
; #pragma unroll
;                 for (int z = 0; z < 2; ++z) { const int rg = 2 * rp + z, d0 = 32 * dt + 8 * rg + 4 * hh; const f32x4 sg = *(const f32x4*)(subln + d0);
;                     w[z].x = pkh(o[dt][4 * rg] * rstd * sg[0], o[dt][4 * rg + 1] * rstd * sg[1]); w[z].y = pkh(o[dt][4 * rg + 2] * rstd * sg[2], o[dt][4 * rg + 3] * rstd * sg[3]); }
	v_pk_fma_f32 v[54:55], v[64:65], v[82:83], v[30:31] op_sel_hi:[1,0,1] neg_lo:[0,0,1] neg_hi:[0,0,1]
	v_pk_mul_f32 v[30:31], v[198:199], v[128:129]
	v_add_f32_e32 v2, v2, v131
	v_readlane_b32 s12, v251, 24
	v_readlane_b32 s13, v251, 25
	v_pk_fma_f32 v[62:63], v[62:63], v[82:83], v[30:31] op_sel_hi:[1,0,1] neg_lo:[0,0,1] neg_hi:[0,0,1]
	v_pk_mul_f32 v[30:31], v[198:199], v[118:119]
	v_add_f32_e32 v2, v2, v138
	s_nop 1
	global_load_dwordx4 v[8:11], v83, s[12:13]
	global_load_dwordx4 v[4:7], v83, s[12:13] offset:32
	v_pk_mul_f32 v[142:143], v[66:67], v[66:67]
	v_pk_fma_f32 v[60:61], v[60:61], v[82:83], v[30:31] op_sel_hi:[1,0,1] neg_lo:[0,0,1] neg_hi:[0,0,1]
	v_pk_mul_f32 v[30:31], v[198:199], v[112:113]
	v_add_f32_e32 v2, v2, v139
	v_pk_fma_f32 v[58:59], v[58:59], v[82:83], v[30:31] op_sel_hi:[1,0,1] neg_lo:[0,0,1] neg_hi:[0,0,1]
	v_add_f32_e32 v2, v2, v142
	v_pk_mul_f32 v[112:113], v[58:59], v[58:59]
	v_add_f32_e32 v2, v2, v143
	v_add_f32_e32 v2, v2, v112
	v_pk_mul_f32 v[118:119], v[60:61], v[60:61]
	v_add_f32_e32 v2, v2, v113
	v_pk_mul_f32 v[30:31], v[198:199], v[122:123]
	v_add_f32_e32 v2, v2, v118
	v_pk_mul_f32 v[128:129], v[62:63], v[62:63]
	v_pk_fma_f32 v[40:41], v[40:41], v[82:83], v[30:31] op_sel_hi:[1,0,1] neg_lo:[0,0,1] neg_hi:[0,0,1]
	v_pk_mul_f32 v[30:31], v[198:199], v[114:115]
	v_add_f32_e32 v2, v2, v119
	v_pk_fma_f32 v[50:51], v[38:39], v[82:83], v[30:31] op_sel_hi:[1,0,1] neg_lo:[0,0,1] neg_hi:[0,0,1]
	v_pk_mul_f32 v[30:31], v[198:199], v[106:107]
	v_add_f32_e32 v2, v2, v128
	v_pk_mul_f32 v[64:65], v[54:55], v[54:55]
	v_pk_fma_f32 v[52:53], v[36:37], v[82:83], v[30:31] op_sel_hi:[1,0,1] neg_lo:[0,0,1] neg_hi:[0,0,1]
	v_pk_mul_f32 v[30:31], v[198:199], v[102:103]
	v_add_f32_e32 v2, v2, v129
	v_pk_fma_f32 v[56:57], v[34:35], v[82:83], v[30:31] op_sel_hi:[1,0,1] neg_lo:[0,0,1] neg_hi:[0,0,1]
	v_add_f32_e32 v2, v2, v64
	v_pk_mul_f32 v[102:103], v[56:57], v[56:57]
	v_add_f32_e32 v2, v2, v65
	v_add_f32_e32 v2, v2, v102
	v_pk_mul_f32 v[106:107], v[52:53], v[52:53]
	v_add_f32_e32 v2, v2, v103
	v_add_f32_e32 v2, v2, v106
	v_pk_mul_f32 v[114:115], v[50:51], v[50:51]
	v_pk_mul_f32 v[32:33], v[198:199], v[104:105]
	v_add_f32_e32 v2, v2, v107
	v_pk_fma_f32 v[34:35], v[46:47], v[82:83], v[32:33] op_sel_hi:[1,0,1] neg_lo:[0,0,1] neg_hi:[0,0,1]
	v_pk_mul_f32 v[32:33], v[198:199], v[100:101]
	v_add_f32_e32 v2, v2, v114
	v_pk_mul_f32 v[122:123], v[40:41], v[40:41]
	v_pk_fma_f32 v[36:37], v[44:45], v[82:83], v[32:33] op_sel_hi:[1,0,1] neg_lo:[0,0,1] neg_hi:[0,0,1]
	v_pk_mul_f32 v[32:33], v[198:199], v[96:97]
	v_add_f32_e32 v2, v2, v115
	v_pk_fma_f32 v[38:39], v[42:43], v[82:83], v[32:33] op_sel_hi:[1,0,1] neg_lo:[0,0,1] neg_hi:[0,0,1]
	v_add_f32_e32 v2, v2, v122
	v_pk_mul_f32 v[42:43], v[38:39], v[38:39]
	v_add_f32_e32 v2, v2, v123
	v_add_f32_e32 v2, v2, v42
	v_pk_mul_f32 v[44:45], v[36:37], v[36:37]
	v_add_f32_e32 v2, v2, v43
	v_pk_mul_f32 v[32:33], v[198:199], v[98:99]
	v_add_f32_e32 v2, v2, v44
	v_pk_mul_f32 v[30:31], v[198:199], v[110:111]
	v_pk_mul_f32 v[46:47], v[34:35], v[34:35]
	v_pk_fma_f32 v[24:25], v[24:25], v[82:83], v[32:33] op_sel_hi:[1,0,1] neg_lo:[0,0,1] neg_hi:[0,0,1]
	v_pk_mul_f32 v[32:33], v[198:199], v[94:95]
	v_add_f32_e32 v2, v2, v45
	v_pk_fma_f32 v[30:31], v[48:49], v[82:83], v[30:31] op_sel_hi:[1,0,1] neg_lo:[0,0,1] neg_hi:[0,0,1]
	v_pk_fma_f32 v[22:23], v[22:23], v[82:83], v[32:33] op_sel_hi:[1,0,1] neg_lo:[0,0,1] neg_hi:[0,0,1]
	v_pk_mul_f32 v[32:33], v[198:199], v[90:91]
	v_add_f32_e32 v2, v2, v46
	v_pk_mul_f32 v[48:49], v[30:31], v[30:31]
	v_pk_fma_f32 v[20:21], v[20:21], v[82:83], v[32:33] op_sel_hi:[1,0,1] neg_lo:[0,0,1] neg_hi:[0,0,1]
	v_pk_mul_f32 v[32:33], v[198:199], v[88:89]
	v_add_f32_e32 v2, v2, v47
	v_pk_fma_f32 v[32:33], v[18:19], v[82:83], v[32:33] op_sel_hi:[1,0,1] neg_lo:[0,0,1] neg_hi:[0,0,1]
	v_add_f32_e32 v2, v2, v48
	v_pk_mul_f32 v[88:89], v[32:33], v[32:33]
	v_add_f32_e32 v2, v2, v49
	v_add_f32_e32 v2, v2, v88
	v_pk_mul_f32 v[90:91], v[20:21], v[20:21]
	v_add_f32_e32 v2, v2, v89
	v_add_f32_e32 v2, v2, v90
	v_pk_mul_f32 v[94:95], v[22:23], v[22:23]
	v_add_f32_e32 v2, v2, v91
	v_add_f32_e32 v2, v2, v94
	v_pk_mul_f32 v[96:97], v[24:25], v[24:25]
	v_pk_mul_f32 v[18:19], v[198:199], v[86:87]
	v_add_f32_e32 v2, v2, v95
	v_pk_fma_f32 v[18:19], v[26:27], v[82:83], v[18:19] op_sel_hi:[1,0,1] neg_lo:[0,0,1] neg_hi:[0,0,1]
	v_add_f32_e32 v2, v2, v96
	v_pk_mul_f32 v[26:27], v[18:19], v[18:19]
	v_add_f32_e32 v2, v2, v97
	v_add_f32_e32 v2, v2, v26
	v_add_f32_e32 v2, v2, v27
	v_add_f32_e32 v2, v2, v84
	v_add_f32_e32 v2, v2, v85
	v_add_f32_e32 v2, v2, v92
	v_pk_mul_f32 v[120:121], v[28:29], v[28:29]
	v_add_f32_e32 v2, v2, v93
	v_add_f32_e32 v2, v2, v120
	v_add_f32_e32 v2, v2, v121
	ds_bpermute_b32 v26, v217, v2
	s_mov_b32 s0, 0xf800000
	v_readlane_b32 s1, v251, 13
	v_readlane_b32 s2, v251, 14
	s_mov_b32 s2, 0x3f4ccccd
	s_waitcnt lgkmcnt(0)
	v_add_f32_e32 v2, v2, v26
	v_fmamk_f32 v2, v2, 0x3c000000, v1
	v_cmp_gt_f32_e32 vcc, s0, v2
	v_mul_f32_e32 v26, 0x4f800000, v2
	v_readlane_b32 s3, v251, 15
	v_cndmask_b32_e32 v2, v2, v26, vcc
	v_sqrt_f32_e32 v26, v2
	v_readlane_b32 s4, v251, 16
	v_readlane_b32 s5, v251, 17
	v_readlane_b32 s6, v251, 18
	v_add_u32_e32 v27, -1, v26
	v_fma_f32 v42, -v27, v26, v2
	v_cmp_ge_f32_e64 s[0:1], 0, v42
	v_add_u32_e32 v42, 1, v26
	v_readlane_b32 s7, v251, 19
	v_cndmask_b32_e64 v27, v26, v27, s[0:1]
	v_fma_f32 v26, -v42, v26, v2
	v_cmp_lt_f32_e64 s[0:1], 0, v26
	v_readlane_b32 s8, v251, 20
	v_readlane_b32 s9, v251, 21
	v_cndmask_b32_e64 v26, v27, v42, s[0:1]
	v_mul_f32_e32 v27, 0x37800000, v26
	v_cndmask_b32_e32 v26, v26, v27, vcc
	v_cmp_class_f32_e32 vcc, v2, v203
	v_readlane_b32 s10, v251, 22
	v_readlane_b32 s11, v251, 23
	v_cndmask_b32_e32 v2, v26, v2, vcc
	v_div_scale_f32 v26, s[0:1], v2, v2, s2
	v_rcp_f32_e32 v27, v26
	v_readlane_b32 s14, v251, 26
	v_readlane_b32 s15, v251, 27
	v_fma_f32 v42, -v26, v27, 1.0
	v_fmac_f32_e32 v27, v42, v27
	v_div_scale_f32 v42, vcc, s2, v2, s2
	v_mul_f32_e32 v43, v42, v27
	v_fma_f32 v44, -v26, v43, v42
	v_fmac_f32_e32 v43, v44, v27
	v_fma_f32 v26, -v26, v43, v42
	v_div_fmas_f32 v26, v26, v27, v43
	v_div_fixup_f32 v2, v26, v2, s2
	v_pk_mul_f32 v[26:27], v[132:133], v[2:3] op_sel_hi:[1,0]
	s_waitcnt vmcnt(1)
; __device__ __forceinline__ void diff_unit(int u, const f16* Z, f16* Y, const float* subln, float lam, LAS unsigned char* lds) {
;     ...
;         f16* yr = Y + (size_t)qrow * DM + 512 + 128 * h;
; #pragma unroll
;         for (int dt = 0; dt < 4; ++dt)
; #pragma unroll
;             for (int rp = 0; rp < 2; ++rp) { u32x2 w[2];
; #pragma unroll
;                 for (int z = 0; z < 2; ++z) { const int rg = 2 * rp + z, d0 = 32 * dt + 8 * rg + 4 * hh; const f32x4 sg = *(const f32x4*)(subln + d0);
;                     w[z].x = pkh(o[dt][4 * rg] * rstd * sg[0], o[dt][4 * rg + 1] * rstd * sg[1]); w[z].y = pkh(o[dt][4 * rg + 2] * rstd * sg[2], o[dt][4 * rg + 3] * rstd * sg[3]); }
;                 store_pair16(yr + 32 * dt + 16 * rp, w[0], w[1], hh); }
	v_pk_mul_f32 v[8:9], v[8:9], v[26:27]
	v_pk_mul_f32 v[26:27], v[126:127], v[2:3] op_sel_hi:[1,0]
	v_cvt_pk_f16_f32 v8, v8, v9
	v_pk_mul_f32 v[10:11], v[10:11], v[26:27]
	s_nop 0
	v_cvt_pk_f16_f32 v9, v10, v11
	v_pk_mul_f32 v[10:11], v[116:117], v[2:3] op_sel_hi:[1,0]
	s_waitcnt vmcnt(0)
	v_pk_mul_f32 v[4:5], v[4:5], v[10:11]
	s_nop 0
	v_cvt_pk_f16_f32 v10, v4, v5
	v_pk_mul_f32 v[4:5], v[108:109], v[2:3] op_sel_hi:[1,0]
	s_nop 0
	v_permlane32_swap_b32_e32 v8, v10
	v_pk_mul_f32 v[4:5], v[6:7], v[4:5]
	s_nop 0
	v_cvt_pk_f16_f32 v11, v4, v5
	s_nop 1
	v_permlane32_swap_b32_e32 v9, v11
	global_store_dwordx4 v[16:17], v[8:11], off offset:1024 sc0 sc1
	global_load_dwordx4 v[4:7], v83, s[12:13] offset:64
	s_nop 0
	v_pk_mul_f32 v[8:9], v[80:81], v[2:3] op_sel_hi:[1,0]
	v_pk_mul_f32 v[10:11], v[72:73], v[2:3] op_sel_hi:[1,0]
	s_waitcnt vmcnt(0)
	v_pk_mul_f32 v[4:5], v[4:5], v[8:9]
	v_pk_mul_f32 v[8:9], v[78:79], v[2:3] op_sel_hi:[1,0]
	v_cvt_pk_f16_f32 v4, v4, v5
	v_pk_mul_f32 v[6:7], v[6:7], v[8:9]
	s_nop 0
	v_cvt_pk_f16_f32 v5, v6, v7
	global_load_dwordx4 v[6:9], v83, s[12:13] offset:96
	s_waitcnt vmcnt(0)
	v_pk_mul_f32 v[6:7], v[6:7], v[10:11]
	v_pk_mul_f32 v[10:11], v[70:71], v[2:3] op_sel_hi:[1,0]
	v_cvt_pk_f16_f32 v6, v6, v7
	v_pk_mul_f32 v[8:9], v[8:9], v[10:11]
	s_nop 0
	v_permlane32_swap_b32_e32 v4, v6
	v_cvt_pk_f16_f32 v7, v8, v9
	s_nop 1
	v_permlane32_swap_b32_e32 v5, v7
	global_store_dwordx4 v[16:17], v[4:7], off offset:1056 sc0 sc1
	global_load_dwordx4 v[4:7], v83, s[12:13] offset:128
	v_pk_mul_f32 v[8:9], v[76:77], v[2:3] op_sel_hi:[1,0]
	v_pk_mul_f32 v[10:11], v[68:69], v[2:3] op_sel_hi:[1,0]
	s_waitcnt vmcnt(0)
	v_pk_mul_f32 v[4:5], v[8:9], v[4:5]
	v_pk_mul_f32 v[8:9], v[74:75], v[2:3] op_sel_hi:[1,0]
	v_cvt_pk_f16_f32 v4, v4, v5
	v_pk_mul_f32 v[6:7], v[8:9], v[6:7]
	s_nop 0
	v_cvt_pk_f16_f32 v5, v6, v7
	global_load_dwordx4 v[6:9], v83, s[12:13] offset:160
	s_waitcnt vmcnt(0)
	v_pk_mul_f32 v[6:7], v[10:11], v[6:7]
	v_pk_mul_f32 v[10:11], v[66:67], v[2:3] op_sel_hi:[1,0]
	v_cvt_pk_f16_f32 v6, v6, v7
	v_pk_mul_f32 v[8:9], v[10:11], v[8:9]
	s_nop 0
	v_permlane32_swap_b32_e32 v4, v6
	v_cvt_pk_f16_f32 v7, v8, v9
	s_nop 1
	v_permlane32_swap_b32_e32 v5, v7
	global_store_dwordx4 v[16:17], v[4:7], off offset:1088 sc0 sc1
	global_load_dwordx4 v[4:7], v83, s[12:13] offset:192
	v_pk_mul_f32 v[8:9], v[58:59], v[2:3] op_sel_hi:[1,0]
	v_pk_mul_f32 v[10:11], v[62:63], v[2:3] op_sel_hi:[1,0]
	s_waitcnt vmcnt(0)
	v_pk_mul_f32 v[4:5], v[8:9], v[4:5]
	v_pk_mul_f32 v[8:9], v[60:61], v[2:3] op_sel_hi:[1,0]
	v_cvt_pk_f16_f32 v4, v4, v5
	v_pk_mul_f32 v[6:7], v[8:9], v[6:7]
	s_nop 0
	v_cvt_pk_f16_f32 v5, v6, v7
	global_load_dwordx4 v[6:9], v83, s[12:13] offset:224
	s_waitcnt vmcnt(0)
	v_pk_mul_f32 v[6:7], v[10:11], v[6:7]
	v_pk_mul_f32 v[10:11], v[54:55], v[2:3] op_sel_hi:[1,0]
	v_cvt_pk_f16_f32 v6, v6, v7
	v_pk_mul_f32 v[8:9], v[10:11], v[8:9]
	s_nop 0
	v_permlane32_swap_b32_e32 v4, v6
	v_cvt_pk_f16_f32 v7, v8, v9
	s_nop 1
	v_permlane32_swap_b32_e32 v5, v7
	global_store_dwordx4 v[16:17], v[4:7], off offset:1120 sc0 sc1
	global_load_dwordx4 v[4:7], v83, s[12:13] offset:256
	v_pk_mul_f32 v[8:9], v[56:57], v[2:3] op_sel_hi:[1,0]
	v_pk_mul_f32 v[10:11], v[50:51], v[2:3] op_sel_hi:[1,0]
	s_waitcnt vmcnt(0)
	v_pk_mul_f32 v[4:5], v[8:9], v[4:5]
	v_pk_mul_f32 v[8:9], v[52:53], v[2:3] op_sel_hi:[1,0]
	v_cvt_pk_f16_f32 v4, v4, v5
	v_pk_mul_f32 v[6:7], v[8:9], v[6:7]
	s_nop 0
	v_cvt_pk_f16_f32 v5, v6, v7
	global_load_dwordx4 v[6:9], v83, s[12:13] offset:288
	s_waitcnt vmcnt(0)
	v_pk_mul_f32 v[6:7], v[10:11], v[6:7]
	v_pk_mul_f32 v[10:11], v[40:41], v[2:3] op_sel_hi:[1,0]
	v_cvt_pk_f16_f32 v6, v6, v7
	v_pk_mul_f32 v[8:9], v[10:11], v[8:9]
	s_nop 0
	v_permlane32_swap_b32_e32 v4, v6
	v_cvt_pk_f16_f32 v7, v8, v9
	s_nop 1
	v_permlane32_swap_b32_e32 v5, v7
	global_store_dwordx4 v[16:17], v[4:7], off offset:1152 sc0 sc1
	global_load_dwordx4 v[4:7], v83, s[12:13] offset:320
	v_pk_mul_f32 v[8:9], v[38:39], v[2:3] op_sel_hi:[1,0]
	v_pk_mul_f32 v[10:11], v[34:35], v[2:3] op_sel_hi:[1,0]
	s_waitcnt vmcnt(0)
	v_pk_mul_f32 v[4:5], v[8:9], v[4:5]
	v_pk_mul_f32 v[8:9], v[36:37], v[2:3] op_sel_hi:[1,0]
	v_cvt_pk_f16_f32 v4, v4, v5
	v_pk_mul_f32 v[6:7], v[8:9], v[6:7]
	s_nop 0
	v_cvt_pk_f16_f32 v5, v6, v7
	global_load_dwordx4 v[6:9], v83, s[12:13] offset:352
	s_waitcnt vmcnt(0)
	v_pk_mul_f32 v[6:7], v[10:11], v[6:7]
	v_pk_mul_f32 v[10:11], v[30:31], v[2:3] op_sel_hi:[1,0]
	v_cvt_pk_f16_f32 v6, v6, v7
	v_pk_mul_f32 v[8:9], v[10:11], v[8:9]
	s_nop 0
	v_permlane32_swap_b32_e32 v4, v6
	v_cvt_pk_f16_f32 v7, v8, v9
	s_nop 1
	v_permlane32_swap_b32_e32 v5, v7
	global_store_dwordx4 v[16:17], v[4:7], off offset:1184 sc0 sc1
	global_load_dwordx4 v[4:7], v83, s[12:13] offset:384
	v_pk_mul_f32 v[8:9], v[32:33], v[2:3] op_sel_hi:[1,0]
	v_pk_mul_f32 v[10:11], v[22:23], v[2:3] op_sel_hi:[1,0]
	s_waitcnt vmcnt(0)
	v_pk_mul_f32 v[4:5], v[8:9], v[4:5]
	v_pk_mul_f32 v[8:9], v[20:21], v[2:3] op_sel_hi:[1,0]
	v_cvt_pk_f16_f32 v4, v4, v5
	v_pk_mul_f32 v[6:7], v[8:9], v[6:7]
	s_nop 0
	v_cvt_pk_f16_f32 v5, v6, v7
	global_load_dwordx4 v[6:9], v83, s[12:13] offset:416
	s_waitcnt vmcnt(0)
	v_pk_mul_f32 v[6:7], v[10:11], v[6:7]
	v_pk_mul_f32 v[10:11], v[24:25], v[2:3] op_sel_hi:[1,0]
	v_cvt_pk_f16_f32 v6, v6, v7
	v_pk_mul_f32 v[8:9], v[10:11], v[8:9]
	s_nop 0
	v_permlane32_swap_b32_e32 v4, v6
	v_cvt_pk_f16_f32 v7, v8, v9
	s_nop 1
	v_permlane32_swap_b32_e32 v5, v7
	global_store_dwordx4 v[16:17], v[4:7], off offset:1216 sc0 sc1
	global_load_dwordx4 v[4:7], v83, s[12:13] offset:448
	v_pk_mul_f32 v[8:9], v[18:19], v[2:3] op_sel_hi:[1,0]
	v_pk_mul_f32 v[10:11], v[14:15], v[2:3] op_sel_hi:[1,0]
	s_waitcnt vmcnt(0)
	v_pk_mul_f32 v[4:5], v[8:9], v[4:5]
	v_pk_mul_f32 v[8:9], v[12:13], v[2:3] op_sel_hi:[1,0]
	v_cvt_pk_f16_f32 v4, v4, v5
	v_pk_mul_f32 v[6:7], v[8:9], v[6:7]
	s_nop 0
	v_cvt_pk_f16_f32 v5, v6, v7
	global_load_dwordx4 v[6:9], v83, s[12:13] offset:480
	s_waitcnt vmcnt(0)
	v_pk_mul_f32 v[6:7], v[10:11], v[6:7]
	v_pk_mul_f32 v[10:11], v[28:29], v[2:3] op_sel_hi:[1,0]
	v_cvt_pk_f16_f32 v6, v6, v7
	v_pk_mul_f32 v[8:9], v[10:11], v[8:9]
	s_nop 0
	v_permlane32_swap_b32_e32 v4, v6
	v_cvt_pk_f16_f32 v7, v8, v9
	s_nop 1
	v_permlane32_swap_b32_e32 v5, v7
	global_store_dwordx4 v[16:17], v[4:7], off offset:1248 sc0 sc1

; template <bool BF> __device__ __forceinline__ unsigned pk16(float lo, float hi) { return BF ? pkb(lo, hi) : pkh(lo, hi); }
;     static __device__ __forceinline__ void store(const CvItem& d, int tid, const f32x4 (&v)[2][8]) {
;         const int lane = tid & 63, wave = tid >> 6, kg = lane >> 3, ng = lane & 7; const int nblk = d.N / 128, kb = d.r / nblk, nb = d.r % nblk;
; #pragma unroll
;         for (int t = 0; t < 2; ++t) { const int sb = 2 * wave + t, k0 = 256 * kb + 64 * (sb >> 2) + 8 * kg, n0 = 128 * nb + 32 * (sb & 3) + 4 * ng;
; #pragma unroll
;             for (int j = 0; j < 4; ++j) { u32x4 w; w.x = pk16<MOE_BF16>(v[t][0][j], v[t][1][j]); w.y = pk16<MOE_BF16>(v[t][2][j], v[t][3][j]); w.z = pk16<MOE_BF16>(v[t][4][j], v[t][5][j]); w.w = pk16<MOE_BF16>(v[t][6][j], v[t][7][j]);
;                 const int n = n0 + j, row = d.add >= 0 ? (n >> 7) * 256 + (n & 127) + d.add : n;
;                 *(u32x4*)(d.WT + (size_t)row * d.K + k0) = w; } } }
;     __device__ __forceinline__ void run_all(int tid) const {
;     ...
;             const CvItem d0 = decode(it); load(d0, tid, va);
;             const bool two = it + 1 < it_hi; const CvItem d1 = decode(two ? it + 1 : it);
;             if (two) load(d1, tid, vb);
;             store(d0, tid, va);
;             if (two) store(d1, tid, vb); }
.LBB0_606:
	s_lshl_b32 s18, s25, 8
	s_add_i32 s1, s18, s1
	s_waitcnt vmcnt(13)
	v_cvt_pk_bf16_f32 v136, v100, v104
	v_add_u32_e32 v100, s1, v214
	v_cndmask_b32_e64 v100, v100, v132, s[8:9]
	v_ashrrev_i32_e32 v104, 31, v100
	s_waitcnt vmcnt(9)
	v_cvt_pk_bf16_f32 v137, v108, v112
	v_mul_lo_u32 v104, s10, v104
	v_mul_lo_u32 v108, s11, v100
	v_mad_u64_u32 v[140:141], s[18:19], s10, v100, 0
	v_add3_u32 v141, v141, v104, v108
	v_lshl_add_u64 v[140:141], v[140:141], 1, s[6:7]
	v_lshlrev_b64 v[142:143], 1, v[134:135]
	s_waitcnt vmcnt(5)
	v_cvt_pk_bf16_f32 v138, v116, v120
	s_waitcnt vmcnt(1)
	v_cvt_pk_bf16_f32 v139, v124, v128
	v_lshl_add_u64 v[134:135], v[140:141], 0, v[142:143]
	global_store_dwordx4 v[134:135], v[136:139], off sc0 sc1
	v_cvt_pk_bf16_f32 v134, v101, v105
	v_bitop3_b32 v101, v132, s79, 1 bitop3:0xc8
	v_or_b32_e32 v100, 1, v132
	v_add_u32_e32 v101, s1, v101
	v_cndmask_b32_e64 v100, v101, v100, s[8:9]
	v_ashrrev_i32_e32 v101, 31, v100
	v_mul_lo_u32 v104, s10, v101
	v_mul_lo_u32 v105, s11, v100
	v_mad_u64_u32 v[100:101], s[18:19], s10, v100, 0
	v_add3_u32 v101, v101, v104, v105
	v_lshl_add_u64 v[100:101], v[100:101], 1, s[6:7]
	v_cvt_pk_bf16_f32 v135, v109, v113
	v_cvt_pk_bf16_f32 v136, v117, v121
	v_cvt_pk_bf16_f32 v137, v125, v129
	v_lshl_add_u64 v[100:101], v[100:101], 0, v[142:143]
	s_movk_i32 s18, 0x5e
	global_store_dwordx4 v[100:101], v[134:137], off sc0 sc1
	v_bitop3_b32 v101, v132, s18, 2 bitop3:0xc8
	v_or_b32_e32 v100, 2, v132
	v_add_u32_e32 v101, s1, v101
	v_cndmask_b32_e64 v100, v101, v100, s[8:9]
	v_ashrrev_i32_e32 v101, 31, v100
	v_cvt_pk_bf16_f32 v134, v102, v106
	v_mul_lo_u32 v102, s10, v101
	v_mul_lo_u32 v104, s11, v100
	v_mad_u64_u32 v[100:101], s[18:19], s10, v100, 0
	s_movk_i32 s18, 0x5f
	s_nop 0
	v_bitop3_b32 v105, v132, s18, 3 bitop3:0xc8
	v_add3_u32 v101, v101, v102, v104
	v_or_b32_e32 v104, 3, v132
	v_add_u32_e32 v105, s1, v105
	v_lshl_add_u64 v[100:101], v[100:101], 1, s[6:7]
	v_cndmask_b32_e64 v104, v105, v104, s[8:9]
	v_cvt_pk_bf16_f32 v135, v110, v114
	v_cvt_pk_bf16_f32 v136, v118, v122
	v_cvt_pk_bf16_f32 v137, v126, v130
	v_lshl_add_u64 v[100:101], v[100:101], 0, v[142:143]
	v_ashrrev_i32_e32 v105, 31, v104
	global_store_dwordx4 v[100:101], v[134:137], off sc0 sc1
	v_cvt_pk_bf16_f32 v100, v103, v107
	v_mul_lo_u32 v106, s10, v105
	v_mul_lo_u32 v107, s11, v104
	v_mad_u64_u32 v[104:105], s[18:19], s10, v104, 0
	v_add3_u32 v105, v105, v106, v107
	v_lshl_add_u64 v[104:105], v[104:105], 1, s[6:7]
	v_cvt_pk_bf16_f32 v101, v111, v115
	v_cvt_pk_bf16_f32 v102, v119, v123
	v_cvt_pk_bf16_f32 v103, v127, v131
	v_lshl_add_u64 v[104:105], v[104:105], 0, v[142:143]
	s_movk_i32 s18, 0x7c
	global_store_dwordx4 v[104:105], v[100:103], off sc0 sc1
	v_or_b32_e32 v133, 32, v132
	s_and_b64 vcc, exec, s[4:5]
	v_cvt_pk_bf16_f32 v100, v68, v72
	v_bitop3_b32 v68, v132, s18, 32 bitop3:0xc8
	v_add_u32_e32 v68, s1, v68
	v_cndmask_b32_e64 v68, v68, v133, s[8:9]
	v_ashrrev_i32_e32 v72, 31, v68
	v_cvt_pk_bf16_f32 v101, v76, v80
	v_mul_lo_u32 v72, s10, v72
	v_mul_lo_u32 v76, s11, v68
	v_mad_u64_u32 v[104:105], s[18:19], s10, v68, 0
	v_add3_u32 v105, v105, v72, v76
	v_lshl_add_u64 v[104:105], v[104:105], 1, s[6:7]
	v_cvt_pk_bf16_f32 v102, v84, v88
	s_waitcnt vmcnt(4)
	v_cvt_pk_bf16_f32 v103, v92, v96
	v_lshl_add_u64 v[104:105], v[104:105], 0, v[142:143]
	s_movk_i32 s18, 0x7d
	global_store_dwordx4 v[104:105], v[100:103], off sc0 sc1
	v_or_b32_e32 v68, 33, v132
	s_nop 0
	v_cvt_pk_bf16_f32 v100, v69, v73
	v_bitop3_b32 v69, v132, s18, 33 bitop3:0xc8
	v_add_u32_e32 v69, s1, v69
	v_cndmask_b32_e64 v68, v69, v68, s[8:9]
	v_ashrrev_i32_e32 v69, 31, v68
	v_mul_lo_u32 v72, s10, v69
	v_mul_lo_u32 v73, s11, v68
	v_mad_u64_u32 v[68:69], s[18:19], s10, v68, 0
	v_add3_u32 v69, v69, v72, v73
	v_lshl_add_u64 v[68:69], v[68:69], 1, s[6:7]
	v_cvt_pk_bf16_f32 v101, v77, v81
	v_cvt_pk_bf16_f32 v102, v85, v89
	v_cvt_pk_bf16_f32 v103, v93, v97
	v_lshl_add_u64 v[68:69], v[68:69], 0, v[142:143]
	s_movk_i32 s18, 0x7e
	global_store_dwordx4 v[68:69], v[100:103], off sc0 sc1
	v_bitop3_b32 v69, v132, s18, 34 bitop3:0xc8
	v_or_b32_e32 v68, 34, v132
	v_add_u32_e32 v69, s1, v69
	v_cndmask_b32_e64 v68, v69, v68, s[8:9]
	v_ashrrev_i32_e32 v69, 31, v68
	v_cvt_pk_bf16_f32 v100, v70, v74
	v_mul_lo_u32 v70, s10, v69
	v_mul_lo_u32 v72, s11, v68
	v_mad_u64_u32 v[68:69], s[18:19], s10, v68, 0
	s_movk_i32 s18, 0x7f
	s_nop 0
	v_bitop3_b32 v73, v132, s18, 35 bitop3:0xc8
	v_add3_u32 v69, v69, v70, v72
	v_or_b32_e32 v72, 35, v132
	v_add_u32_e32 v73, s1, v73
	v_lshl_add_u64 v[68:69], v[68:69], 1, s[6:7]
	v_cndmask_b32_e64 v72, v73, v72, s[8:9]
	v_cvt_pk_bf16_f32 v101, v78, v82
	v_cvt_pk_bf16_f32 v102, v86, v90
	v_cvt_pk_bf16_f32 v103, v94, v98
	v_lshl_add_u64 v[68:69], v[68:69], 0, v[142:143]
	v_ashrrev_i32_e32 v73, 31, v72
	global_store_dwordx4 v[68:69], v[100:103], off sc0 sc1
	v_cvt_pk_bf16_f32 v68, v71, v75
	v_mul_lo_u32 v74, s10, v73
	v_mul_lo_u32 v75, s11, v72
	v_mad_u64_u32 v[72:73], s[8:9], s10, v72, 0
	v_add3_u32 v73, v73, v74, v75
	v_lshl_add_u64 v[72:73], v[72:73], 1, s[6:7]
	v_cvt_pk_bf16_f32 v69, v79, v83
	v_cvt_pk_bf16_f32 v70, v87, v91
	v_cvt_pk_bf16_f32 v71, v95, v99
	v_lshl_add_u64 v[72:73], v[72:73], 0, v[142:143]
	global_store_dwordx4 v[72:73], v[68:71], off sc0 sc1
	s_cbranch_vccnz .LBB0_589
; template <bool BF> __device__ __forceinline__ unsigned pk16(float lo, float hi) { return BF ? pkb(lo, hi) : pkh(lo, hi); }
;     static __device__ __forceinline__ void store(const CvItem& d, int tid, const f32x4 (&v)[2][8]) {
;         const int lane = tid & 63, wave = tid >> 6, kg = lane >> 3, ng = lane & 7; const int nblk = d.N / 128, kb = d.r / nblk, nb = d.r % nblk;
; #pragma unroll
;         for (int t = 0; t < 2; ++t) { const int sb = 2 * wave + t, k0 = 256 * kb + 64 * (sb >> 2) + 8 * kg, n0 = 128 * nb + 32 * (sb & 3) + 4 * ng;
; #pragma unroll
;             for (int j = 0; j < 4; ++j) { u32x4 w; w.x = pk16<MOE_BF16>(v[t][0][j], v[t][1][j]); w.y = pk16<MOE_BF16>(v[t][2][j], v[t][3][j]); w.z = pk16<MOE_BF16>(v[t][4][j], v[t][5][j]); w.w = pk16<MOE_BF16>(v[t][6][j], v[t][7][j]);
;                 const int n = n0 + j, row = d.add >= 0 ? (n >> 7) * 256 + (n & 127) + d.add : n;
;                 *(u32x4*)(d.WT + (size_t)row * d.K + k0) = w; } } }
;     __device__ __forceinline__ void run_all(int tid) const {
;     ...
;             if (two) store(d1, tid, vb); }
	s_lshr_b32 s1, s24, 7
	v_cvt_f32_i32_e32 v68, s1
	s_ashr_i32 s4, s20, 30
	s_or_b32 s6, s4, 1
	v_cvt_pk_bf16_f32 v70, v48, v52
	v_rcp_iflag_f32_e32 v69, v68
	v_cvt_pk_bf16_f32 v71, v60, v64
	v_mul_f32_e32 v69, v2, v69
	v_trunc_f32_e32 v69, v69
	v_fma_f32 v2, -v69, v68, v2
	v_cvt_i32_f32_e32 v69, v69
	v_cmp_ge_f32_e64 s[4:5], |v2|, v68
	s_and_b64 s[4:5], s[4:5], exec
	s_cselect_b32 s4, s6, 0
	v_add_u32_e32 v2, s4, v69
	v_bfe_i32 v68, v2, 0, 16
	v_mul_lo_u32 v2, v2, s1
	v_sub_u32_e32 v2, s3, v2
	v_bfe_i32 v2, v2, 0, 16
	v_lshl_or_b32 v76, v2, 7, v214
	v_lshlrev_b32_e32 v2, 8, v2
	v_add_u32_e32 v2, s23, v2
	v_add_u32_e32 v74, v2, v214
	v_cndmask_b32_e64 v74, v74, v76, s[14:15]
	v_ashrrev_i32_e32 v75, 31, v74
	v_lshl_or_b32 v72, v68, 8, v213
	v_mul_lo_u32 v77, s16, v75
	v_mul_lo_u32 v78, s17, v74
	v_mad_u64_u32 v[74:75], s[4:5], s16, v74, 0
	v_ashrrev_i32_e32 v73, 31, v72
	v_add3_u32 v75, v75, v77, v78
	v_lshl_add_u64 v[74:75], v[74:75], 1, s[12:13]
	v_lshlrev_b64 v[72:73], 1, v[72:73]
	v_cvt_pk_bf16_f32 v68, v16, v36
	v_cvt_pk_bf16_f32 v69, v44, v56
	v_lshl_add_u64 v[74:75], v[74:75], 0, v[72:73]
	global_store_dwordx4 v[74:75], v[68:71], off sc0 sc1
	v_bitop3_b32 v75, v76, s79, 1 bitop3:0xc8
	v_or_b32_e32 v74, 1, v76
	v_add_u32_e32 v75, v75, v2
	v_cndmask_b32_e64 v74, v75, v74, s[14:15]
	v_ashrrev_i32_e32 v75, 31, v74
	v_mul_lo_u32 v77, s16, v75
	v_mul_lo_u32 v78, s17, v74
	v_mad_u64_u32 v[74:75], s[4:5], s16, v74, 0
	v_add3_u32 v75, v75, v77, v78
	v_lshl_add_u64 v[74:75], v[74:75], 1, s[12:13]
	v_cvt_pk_bf16_f32 v68, v17, v37
	v_cvt_pk_bf16_f32 v69, v45, v57
	v_cvt_pk_bf16_f32 v70, v49, v53
	v_cvt_pk_bf16_f32 v71, v61, v65
	v_lshl_add_u64 v[74:75], v[74:75], 0, v[72:73]
	s_movk_i32 s1, 0x5e
	global_store_dwordx4 v[74:75], v[68:71], off sc0 sc1
	v_bitop3_b32 v75, v76, s1, 2 bitop3:0xc8
	v_or_b32_e32 v74, 2, v76
	v_add_u32_e32 v75, v75, v2
	v_cndmask_b32_e64 v74, v75, v74, s[14:15]
	v_ashrrev_i32_e32 v75, 31, v74
	v_mul_lo_u32 v77, s16, v75
	v_mul_lo_u32 v78, s17, v74
	v_mad_u64_u32 v[74:75], s[4:5], s16, v74, 0
	v_add3_u32 v75, v75, v77, v78
	v_lshl_add_u64 v[74:75], v[74:75], 1, s[12:13]
	v_cvt_pk_bf16_f32 v68, v18, v38
	v_cvt_pk_bf16_f32 v69, v46, v58
	v_cvt_pk_bf16_f32 v70, v50, v54
	v_cvt_pk_bf16_f32 v71, v62, v66
	v_lshl_add_u64 v[74:75], v[74:75], 0, v[72:73]
	s_movk_i32 s1, 0x5f
	global_store_dwordx4 v[74:75], v[68:71], off sc0 sc1
	v_bitop3_b32 v75, v76, s1, 3 bitop3:0xc8
	v_or_b32_e32 v74, 3, v76
	v_add_u32_e32 v75, v75, v2
	v_cndmask_b32_e64 v74, v75, v74, s[14:15]
	v_ashrrev_i32_e32 v75, 31, v74
	v_mul_lo_u32 v77, s16, v75
	v_mul_lo_u32 v78, s17, v74
	v_mad_u64_u32 v[74:75], s[4:5], s16, v74, 0
	v_add3_u32 v75, v75, v77, v78
	v_lshl_add_u64 v[74:75], v[74:75], 1, s[12:13]
	v_cvt_pk_bf16_f32 v68, v19, v39
	v_cvt_pk_bf16_f32 v69, v47, v59
	v_cvt_pk_bf16_f32 v70, v51, v55
	v_cvt_pk_bf16_f32 v71, v63, v67
	v_lshl_add_u64 v[74:75], v[74:75], 0, v[72:73]
	s_movk_i32 s1, 0x7c
	global_store_dwordx4 v[74:75], v[68:71], off sc0 sc1
	v_bitop3_b32 v75, v76, s1, 32 bitop3:0xc8
	v_or_b32_e32 v74, 32, v76
	v_add_u32_e32 v75, v75, v2
	v_cndmask_b32_e64 v74, v75, v74, s[14:15]
	v_ashrrev_i32_e32 v75, 31, v74
	v_mul_lo_u32 v77, s16, v75
	v_mul_lo_u32 v78, s17, v74
	v_mad_u64_u32 v[74:75], s[4:5], s16, v74, 0
	v_add3_u32 v75, v75, v77, v78
	v_lshl_add_u64 v[74:75], v[74:75], 1, s[12:13]
	v_cvt_pk_bf16_f32 v68, v4, v8
	v_cvt_pk_bf16_f32 v69, v12, v20
	v_cvt_pk_bf16_f32 v70, v24, v28
	v_cvt_pk_bf16_f32 v71, v32, v40
	v_lshl_add_u64 v[74:75], v[74:75], 0, v[72:73]
	s_movk_i32 s1, 0x7d
	global_store_dwordx4 v[74:75], v[68:71], off sc0 sc1
	v_bitop3_b32 v75, v76, s1, 33 bitop3:0xc8
	v_or_b32_e32 v74, 33, v76
	v_add_u32_e32 v75, v75, v2
	v_cndmask_b32_e64 v74, v75, v74, s[14:15]
	v_ashrrev_i32_e32 v75, 31, v74
	v_mul_lo_u32 v77, s16, v75
	v_mul_lo_u32 v78, s17, v74
	v_mad_u64_u32 v[74:75], s[4:5], s16, v74, 0
	v_add3_u32 v75, v75, v77, v78
	v_lshl_add_u64 v[74:75], v[74:75], 1, s[12:13]
	v_cvt_pk_bf16_f32 v68, v5, v9
	v_cvt_pk_bf16_f32 v69, v13, v21
	v_cvt_pk_bf16_f32 v70, v25, v29
	v_cvt_pk_bf16_f32 v71, v33, v41
	v_lshl_add_u64 v[74:75], v[74:75], 0, v[72:73]
	s_movk_i32 s1, 0x7e
	global_store_dwordx4 v[74:75], v[68:71], off sc0 sc1
	v_bitop3_b32 v75, v76, s1, 34 bitop3:0xc8
	v_or_b32_e32 v74, 34, v76
	v_add_u32_e32 v75, v75, v2
	v_cndmask_b32_e64 v74, v75, v74, s[14:15]
	v_ashrrev_i32_e32 v75, 31, v74
	v_mul_lo_u32 v77, s16, v75
	v_mul_lo_u32 v78, s17, v74
	v_mad_u64_u32 v[74:75], s[4:5], s16, v74, 0
	v_add3_u32 v75, v75, v77, v78
	v_lshl_add_u64 v[74:75], v[74:75], 1, s[12:13]
	v_cvt_pk_bf16_f32 v68, v6, v10
	v_cvt_pk_bf16_f32 v69, v14, v22
	v_cvt_pk_bf16_f32 v70, v26, v30
	v_cvt_pk_bf16_f32 v71, v34, v42
	v_lshl_add_u64 v[74:75], v[74:75], 0, v[72:73]
	s_movk_i32 s1, 0x7f
	global_store_dwordx4 v[74:75], v[68:71], off sc0 sc1
	v_bitop3_b32 v75, v76, s1, 35 bitop3:0xc8
	v_or_b32_e32 v74, 35, v76
	v_add_u32_e32 v2, v75, v2
	v_cndmask_b32_e64 v2, v2, v74, s[14:15]
	v_ashrrev_i32_e32 v74, 31, v2
	v_mul_lo_u32 v76, s16, v74
	v_mul_lo_u32 v77, s17, v2
	v_mad_u64_u32 v[74:75], s[4:5], s16, v2, 0
	v_add3_u32 v75, v75, v76, v77
	v_lshl_add_u64 v[74:75], v[74:75], 1, s[12:13]
	v_cvt_pk_bf16_f32 v68, v7, v11
	v_cvt_pk_bf16_f32 v69, v15, v23
	v_cvt_pk_bf16_f32 v70, v27, v31
	v_cvt_pk_bf16_f32 v71, v35, v43
	v_lshl_add_u64 v[72:73], v[74:75], 0, v[72:73]
	global_store_dwordx4 v[72:73], v[68:71], off sc0 sc1
	s_branch .LBB0_589

; template <bool BF> __device__ __forceinline__ unsigned pk16(float lo, float hi) { return BF ? pkb(lo, hi) : pkh(lo, hi); }
;     static __device__ __forceinline__ void store(const CvItem& d, int tid, const f32x4 (&v)[2][8]) {
;         const int lane = tid & 63, wave = tid >> 6, kg = lane >> 3, ng = lane & 7; const int nblk = d.N / 128, kb = d.r / nblk, nb = d.r % nblk;
; #pragma unroll
;         for (int t = 0; t < 2; ++t) { const int sb = 2 * wave + t, k0 = 256 * kb + 64 * (sb >> 2) + 8 * kg, n0 = 128 * nb + 32 * (sb & 3) + 4 * ng;
; #pragma unroll
;             for (int j = 0; j < 4; ++j) { u32x4 w; w.x = pk16<MOE_BF16>(v[t][0][j], v[t][1][j]); w.y = pk16<MOE_BF16>(v[t][2][j], v[t][3][j]); w.z = pk16<MOE_BF16>(v[t][4][j], v[t][5][j]); w.w = pk16<MOE_BF16>(v[t][6][j], v[t][7][j]);
;                 const int n = n0 + j, row = d.add >= 0 ? (n >> 7) * 256 + (n & 127) + d.add : n;
;                 *(u32x4*)(d.WT + (size_t)row * d.K + k0) = w; } } }
.LBB0_637:
	s_lshl_b32 s18, s31, 8
	s_add_i32 s20, s18, s27
	s_waitcnt vmcnt(0)
	v_cvt_pk_bf16_f32 v136, v98, v102
	v_add_u32_e32 v98, s20, v134
	v_cndmask_b32_e64 v98, v98, v130, s[8:9]
	v_ashrrev_i32_e32 v102, 31, v98
	v_cvt_pk_bf16_f32 v137, v106, v110
	v_mul_lo_u32 v102, s10, v102
	v_mul_lo_u32 v106, s11, v98
	v_mad_u64_u32 v[140:141], s[18:19], s10, v98, 0
	v_add3_u32 v141, v141, v102, v106
	v_lshl_add_u64 v[140:141], v[140:141], 1, s[6:7]
	v_lshlrev_b64 v[132:133], 1, v[132:133]
	v_cvt_pk_bf16_f32 v138, v114, v118
	v_cvt_pk_bf16_f32 v139, v122, v126
	v_lshl_add_u64 v[140:141], v[140:141], 0, v[132:133]
	global_store_dwordx4 v[140:141], v[136:139], off sc0 sc1
	v_or_b32_e32 v98, 1, v130
	v_or_b32_e32 v135, 32, v130
	v_cvt_pk_bf16_f32 v136, v99, v103
	v_bitop3_b32 v99, v130, s1, 1 bitop3:0xc8
	v_add_u32_e32 v99, s20, v99
	v_cndmask_b32_e64 v98, v99, v98, s[8:9]
	v_ashrrev_i32_e32 v99, 31, v98
	v_mul_lo_u32 v102, s10, v99
	v_mul_lo_u32 v103, s11, v98
	v_mad_u64_u32 v[98:99], s[18:19], s10, v98, 0
	v_add3_u32 v99, v99, v102, v103
	v_lshl_add_u64 v[98:99], v[98:99], 1, s[6:7]
	v_cvt_pk_bf16_f32 v137, v107, v111
	v_cvt_pk_bf16_f32 v138, v115, v119
	v_cvt_pk_bf16_f32 v139, v123, v127
	v_lshl_add_u64 v[98:99], v[98:99], 0, v[132:133]
	global_store_dwordx4 v[98:99], v[136:139], off sc0 sc1
	v_bitop3_b32 v99, v130, s3, 2 bitop3:0xc8
	v_or_b32_e32 v98, 2, v130
	v_add_u32_e32 v99, s20, v99
	v_cndmask_b32_e64 v98, v99, v98, s[8:9]
	v_ashrrev_i32_e32 v99, 31, v98
	v_cvt_pk_bf16_f32 v136, v100, v104
	v_mul_lo_u32 v100, s10, v99
	v_mul_lo_u32 v102, s11, v98
	v_mad_u64_u32 v[98:99], s[18:19], s10, v98, 0
	v_bitop3_b32 v103, v130, s22, 3 bitop3:0xc8
	v_add3_u32 v99, v99, v100, v102
	v_or_b32_e32 v102, 3, v130
	v_add_u32_e32 v103, s20, v103
	v_lshl_add_u64 v[98:99], v[98:99], 1, s[6:7]
	v_cndmask_b32_e64 v102, v103, v102, s[8:9]
	v_cvt_pk_bf16_f32 v137, v108, v112
	v_cvt_pk_bf16_f32 v138, v116, v120
	v_cvt_pk_bf16_f32 v139, v124, v128
	v_lshl_add_u64 v[98:99], v[98:99], 0, v[132:133]
	v_ashrrev_i32_e32 v103, 31, v102
	global_store_dwordx4 v[98:99], v[136:139], off sc0 sc1
	v_cvt_pk_bf16_f32 v98, v101, v105
	v_mul_lo_u32 v104, s10, v103
	v_mul_lo_u32 v105, s11, v102
	v_mad_u64_u32 v[102:103], s[18:19], s10, v102, 0
	v_add3_u32 v103, v103, v104, v105
	v_lshl_add_u64 v[102:103], v[102:103], 1, s[6:7]
	v_cvt_pk_bf16_f32 v99, v109, v113
	v_cvt_pk_bf16_f32 v100, v117, v121
	v_cvt_pk_bf16_f32 v101, v125, v129
	v_lshl_add_u64 v[102:103], v[102:103], 0, v[132:133]
	global_store_dwordx4 v[102:103], v[98:101], off sc0 sc1
	s_and_b64 vcc, exec, s[4:5]
	s_nop 0
	v_cvt_pk_bf16_f32 v98, v66, v70
	v_bitop3_b32 v66, v130, s23, 32 bitop3:0xc8
	v_add_u32_e32 v66, s20, v66
	v_cndmask_b32_e64 v66, v66, v135, s[8:9]
	v_ashrrev_i32_e32 v70, 31, v66
	v_cvt_pk_bf16_f32 v99, v74, v78
	v_mul_lo_u32 v70, s10, v70
	v_mul_lo_u32 v74, s11, v66
	v_mad_u64_u32 v[102:103], s[18:19], s10, v66, 0
	v_add3_u32 v103, v103, v70, v74
	v_lshl_add_u64 v[102:103], v[102:103], 1, s[6:7]
	v_cvt_pk_bf16_f32 v100, v82, v86
	v_cvt_pk_bf16_f32 v101, v90, v94
	v_lshl_add_u64 v[102:103], v[102:103], 0, v[132:133]
	global_store_dwordx4 v[102:103], v[98:101], off sc0 sc1
	v_or_b32_e32 v66, 33, v130
	s_nop 0
	v_cvt_pk_bf16_f32 v98, v67, v71
	v_bitop3_b32 v67, v130, s24, 33 bitop3:0xc8
	v_add_u32_e32 v67, s20, v67
	v_cndmask_b32_e64 v66, v67, v66, s[8:9]
	v_ashrrev_i32_e32 v67, 31, v66
	v_mul_lo_u32 v70, s10, v67
	v_mul_lo_u32 v71, s11, v66
	v_mad_u64_u32 v[66:67], s[18:19], s10, v66, 0
	v_add3_u32 v67, v67, v70, v71
	v_lshl_add_u64 v[66:67], v[66:67], 1, s[6:7]
	v_cvt_pk_bf16_f32 v99, v75, v79
	v_cvt_pk_bf16_f32 v100, v83, v87
	v_cvt_pk_bf16_f32 v101, v91, v95
	v_lshl_add_u64 v[66:67], v[66:67], 0, v[132:133]
	global_store_dwordx4 v[66:67], v[98:101], off sc0 sc1
	v_bitop3_b32 v67, v130, s25, 34 bitop3:0xc8
	v_or_b32_e32 v66, 34, v130
	v_add_u32_e32 v67, s20, v67
	v_cndmask_b32_e64 v66, v67, v66, s[8:9]
	v_ashrrev_i32_e32 v67, 31, v66
	v_cvt_pk_bf16_f32 v98, v68, v72
	v_mul_lo_u32 v68, s10, v67
	v_mul_lo_u32 v70, s11, v66
	v_mad_u64_u32 v[66:67], s[18:19], s10, v66, 0
	v_bitop3_b32 v71, v130, s26, 35 bitop3:0xc8
	v_add3_u32 v67, v67, v68, v70
	v_or_b32_e32 v70, 35, v130
	v_add_u32_e32 v71, s20, v71
	v_lshl_add_u64 v[66:67], v[66:67], 1, s[6:7]
	v_cndmask_b32_e64 v70, v71, v70, s[8:9]
	v_cvt_pk_bf16_f32 v99, v76, v80
	v_cvt_pk_bf16_f32 v100, v84, v88
	v_cvt_pk_bf16_f32 v101, v92, v96
	v_lshl_add_u64 v[66:67], v[66:67], 0, v[132:133]
	v_ashrrev_i32_e32 v71, 31, v70
	global_store_dwordx4 v[66:67], v[98:101], off sc0 sc1
	v_cvt_pk_bf16_f32 v66, v69, v73
	v_mul_lo_u32 v72, s10, v71
	v_mul_lo_u32 v73, s11, v70
	v_mad_u64_u32 v[70:71], s[8:9], s10, v70, 0
	v_add3_u32 v71, v71, v72, v73
	v_lshl_add_u64 v[70:71], v[70:71], 1, s[6:7]
	v_cvt_pk_bf16_f32 v67, v77, v81
	v_cvt_pk_bf16_f32 v68, v85, v89
	v_cvt_pk_bf16_f32 v69, v93, v97
	v_lshl_add_u64 v[70:71], v[70:71], 0, v[132:133]
	global_store_dwordx4 v[70:71], v[66:69], off sc0 sc1
	s_cbranch_vccnz .LBB0_620
; template <bool BF> __device__ __forceinline__ unsigned pk16(float lo, float hi) { return BF ? pkb(lo, hi) : pkh(lo, hi); }
;     static __device__ __forceinline__ void store(const CvItem& d, int tid, const f32x4 (&v)[2][8]) {
;         const int lane = tid & 63, wave = tid >> 6, kg = lane >> 3, ng = lane & 7; const int nblk = d.N / 128, kb = d.r / nblk, nb = d.r % nblk;
; #pragma unroll
;         for (int t = 0; t < 2; ++t) { const int sb = 2 * wave + t, k0 = 256 * kb + 64 * (sb >> 2) + 8 * kg, n0 = 128 * nb + 32 * (sb & 3) + 4 * ng;
; #pragma unroll
;             for (int j = 0; j < 4; ++j) { u32x4 w; w.x = pk16<MOE_BF16>(v[t][0][j], v[t][1][j]); w.y = pk16<MOE_BF16>(v[t][2][j], v[t][3][j]); w.z = pk16<MOE_BF16>(v[t][4][j], v[t][5][j]); w.w = pk16<MOE_BF16>(v[t][6][j], v[t][7][j]);
;                 const int n = n0 + j, row = d.add >= 0 ? (n >> 7) * 256 + (n & 127) + d.add : n;
;                 *(u32x4*)(d.WT + (size_t)row * d.K + k0) = w; } } }
	s_lshr_b32 s6, s30, 7
	v_cvt_f32_i32_e32 v66, s6
	s_ashr_i32 s4, s33, 30
	s_or_b32 s7, s4, 1
	v_cvt_pk_bf16_f32 v69, v58, v62
	v_rcp_iflag_f32_e32 v67, v66
	s_nop 0
	v_mul_f32_e32 v67, v131, v67
	v_trunc_f32_e32 v67, v67
	v_fma_f32 v68, -v67, v66, v131
	v_cvt_i32_f32_e32 v67, v67
	v_cmp_ge_f32_e64 s[4:5], |v68|, v66
	s_and_b64 s[4:5], s[4:5], exec
	s_cselect_b32 s4, s7, 0
	v_add_u32_e32 v66, s4, v67
	v_bfe_i32 v67, v66, 0, 16
	v_mul_lo_u32 v66, v66, s6
	v_sub_u32_e32 v66, s28, v66
	v_bfe_i32 v66, v66, 0, 16
	v_lshlrev_b32_e32 v72, 8, v66
	v_add_u32_e32 v75, s29, v72
	v_lshl_or_b32 v74, v66, 7, v134
	v_add_u32_e32 v72, v75, v134
	v_cndmask_b32_e64 v72, v72, v74, s[14:15]
	v_ashrrev_i32_e32 v73, 31, v72
	v_lshl_or_b32 v70, v67, 8, v1
	v_mul_lo_u32 v76, s16, v73
	v_mul_lo_u32 v77, s17, v72
	v_mad_u64_u32 v[72:73], s[4:5], s16, v72, 0
	v_ashrrev_i32_e32 v71, 31, v70
	v_add3_u32 v73, v73, v76, v77
	v_lshl_add_u64 v[72:73], v[72:73], 1, s[12:13]
	v_lshlrev_b64 v[70:71], 1, v[70:71]
	v_cvt_pk_bf16_f32 v66, v14, v34
	v_cvt_pk_bf16_f32 v67, v42, v54
	v_cvt_pk_bf16_f32 v68, v46, v50
	v_lshl_add_u64 v[72:73], v[72:73], 0, v[70:71]
	global_store_dwordx4 v[72:73], v[66:69], off sc0 sc1
	v_bitop3_b32 v73, v74, s1, 1 bitop3:0xc8
	v_or_b32_e32 v72, 1, v74
	v_add_u32_e32 v73, v73, v75
	v_cndmask_b32_e64 v72, v73, v72, s[14:15]
	v_ashrrev_i32_e32 v73, 31, v72
	v_mul_lo_u32 v76, s16, v73
	v_mul_lo_u32 v77, s17, v72
	v_mad_u64_u32 v[72:73], s[4:5], s16, v72, 0
	v_add3_u32 v73, v73, v76, v77
	v_lshl_add_u64 v[72:73], v[72:73], 1, s[12:13]
	v_cvt_pk_bf16_f32 v66, v15, v35
	v_cvt_pk_bf16_f32 v67, v43, v55
	v_cvt_pk_bf16_f32 v68, v47, v51
	v_cvt_pk_bf16_f32 v69, v59, v63
	v_lshl_add_u64 v[72:73], v[72:73], 0, v[70:71]
	global_store_dwordx4 v[72:73], v[66:69], off sc0 sc1
	v_bitop3_b32 v73, v74, s3, 2 bitop3:0xc8
	v_or_b32_e32 v72, 2, v74
	v_add_u32_e32 v73, v73, v75
	v_cndmask_b32_e64 v72, v73, v72, s[14:15]
	v_ashrrev_i32_e32 v73, 31, v72
	v_mul_lo_u32 v76, s16, v73
	v_mul_lo_u32 v77, s17, v72
	v_mad_u64_u32 v[72:73], s[4:5], s16, v72, 0
	v_add3_u32 v73, v73, v76, v77
	v_lshl_add_u64 v[72:73], v[72:73], 1, s[12:13]
	v_cvt_pk_bf16_f32 v66, v16, v36
	v_cvt_pk_bf16_f32 v67, v44, v56
	v_cvt_pk_bf16_f32 v68, v48, v52
	v_cvt_pk_bf16_f32 v69, v60, v64
	v_lshl_add_u64 v[72:73], v[72:73], 0, v[70:71]
	global_store_dwordx4 v[72:73], v[66:69], off sc0 sc1
	v_bitop3_b32 v73, v74, s22, 3 bitop3:0xc8
	v_or_b32_e32 v72, 3, v74
	v_add_u32_e32 v73, v73, v75
	v_cndmask_b32_e64 v72, v73, v72, s[14:15]
	v_ashrrev_i32_e32 v73, 31, v72
	v_mul_lo_u32 v76, s16, v73
	v_mul_lo_u32 v77, s17, v72
	v_mad_u64_u32 v[72:73], s[4:5], s16, v72, 0
	v_add3_u32 v73, v73, v76, v77
	v_lshl_add_u64 v[72:73], v[72:73], 1, s[12:13]
	v_cvt_pk_bf16_f32 v66, v17, v37
	v_cvt_pk_bf16_f32 v67, v45, v57
	v_cvt_pk_bf16_f32 v68, v49, v53
	v_cvt_pk_bf16_f32 v69, v61, v65
	v_lshl_add_u64 v[72:73], v[72:73], 0, v[70:71]
	global_store_dwordx4 v[72:73], v[66:69], off sc0 sc1
	v_bitop3_b32 v73, v74, s23, 32 bitop3:0xc8
	v_or_b32_e32 v72, 32, v74
	v_add_u32_e32 v73, v73, v75
	v_cndmask_b32_e64 v72, v73, v72, s[14:15]
	v_ashrrev_i32_e32 v73, 31, v72
	v_mul_lo_u32 v76, s16, v73
	v_mul_lo_u32 v77, s17, v72
	v_mad_u64_u32 v[72:73], s[4:5], s16, v72, 0
	v_add3_u32 v73, v73, v76, v77
	v_lshl_add_u64 v[72:73], v[72:73], 1, s[12:13]
	v_cvt_pk_bf16_f32 v66, v2, v6
	v_cvt_pk_bf16_f32 v67, v10, v18
	v_cvt_pk_bf16_f32 v68, v22, v26
	v_cvt_pk_bf16_f32 v69, v30, v38
	v_lshl_add_u64 v[72:73], v[72:73], 0, v[70:71]
	global_store_dwordx4 v[72:73], v[66:69], off sc0 sc1
	v_bitop3_b32 v73, v74, s24, 33 bitop3:0xc8
	v_or_b32_e32 v72, 33, v74
	v_add_u32_e32 v73, v73, v75
	v_cndmask_b32_e64 v72, v73, v72, s[14:15]
	v_ashrrev_i32_e32 v73, 31, v72
	v_mul_lo_u32 v76, s16, v73
	v_mul_lo_u32 v77, s17, v72
	v_mad_u64_u32 v[72:73], s[4:5], s16, v72, 0
	v_add3_u32 v73, v73, v76, v77
	v_lshl_add_u64 v[72:73], v[72:73], 1, s[12:13]
	v_cvt_pk_bf16_f32 v66, v3, v7
	v_cvt_pk_bf16_f32 v67, v11, v19
	v_cvt_pk_bf16_f32 v68, v23, v27
	v_cvt_pk_bf16_f32 v69, v31, v39
	v_lshl_add_u64 v[72:73], v[72:73], 0, v[70:71]
	global_store_dwordx4 v[72:73], v[66:69], off sc0 sc1
	v_bitop3_b32 v73, v74, s25, 34 bitop3:0xc8
	v_or_b32_e32 v72, 34, v74
	v_add_u32_e32 v73, v73, v75
	v_cndmask_b32_e64 v72, v73, v72, s[14:15]
	v_ashrrev_i32_e32 v73, 31, v72
	v_mul_lo_u32 v76, s16, v73
	v_mul_lo_u32 v77, s17, v72
	v_mad_u64_u32 v[72:73], s[4:5], s16, v72, 0
	v_add3_u32 v73, v73, v76, v77
	v_lshl_add_u64 v[72:73], v[72:73], 1, s[12:13]
	v_cvt_pk_bf16_f32 v66, v4, v8
	v_cvt_pk_bf16_f32 v67, v12, v20
	v_cvt_pk_bf16_f32 v68, v24, v28
	v_cvt_pk_bf16_f32 v69, v32, v40
	v_lshl_add_u64 v[72:73], v[72:73], 0, v[70:71]
	global_store_dwordx4 v[72:73], v[66:69], off sc0 sc1
	v_bitop3_b32 v73, v74, s26, 35 bitop3:0xc8
	v_or_b32_e32 v72, 35, v74
	v_add_u32_e32 v73, v73, v75
	v_cndmask_b32_e64 v72, v73, v72, s[14:15]
	v_ashrrev_i32_e32 v73, 31, v72
	v_mul_lo_u32 v74, s16, v73
	v_mul_lo_u32 v75, s17, v72
	v_mad_u64_u32 v[72:73], s[4:5], s16, v72, 0
	v_add3_u32 v73, v73, v74, v75
	v_lshl_add_u64 v[72:73], v[72:73], 1, s[12:13]
	v_cvt_pk_bf16_f32 v66, v5, v9
	v_cvt_pk_bf16_f32 v67, v13, v21
	v_cvt_pk_bf16_f32 v68, v25, v29
	v_cvt_pk_bf16_f32 v69, v33, v41
	v_lshl_add_u64 v[70:71], v[72:73], 0, v[70:71]
	global_store_dwordx4 v[70:71], v[66:69], off sc0 sc1
	s_branch .LBB0_620

;     __device__ __forceinline__ void operator()() { if (cnt == turn) run_all(tid_); ++cnt; }
;     __device__ __forceinline__ void operator()(const Acc& acc, const Unit& u, int wr, int wc, int fr, int fq) const {
;         const int col0 = u.pn * BM + wc * 32 + 8 * fq; const int b = (u.pm * BM) / SEQ;
;         f32x4 gv[2][2];
; #pragma unroll
;         for (int bj = 0; bj < 2; ++bj)
; #pragma unroll
;             for (int n = 0; n < 2; ++n) gv[bj][n] = *(const f32x4*)(gate + (size_t)b * gstride + col0 + bj * HALF + 4 * n);
; #pragma unroll
;         for (int ai = 0; ai < 2; ++ai)
; #pragma unroll
;             for (int m = 0; m < 4; ++m) { const size_t off = (size_t)(u.pm * BM + ai * HALF + wr * 64 + m * 16 + fr) * DM + col0;
; #pragma unroll
;                 for (int bj = 0; bj < 2; ++bj) { f32x4 b0, b1;
;                     if constexpr (BASE16) { const f16x8 bv = *(const f16x8*)((const f16*)base + off + bj * HALF);
;                         b0 = (f32x4){(float)bv[0], (float)bv[1], (float)bv[2], (float)bv[3]}; b1 = (f32x4){(float)bv[4], (float)bv[5], (float)bv[6], (float)bv[7]}; }
;                     else { b0 = *(const f32x4*)((const float*)base + off + bj * HALF); b1 = *(const f32x4*)((const float*)base + off + bj * HALF + 4); }
;                     const f32x4 v0 = b0 + gv[bj][0] * acc[ai][bj][m][0], v1 = b1 + gv[bj][1] * acc[ai][bj][m][1];
;                     u32x4 w; w.x = pkh(v0[0], v0[1]); w.y = pkh(v0[2], v0[3]); w.z = pkh(v1[0], v1[1]); w.w = pkh(v1[2], v1[3]);
;                     *(u32x4*)(out + off + bj * HALF) = w; }
.LBB0_718:
	v_lshl_or_b32 v162, s3, 8, v167
	s_ashr_i32 s3, s2, 31
	s_lshr_b32 s3, s3, 29
	s_add_i32 s3, s2, s3
	s_ashr_i32 s3, s3, 3
	v_lshl_add_u32 v164, s2, 8, v1
	s_mul_hi_i32 s13, s3, 0x6000
	s_mulk_i32 s3, 0x6000
	v_ashrrev_i32_e32 v165, 31, v164
	s_add_u32 s20, s36, s3
	v_ashrrev_i32_e32 v163, 31, v162
	v_lshlrev_b64 v[134:135], 10, v[164:165]
	v_readlane_b32 s44, v251, 60
	s_addc_u32 s21, s37, s13
	v_lshl_add_u64 v[138:139], v[134:135], 0, v[162:163]
	v_readlane_b32 s45, v251, 61
	v_lshl_add_u64 v[142:143], v[162:163], 2, s[20:21]
	global_load_dwordx4 v[130:133], v[142:143], off
	v_lshl_add_u64 v[180:181], v[138:139], 2, s[44:45]
	global_load_dwordx4 v[172:175], v[180:181], off nt
	global_load_dwordx4 v[176:179], v[180:181], off offset:16 nt
	global_load_dwordx4 v[134:137], v[142:143], off offset:16
	v_lshl_add_u64 v[182:183], v[138:139], 1, s[66:67]
	global_load_dwordx4 v[138:141], v[142:143], off offset:528
	s_nop 0
	global_load_dwordx4 v[142:145], v[142:143], off offset:512
	s_andn2_b64 vcc, exec, s[4:5]
	s_mov_b64 s[2:3], -1
	v_readlane_b32 s46, v251, 62
	v_readlane_b32 s47, v251, 63
	v_readlane_b32 s48, v250, 0
	v_readlane_b32 s49, v250, 1
	v_readlane_b32 s50, v250, 2
	v_readlane_b32 s51, v250, 3
	v_readlane_b32 s52, v250, 4
	v_readlane_b32 s53, v250, 5
	v_readlane_b32 s54, v250, 6
	v_readlane_b32 s55, v250, 7
	v_readlane_b32 s56, v250, 8
	v_readlane_b32 s57, v250, 9
	v_readlane_b32 s58, v250, 10
	v_readlane_b32 s59, v250, 11
	s_waitcnt vmcnt(0)
	v_pk_fma_f32 v[128:129], v[128:129], v[132:133], v[174:175]
	v_pk_fma_f32 v[126:127], v[126:127], v[130:131], v[172:173]
	v_pk_fma_f32 v[172:173], v[124:125], v[136:137], v[178:179]
	v_pk_fma_f32 v[124:125], v[122:123], v[134:135], v[176:177]
	v_cvt_pk_f16_f32 v122, v126, v127
	v_cvt_pk_f16_f32 v123, v128, v129
	v_cvt_pk_f16_f32 v124, v124, v125
	v_cvt_pk_f16_f32 v125, v172, v173
	global_store_dwordx4 v[182:183], v[122:125], off sc0 sc1
	global_load_dwordx4 v[122:125], v[180:181], off offset:512 nt
	s_nop 0
	global_load_dwordx4 v[126:129], v[180:181], off offset:528 nt
	v_or_b32_e32 v172, 16, v164
	v_ashrrev_i32_e32 v173, 31, v172
	v_lshlrev_b64 v[172:173], 10, v[172:173]
	v_lshl_add_u64 v[172:173], v[172:173], 0, v[162:163]
	v_lshl_add_u64 v[174:175], v[172:173], 2, s[44:45]
	s_waitcnt vmcnt(1)
	v_pk_fma_f32 v[120:121], v[120:121], v[144:145], v[124:125]
	v_pk_fma_f32 v[118:119], v[118:119], v[142:143], v[122:123]
	s_waitcnt vmcnt(0)
	v_pk_fma_f32 v[122:123], v[116:117], v[140:141], v[128:129]
	v_pk_fma_f32 v[116:117], v[114:115], v[138:139], v[126:127]
	v_cvt_pk_f16_f32 v114, v118, v119
	v_cvt_pk_f16_f32 v115, v120, v121
	v_cvt_pk_f16_f32 v116, v116, v117
	v_cvt_pk_f16_f32 v117, v122, v123
	global_store_dwordx4 v[182:183], v[114:117], off offset:256 sc0 sc1
	global_load_dwordx4 v[114:117], v[174:175], off nt
	s_nop 0
	global_load_dwordx4 v[118:121], v[174:175], off offset:16 nt
	v_lshl_add_u64 v[122:123], v[172:173], 1, s[66:67]
	s_waitcnt vmcnt(1)
	v_pk_fma_f32 v[112:113], v[112:113], v[132:133], v[116:117]
	v_pk_fma_f32 v[110:111], v[110:111], v[130:131], v[114:115]
	s_waitcnt vmcnt(0)
	v_pk_fma_f32 v[114:115], v[108:109], v[136:137], v[120:121]
	v_pk_fma_f32 v[108:109], v[106:107], v[134:135], v[118:119]
	v_cvt_pk_f16_f32 v106, v110, v111
	v_cvt_pk_f16_f32 v107, v112, v113
	v_cvt_pk_f16_f32 v108, v108, v109
	v_cvt_pk_f16_f32 v109, v114, v115
	global_store_dwordx4 v[122:123], v[106:109], off sc0 sc1
	global_load_dwordx4 v[106:109], v[174:175], off offset:512 nt
	s_nop 0
	global_load_dwordx4 v[110:113], v[174:175], off offset:528 nt
	v_or_b32_e32 v114, 32, v164
	v_ashrrev_i32_e32 v115, 31, v114
	v_lshlrev_b64 v[114:115], 10, v[114:115]
	v_lshl_add_u64 v[114:115], v[114:115], 0, v[162:163]
	v_lshl_add_u64 v[116:117], v[114:115], 2, s[44:45]
	s_waitcnt vmcnt(1)
	v_pk_fma_f32 v[104:105], v[104:105], v[144:145], v[108:109]
	v_pk_fma_f32 v[102:103], v[102:103], v[142:143], v[106:107]
	s_waitcnt vmcnt(0)
	v_pk_fma_f32 v[106:107], v[100:101], v[140:141], v[112:113]
	v_pk_fma_f32 v[100:101], v[98:99], v[138:139], v[110:111]
	v_cvt_pk_f16_f32 v98, v102, v103
	v_cvt_pk_f16_f32 v99, v104, v105
	v_cvt_pk_f16_f32 v100, v100, v101
	v_cvt_pk_f16_f32 v101, v106, v107
	global_store_dwordx4 v[122:123], v[98:101], off offset:256 sc0 sc1
	global_load_dwordx4 v[98:101], v[116:117], off nt
	global_load_dwordx4 v[102:105], v[116:117], off offset:16 nt
	v_lshl_add_u64 v[106:107], v[114:115], 1, s[66:67]
	s_waitcnt vmcnt(1)
	v_pk_fma_f32 v[96:97], v[96:97], v[132:133], v[100:101]
	v_pk_fma_f32 v[94:95], v[94:95], v[130:131], v[98:99]
	s_waitcnt vmcnt(0)
	v_pk_fma_f32 v[98:99], v[92:93], v[136:137], v[104:105]
	v_pk_fma_f32 v[92:93], v[90:91], v[134:135], v[102:103]
	v_cvt_pk_f16_f32 v90, v94, v95
	v_cvt_pk_f16_f32 v91, v96, v97
	v_cvt_pk_f16_f32 v92, v92, v93
	v_cvt_pk_f16_f32 v93, v98, v99
	global_store_dwordx4 v[106:107], v[90:93], off sc0 sc1
	global_load_dwordx4 v[90:93], v[116:117], off offset:512 nt
	s_nop 0
	global_load_dwordx4 v[94:97], v[116:117], off offset:528 nt
	v_or_b32_e32 v98, 48, v164
	v_ashrrev_i32_e32 v99, 31, v98
	v_lshlrev_b64 v[98:99], 10, v[98:99]
	v_lshl_add_u64 v[98:99], v[98:99], 0, v[162:163]
	v_lshl_add_u64 v[100:101], v[98:99], 2, s[44:45]
	s_waitcnt vmcnt(1)
	v_pk_fma_f32 v[88:89], v[88:89], v[144:145], v[92:93]
	v_pk_fma_f32 v[86:87], v[86:87], v[142:143], v[90:91]
	s_waitcnt vmcnt(0)
	v_pk_fma_f32 v[90:91], v[84:85], v[140:141], v[96:97]
	v_pk_fma_f32 v[84:85], v[82:83], v[138:139], v[94:95]
	v_cvt_pk_f16_f32 v82, v86, v87
	v_cvt_pk_f16_f32 v83, v88, v89
	v_cvt_pk_f16_f32 v84, v84, v85
	v_cvt_pk_f16_f32 v85, v90, v91
	global_store_dwordx4 v[106:107], v[82:85], off offset:256 sc0 sc1
	global_load_dwordx4 v[82:85], v[100:101], off nt
	s_nop 0
	global_load_dwordx4 v[86:89], v[100:101], off offset:16 nt
	v_lshl_add_u64 v[90:91], v[98:99], 1, s[66:67]
	s_waitcnt vmcnt(1)
;     __device__ __forceinline__ void operator()(const Acc& acc, const Unit& u, int wr, int wc, int fr, int fq) const {
;     ...
;         for (int ai = 0; ai < 2; ++ai)
; #pragma unroll
;             for (int m = 0; m < 4; ++m) { const size_t off = (size_t)(u.pm * BM + ai * HALF + wr * 64 + m * 16 + fr) * DM + col0;
; #pragma unroll
;                 for (int bj = 0; bj < 2; ++bj) { f32x4 b0, b1;
;                     if constexpr (BASE16) { const f16x8 bv = *(const f16x8*)((const f16*)base + off + bj * HALF);
;                         b0 = (f32x4){(float)bv[0], (float)bv[1], (float)bv[2], (float)bv[3]}; b1 = (f32x4){(float)bv[4], (float)bv[5], (float)bv[6], (float)bv[7]}; }
;                     else { b0 = *(const f32x4*)((const float*)base + off + bj * HALF); b1 = *(const f32x4*)((const float*)base + off + bj * HALF + 4); }
;                     const f32x4 v0 = b0 + gv[bj][0] * acc[ai][bj][m][0], v1 = b1 + gv[bj][1] * acc[ai][bj][m][1];
;                     u32x4 w; w.x = pkh(v0[0], v0[1]); w.y = pkh(v0[2], v0[3]); w.z = pkh(v1[0], v1[1]); w.w = pkh(v1[2], v1[3]);
;                     *(u32x4*)(out + off + bj * HALF) = w; }
;                 if (m & 1) asm volatile("" ::: "memory"); }
	v_pk_fma_f32 v[80:81], v[80:81], v[132:133], v[84:85]
	v_pk_fma_f32 v[78:79], v[78:79], v[130:131], v[82:83]
	s_waitcnt vmcnt(0)
	v_pk_fma_f32 v[82:83], v[76:77], v[136:137], v[88:89]
	v_pk_fma_f32 v[76:77], v[74:75], v[134:135], v[86:87]
	v_cvt_pk_f16_f32 v74, v78, v79
	v_cvt_pk_f16_f32 v75, v80, v81
	v_cvt_pk_f16_f32 v76, v76, v77
	v_cvt_pk_f16_f32 v77, v82, v83
	global_store_dwordx4 v[90:91], v[74:77], off sc0 sc1
	global_load_dwordx4 v[74:77], v[100:101], off offset:512 nt
	s_nop 0
	global_load_dwordx4 v[78:81], v[100:101], off offset:528 nt
	v_add_u32_e32 v82, 0x80, v164
	v_ashrrev_i32_e32 v83, 31, v82
	v_lshlrev_b64 v[82:83], 10, v[82:83]
	v_lshl_add_u64 v[82:83], v[82:83], 0, v[162:163]
	v_lshl_add_u64 v[84:85], v[82:83], 2, s[44:45]
	s_waitcnt vmcnt(1)
	v_pk_fma_f32 v[72:73], v[72:73], v[144:145], v[76:77]
	v_pk_fma_f32 v[70:71], v[70:71], v[142:143], v[74:75]
	s_waitcnt vmcnt(0)
	v_pk_fma_f32 v[74:75], v[68:69], v[140:141], v[80:81]
	v_pk_fma_f32 v[68:69], v[66:67], v[138:139], v[78:79]
	v_cvt_pk_f16_f32 v66, v70, v71
	v_cvt_pk_f16_f32 v67, v72, v73
	v_cvt_pk_f16_f32 v68, v68, v69
	v_cvt_pk_f16_f32 v69, v74, v75
	global_store_dwordx4 v[90:91], v[66:69], off offset:256 sc0 sc1
	global_load_dwordx4 v[66:69], v[84:85], off nt
	global_load_dwordx4 v[70:73], v[84:85], off offset:16 nt
	v_lshl_add_u64 v[74:75], v[82:83], 1, s[66:67]
	s_waitcnt vmcnt(1)
	v_pk_fma_f32 v[64:65], v[64:65], v[132:133], v[68:69]
	v_pk_fma_f32 v[62:63], v[62:63], v[130:131], v[66:67]
	s_waitcnt vmcnt(0)
	v_pk_fma_f32 v[66:67], v[60:61], v[136:137], v[72:73]
	v_pk_fma_f32 v[60:61], v[58:59], v[134:135], v[70:71]
	v_cvt_pk_f16_f32 v58, v62, v63
	v_cvt_pk_f16_f32 v59, v64, v65
	v_cvt_pk_f16_f32 v60, v60, v61
	v_cvt_pk_f16_f32 v61, v66, v67
	global_store_dwordx4 v[74:75], v[58:61], off sc0 sc1
	global_load_dwordx4 v[58:61], v[84:85], off offset:512 nt
	s_nop 0
	global_load_dwordx4 v[62:65], v[84:85], off offset:528 nt
	v_add_u32_e32 v66, 0x90, v164
	v_ashrrev_i32_e32 v67, 31, v66
	v_lshlrev_b64 v[66:67], 10, v[66:67]
	v_lshl_add_u64 v[66:67], v[66:67], 0, v[162:163]
	v_lshl_add_u64 v[68:69], v[66:67], 2, s[44:45]
	s_waitcnt vmcnt(1)
	v_pk_fma_f32 v[56:57], v[56:57], v[144:145], v[60:61]
	v_pk_fma_f32 v[54:55], v[54:55], v[142:143], v[58:59]
	s_waitcnt vmcnt(0)
	v_pk_fma_f32 v[58:59], v[52:53], v[140:141], v[64:65]
	v_pk_fma_f32 v[52:53], v[50:51], v[138:139], v[62:63]
	v_cvt_pk_f16_f32 v50, v54, v55
	v_cvt_pk_f16_f32 v51, v56, v57
	v_cvt_pk_f16_f32 v52, v52, v53
	v_cvt_pk_f16_f32 v53, v58, v59
	global_store_dwordx4 v[74:75], v[50:53], off offset:256 sc0 sc1
	global_load_dwordx4 v[50:53], v[68:69], off nt
	s_nop 0
	global_load_dwordx4 v[54:57], v[68:69], off offset:16 nt
	v_lshl_add_u64 v[58:59], v[66:67], 1, s[66:67]
	s_waitcnt vmcnt(1)
	v_pk_fma_f32 v[48:49], v[48:49], v[132:133], v[52:53]
	v_pk_fma_f32 v[46:47], v[46:47], v[130:131], v[50:51]
	s_waitcnt vmcnt(0)
	v_pk_fma_f32 v[50:51], v[44:45], v[136:137], v[56:57]
	v_pk_fma_f32 v[44:45], v[42:43], v[134:135], v[54:55]
	v_cvt_pk_f16_f32 v42, v46, v47
	v_cvt_pk_f16_f32 v43, v48, v49
	v_cvt_pk_f16_f32 v44, v44, v45
	v_cvt_pk_f16_f32 v45, v50, v51
	global_store_dwordx4 v[58:59], v[42:45], off sc0 sc1
	global_load_dwordx4 v[42:45], v[68:69], off offset:512 nt
	s_nop 0
	global_load_dwordx4 v[46:49], v[68:69], off offset:528 nt
	v_add_u32_e32 v50, 0xa0, v164
	v_ashrrev_i32_e32 v51, 31, v50
	v_lshlrev_b64 v[50:51], 10, v[50:51]
	v_lshl_add_u64 v[50:51], v[50:51], 0, v[162:163]
	v_lshl_add_u64 v[52:53], v[50:51], 2, s[44:45]
	s_waitcnt vmcnt(1)
	v_pk_fma_f32 v[40:41], v[40:41], v[144:145], v[44:45]
	v_pk_fma_f32 v[38:39], v[38:39], v[142:143], v[42:43]
	s_waitcnt vmcnt(0)
	v_pk_fma_f32 v[42:43], v[36:37], v[140:141], v[48:49]
	v_pk_fma_f32 v[36:37], v[34:35], v[138:139], v[46:47]
	v_cvt_pk_f16_f32 v34, v38, v39
	v_cvt_pk_f16_f32 v35, v40, v41
	v_cvt_pk_f16_f32 v36, v36, v37
	v_cvt_pk_f16_f32 v37, v42, v43
	global_store_dwordx4 v[58:59], v[34:37], off offset:256 sc0 sc1
	global_load_dwordx4 v[34:37], v[52:53], off nt
	global_load_dwordx4 v[38:41], v[52:53], off offset:16 nt
	v_lshl_add_u64 v[42:43], v[50:51], 1, s[66:67]
	s_waitcnt vmcnt(1)
	v_pk_fma_f32 v[32:33], v[32:33], v[132:133], v[36:37]
	v_pk_fma_f32 v[30:31], v[30:31], v[130:131], v[34:35]
	s_waitcnt vmcnt(0)
	v_pk_fma_f32 v[34:35], v[28:29], v[136:137], v[40:41]
	v_pk_fma_f32 v[28:29], v[26:27], v[134:135], v[38:39]
	v_cvt_pk_f16_f32 v26, v30, v31
	v_cvt_pk_f16_f32 v27, v32, v33
	v_cvt_pk_f16_f32 v28, v28, v29
	v_cvt_pk_f16_f32 v29, v34, v35
	global_store_dwordx4 v[42:43], v[26:29], off sc0 sc1
	global_load_dwordx4 v[26:29], v[52:53], off offset:512 nt
	s_nop 0
	global_load_dwordx4 v[30:33], v[52:53], off offset:528 nt
	v_add_u32_e32 v34, 0xb0, v164
	v_ashrrev_i32_e32 v35, 31, v34
	v_lshlrev_b64 v[34:35], 10, v[34:35]
	v_lshl_add_u64 v[34:35], v[34:35], 0, v[162:163]
	v_lshl_add_u64 v[36:37], v[34:35], 2, s[44:45]
	s_waitcnt vmcnt(1)
	v_pk_fma_f32 v[24:25], v[24:25], v[144:145], v[28:29]
	v_pk_fma_f32 v[22:23], v[22:23], v[142:143], v[26:27]
	s_waitcnt vmcnt(0)
	v_pk_fma_f32 v[26:27], v[20:21], v[140:141], v[32:33]
	v_pk_fma_f32 v[20:21], v[18:19], v[138:139], v[30:31]
	v_cvt_pk_f16_f32 v18, v22, v23
	v_cvt_pk_f16_f32 v19, v24, v25
	v_cvt_pk_f16_f32 v20, v20, v21
	v_cvt_pk_f16_f32 v21, v26, v27
	global_store_dwordx4 v[42:43], v[18:21], off offset:256 sc0 sc1
	global_load_dwordx4 v[18:21], v[36:37], off nt
	s_nop 0
	global_load_dwordx4 v[22:25], v[36:37], off offset:16 nt
	v_lshl_add_u64 v[26:27], v[34:35], 1, s[66:67]
	s_waitcnt vmcnt(1)
	v_pk_fma_f32 v[16:17], v[16:17], v[132:133], v[20:21]
	v_pk_fma_f32 v[14:15], v[14:15], v[130:131], v[18:19]
	s_waitcnt vmcnt(0)
	v_pk_fma_f32 v[18:19], v[12:13], v[136:137], v[24:25]
	v_pk_fma_f32 v[12:13], v[10:11], v[134:135], v[22:23]
	v_cvt_pk_f16_f32 v10, v14, v15
	v_cvt_pk_f16_f32 v11, v16, v17
	v_cvt_pk_f16_f32 v12, v12, v13
	v_cvt_pk_f16_f32 v13, v18, v19
	global_store_dwordx4 v[26:27], v[10:13], off sc0 sc1
	global_load_dwordx4 v[10:13], v[36:37], off offset:512 nt
	s_nop 0
	global_load_dwordx4 v[14:17], v[36:37], off offset:528 nt
	s_waitcnt vmcnt(1)
	v_pk_fma_f32 v[8:9], v[8:9], v[144:145], v[12:13]
	v_pk_fma_f32 v[6:7], v[6:7], v[142:143], v[10:11]
	s_waitcnt vmcnt(0)
	v_pk_fma_f32 v[10:11], v[4:5], v[140:141], v[16:17]
	v_pk_fma_f32 v[4:5], v[2:3], v[138:139], v[14:15]
	v_cvt_pk_f16_f32 v2, v6, v7
	v_cvt_pk_f16_f32 v3, v8, v9
	v_cvt_pk_f16_f32 v4, v4, v5
	v_cvt_pk_f16_f32 v5, v10, v11
	global_store_dwordx4 v[26:27], v[2:5], off offset:256 sc0 sc1
	s_cbranch_vccnz .LBB0_707
	s_andn2_b64 vcc, exec, s[6:7]
	s_cbranch_vccnz .LBB0_706
	s_barrier
	s_branch .LBB0_706

; #define LAS __attribute__((address_space(3)))
; template <bool BF> __device__ __forceinline__ unsigned pk16(float lo, float hi) { return BF ? pkb(lo, hi) : pkh(lo, hi); }
; template <bool BF, class RowMap>
; __device__ __forceinline__ void cvt_block(const float* W, int K, int N, f16* WT, const RowMap& rm, int item, int tid, LAS unsigned char* S) {
;     const int lane = tid & 63, wave = tid >> 6;
;     const int nblk = N / 128, kb = item / nblk, nb = item % nblk, k0 = 256 * kb, n0 = 128 * nb;
;     const float* src = W + (size_t)(k0 + 32 * wave + (lane >> 5)) * N + n0 + 4 * (lane & 31);
;     f32x4 v[16];
; #pragma unroll
;     for (int i = 0; i < 16; ++i) v[i] = *(const f32x4*)(src + (size_t)(2 * i) * N);
; #pragma unroll
;     for (int i = 0; i < 16; ++i) { u32x2 w; w.x = pk16<BF>(v[i][0], v[i][1]); w.y = pk16<BF>(v[i][2], v[i][3]);
;         *(LAS u32x2*)(S + (32 * wave + 2 * i + (lane >> 5)) * CVB_RS + 8 * (lane & 31)) = w; }
;     __syncthreads();
; __device__ __forceinline__ void cvt_moe(const float* w1, const float* w3, const float* w2, f16* W13, f16* W2T, int tid, LAS unsigned char* S) {
;     ...
;     for (int it = blockIdx.x; it < NIT; it += gridDim.x) {
;         const int e = it / (2 * I13 + I2); int r = it % (2 * I13 + I2);
;         if (r < I13) { cvt_block<MOE_BF16>(w1 + (size_t)e * DM * DE, DM, DE, W13 + (size_t)e * 2 * DE * DM, MapGLU{0}, r, tid, S); continue; } r -= I13;
;         if (r < I13) { cvt_block<MOE_BF16>(w3 + (size_t)e * DM * DE, DM, DE, W13 + (size_t)e * 2 * DE * DM, MapGLU{128}, r, tid, S); continue; } r -= I13;
;         cvt_block<MOE_BF16>(w2 + (size_t)e * DE * DM, DE, DM, W2T + (size_t)e * DM * DE, MapPlain{}, r, tid, S);
.LBB0_1209:
	s_mul_hi_i32 s0, s35, 0x3e0f83e1
	s_lshr_b32 s2, s0, 31
	s_ashr_i32 s37, s0, 6
	s_add_i32 s37, s37, s2
	s_mul_i32 s0, s37, 0xfffffef8
	s_add_i32 s36, s35, s0
	s_cmpk_gt_i32 s36, 0x57
	s_mov_b64 s[2:3], -1
	s_cbranch_scc0 .LBB0_1215
	s_cmpk_gt_u32 s36, 0xaf
	s_cbranch_scc0 .LBB0_1212
	v_readlane_b32 s40, v251, 0
	s_mul_i32 s2, s37, 0xb00000
	v_readlane_b32 s44, v251, 4
	s_mul_hi_i32 s0, s37, 0xb00000
	v_readlane_b32 s41, v251, 1
	v_readlane_b32 s45, v251, 5
	s_add_u32 s40, s44, s2
	s_addc_u32 s41, s45, s0
	s_mul_i32 s2, s37, 0x580000
	s_mul_hi_i32 s0, s37, 0x580000
	s_add_u32 s3, s78, s2
	v_readlane_b32 s2, v250, 16
	s_addc_u32 s38, s2, s0
	s_lshl_b32 s0, s37, 8
	s_sub_i32 s0, s6, s0
	s_and_b32 s39, s0, 0xf00
	v_or_b32_e32 v5, s39, v1
	s_and_b32 s2, s4, 0x380
	v_lshlrev_b32_e32 v22, 12, v5
	v_mov_b32_e32 v23, v3
	v_lshl_add_u64 v[22:23], s[40:41], 0, v[22:23]
	s_lshl_b32 s0, s2, 2
	v_lshl_add_u64 v[22:23], v[22:23], 0, s[0:1]
	v_lshl_add_u64 v[82:83], v[22:23], 0, v[2:3]
	s_movk_i32 s0, 0x2000
	v_add_co_u32_e32 v26, vcc, s0, v82
	s_movk_i32 s0, 0x4000
	s_nop 0
	v_addc_co_u32_e32 v27, vcc, 0, v83, vcc
	v_add_co_u32_e32 v30, vcc, s0, v82
	s_movk_i32 s0, 0x6000
	s_nop 0
	v_addc_co_u32_e32 v31, vcc, 0, v83, vcc
	v_add_co_u32_e32 v34, vcc, s0, v82
	s_mov_b32 s0, 0x8000
	s_nop 0
	v_addc_co_u32_e32 v35, vcc, 0, v83, vcc
	v_add_co_u32_e32 v38, vcc, s0, v82
	global_load_dwordx4 v[22:25], v[82:83], off nt
	s_nop 0
	global_load_dwordx4 v[26:29], v[26:27], off nt
	v_addc_co_u32_e32 v39, vcc, 0, v83, vcc
	v_add_co_u32_e32 v42, vcc, s10, v82
	global_load_dwordx4 v[30:33], v[30:31], off nt
	s_nop 0
	global_load_dwordx4 v[34:37], v[34:35], off nt
	v_addc_co_u32_e32 v43, vcc, 0, v83, vcc
	v_add_co_u32_e32 v46, vcc, s11, v82
	global_load_dwordx4 v[38:41], v[38:39], off nt
	s_nop 0
	global_load_dwordx4 v[42:45], v[42:43], off nt
	v_addc_co_u32_e32 v47, vcc, 0, v83, vcc
	v_add_co_u32_e32 v50, vcc, s12, v82
	s_lshl_b32 s0, s39, 1
	s_nop 0
	v_addc_co_u32_e32 v51, vcc, 0, v83, vcc
	v_add_co_u32_e32 v54, vcc, s13, v82
	global_load_dwordx4 v[46:49], v[46:47], off nt
	s_nop 0
	global_load_dwordx4 v[50:53], v[50:51], off nt
	v_addc_co_u32_e32 v55, vcc, 0, v83, vcc
	v_add_co_u32_e32 v58, vcc, s14, v82
	s_add_u32 s40, s3, s0
	s_nop 0
	v_addc_co_u32_e32 v59, vcc, 0, v83, vcc
	v_add_co_u32_e32 v62, vcc, s15, v82
	global_load_dwordx4 v[54:57], v[54:55], off nt
	s_nop 0
	global_load_dwordx4 v[58:61], v[58:59], off nt
	v_addc_co_u32_e32 v63, vcc, 0, v83, vcc
	v_add_co_u32_e32 v66, vcc, s16, v82
	s_addc_u32 s41, s38, 0
	s_nop 0
	v_addc_co_u32_e32 v67, vcc, 0, v83, vcc
	v_add_co_u32_e32 v70, vcc, s17, v82
	global_load_dwordx4 v[62:65], v[62:63], off nt
	s_nop 0
	global_load_dwordx4 v[66:69], v[66:67], off nt
	v_addc_co_u32_e32 v71, vcc, 0, v83, vcc
	v_add_co_u32_e32 v74, vcc, s18, v82
	v_mov_b32_e32 v5, v3
	s_nop 0
	v_addc_co_u32_e32 v75, vcc, 0, v83, vcc
	v_add_co_u32_e32 v78, vcc, s19, v82
	global_load_dwordx4 v[70:73], v[70:71], off nt
	s_nop 0
	global_load_dwordx4 v[74:77], v[74:75], off nt
	v_addc_co_u32_e32 v79, vcc, 0, v83, vcc
	v_add_co_u32_e32 v82, vcc, s20, v82
	global_load_dwordx4 v[78:81], v[78:79], off nt
	s_nop 0
	v_addc_co_u32_e32 v83, vcc, 0, v83, vcc
	global_load_dwordx4 v[82:85], v[82:83], off nt
	v_readlane_b32 s42, v251, 2
	v_readlane_b32 s43, v251, 3
	v_readlane_b32 s46, v251, 6
	v_readlane_b32 s47, v251, 7
	s_waitcnt vmcnt(15)
	v_cvt_pk_bf16_f32 v22, v22, v23
	v_cvt_pk_bf16_f32 v23, v24, v25
	s_waitcnt vmcnt(14)
	v_cvt_pk_bf16_f32 v24, v26, v27
	v_cvt_pk_bf16_f32 v25, v28, v29
	ds_write2_b64 v14, v[22:23], v[24:25] offset1:66
	s_waitcnt vmcnt(13)
	v_cvt_pk_bf16_f32 v22, v30, v31
	v_cvt_pk_bf16_f32 v23, v32, v33
	s_waitcnt vmcnt(12)
	v_cvt_pk_bf16_f32 v24, v34, v35
	v_cvt_pk_bf16_f32 v25, v36, v37
	ds_write2_b64 v14, v[22:23], v[24:25] offset0:132 offset1:198
	s_waitcnt vmcnt(11)
	v_cvt_pk_bf16_f32 v22, v38, v39
	v_cvt_pk_bf16_f32 v23, v40, v41
	s_waitcnt vmcnt(10)
	v_cvt_pk_bf16_f32 v24, v42, v43
	v_cvt_pk_bf16_f32 v25, v44, v45
	ds_write2_b64 v18, v[22:23], v[24:25] offset0:8 offset1:74
	s_waitcnt vmcnt(9)
	v_cvt_pk_bf16_f32 v22, v46, v47
	v_cvt_pk_bf16_f32 v23, v48, v49
	s_waitcnt vmcnt(8)
	v_cvt_pk_bf16_f32 v24, v50, v51
	v_cvt_pk_bf16_f32 v25, v52, v53
	ds_write2_b64 v18, v[22:23], v[24:25] offset0:140 offset1:206
	s_waitcnt vmcnt(7)
	v_cvt_pk_bf16_f32 v22, v54, v55
	v_cvt_pk_bf16_f32 v23, v56, v57
	s_waitcnt vmcnt(6)
	v_cvt_pk_bf16_f32 v24, v58, v59
	v_cvt_pk_bf16_f32 v25, v60, v61
	ds_write2_b64 v19, v[22:23], v[24:25] offset0:16 offset1:82
	s_waitcnt vmcnt(5)
	v_cvt_pk_bf16_f32 v22, v62, v63
	v_cvt_pk_bf16_f32 v23, v64, v65
	s_waitcnt vmcnt(4)
	v_cvt_pk_bf16_f32 v24, v66, v67
	v_cvt_pk_bf16_f32 v25, v68, v69
	ds_write2_b64 v19, v[22:23], v[24:25] offset0:148 offset1:214
	s_waitcnt vmcnt(3)
	v_cvt_pk_bf16_f32 v22, v70, v71
	v_cvt_pk_bf16_f32 v23, v72, v73
	s_waitcnt vmcnt(2)
	v_cvt_pk_bf16_f32 v24, v74, v75
	v_cvt_pk_bf16_f32 v25, v76, v77
	ds_write2_b64 v20, v[22:23], v[24:25] offset0:24 offset1:90
	s_waitcnt vmcnt(1)
	v_cvt_pk_bf16_f32 v22, v78, v79
	v_cvt_pk_bf16_f32 v23, v80, v81
	s_waitcnt vmcnt(0)
	v_cvt_pk_bf16_f32 v24, v82, v83
	v_cvt_pk_bf16_f32 v25, v84, v85
	ds_write2_b64 v20, v[22:23], v[24:25] offset0:156 offset1:222
	s_waitcnt lgkmcnt(0)
	s_barrier
; #define LAS __attribute__((address_space(3)))
; #define LDS_WAIT() asm volatile("s_waitcnt lgkmcnt(0)" ::: "memory")
; template <bool BF, class RowMap>
; __device__ __forceinline__ void cvt_block(const float* W, int K, int N, f16* WT, const RowMap& rm, int item, int tid, LAS unsigned char* S) {
;     ...
;     const int g = lane >> 4, i16 = lane & 15, q_ = i16 >> 2, p_ = i16 & 3;
;     LAS unsigned char* T = S;
;     u32x4 wv[8];
; #pragma unroll
;     for (int st = 0; st < 8; ++st) {
;         const int ch = 4 * st + g;
;         const LAS unsigned char* ap = S + (8 * ch + q_) * CVB_RS + (16 * wave + 4 * p_) * 2;
;         const s16x4 lo = __builtin_amdgcn_ds_read_tr16_b64_v4i16((LAS s16x4*)ap);
;         const s16x4 hi = __builtin_amdgcn_ds_read_tr16_b64_v4i16((LAS s16x4*)(ap + 4 * CVB_RS));
;         const u32x2 l2 = __builtin_bit_cast(u32x2, lo), h2 = __builtin_bit_cast(u32x2, hi); wv[st].x = l2.x; wv[st].y = l2.y; wv[st].z = h2.x; wv[st].w = h2.y;
;     }
;     __syncthreads();
; #pragma unroll
;     for (int st = 0; st < 8; ++st) *(LAS u32x4*)(T + (16 * wave + i16) * CVT_TS + 16 * (4 * st + g)) = wv[st];
;     LDS_WAIT();
; #pragma unroll
;     for (int j = 0; j < 8; ++j) { const int nr = 16 * wave + 2 * j + (lane >> 5), ch = lane & 31;
;         const u32x4 w = *(const LAS u32x4*)(T + nr * CVT_TS + 16 * ch);
;         *(u32x4*)(WT + (size_t)rm(n0 + nr) * K + k0 + 8 * ch) = w; }
;     __syncthreads();
; __device__ __forceinline__ void cvt_moe(const float* w1, const float* w3, const float* w2, f16* W13, f16* W2T, int tid, LAS unsigned char* S) {
;     ...
;         if (r < I13) { cvt_block<MOE_BF16>(w3 + (size_t)e * DM * DE, DM, DE, W13 + (size_t)e * 2 * DE * DM, MapGLU{128}, r, tid, S); continue; } r -= I13;
	ds_read_b64_tr_b16 v[22:23], v15
	ds_read_b64_tr_b16 v[24:25], v15 offset:1056
	ds_read_b64_tr_b16 v[26:27], v15 offset:8448
	ds_read_b64_tr_b16 v[28:29], v15 offset:9504
	ds_read_b64_tr_b16 v[30:31], v15 offset:16896
	ds_read_b64_tr_b16 v[32:33], v15 offset:17952
	ds_read_b64_tr_b16 v[34:35], v15 offset:25344
	ds_read_b64_tr_b16 v[36:37], v15 offset:26400
	ds_read_b64_tr_b16 v[38:39], v15 offset:33792
	ds_read_b64_tr_b16 v[40:41], v15 offset:34848
	ds_read_b64_tr_b16 v[42:43], v15 offset:42240
	ds_read_b64_tr_b16 v[44:45], v15 offset:43296
	ds_read_b64_tr_b16 v[46:47], v15 offset:50688
	ds_read_b64_tr_b16 v[48:49], v15 offset:51744
	ds_read_b64_tr_b16 v[50:51], v15 offset:59136
	ds_read_b64_tr_b16 v[52:53], v15 offset:60192
	s_waitcnt lgkmcnt(0)
	s_barrier
	ds_write_b128 v16, v[22:25]
	ds_write_b128 v16, v[26:29] offset:64
	ds_write_b128 v16, v[30:33] offset:128
	ds_write_b128 v16, v[34:37] offset:192
	ds_write_b128 v16, v[38:41] offset:256
	ds_write_b128 v16, v[42:45] offset:320
	ds_write_b128 v16, v[46:49] offset:384
	ds_write_b128 v16, v[50:53] offset:448
	s_waitcnt lgkmcnt(0)
	v_lshl_add_u64 v[30:31], s[40:41], 0, v[4:5]
	ds_read_b128 v[22:25], v17
	v_or_b32_e32 v5, s2, v6
	v_mul_u32_u24_e32 v26, 0x1600, v5
	v_mov_b32_e32 v27, v3
	v_lshl_add_u64 v[32:33], v[30:31], 0, v[26:27]
	ds_read_b128 v[26:29], v17 offset:1056
	v_or_b32_e32 v5, s2, v7
	s_waitcnt lgkmcnt(1)
	global_store_dwordx4 v[32:33], v[22:25], off sc0 sc1
	s_nop 1
	v_mul_u32_u24_e32 v22, 0x1600, v5
	v_mov_b32_e32 v23, v3
	v_lshl_add_u64 v[22:23], v[30:31], 0, v[22:23]
	s_waitcnt lgkmcnt(0)
	global_store_dwordx4 v[22:23], v[26:29], off sc0 sc1
	ds_read_b128 v[22:25], v17 offset:2112
	v_or_b32_e32 v5, s2, v8
	v_mul_u32_u24_e32 v26, 0x1600, v5
	v_mov_b32_e32 v27, v3
	v_lshl_add_u64 v[32:33], v[30:31], 0, v[26:27]
	ds_read_b128 v[26:29], v17 offset:3168
	v_or_b32_e32 v5, s2, v9
	s_waitcnt lgkmcnt(1)
	global_store_dwordx4 v[32:33], v[22:25], off sc0 sc1
	s_nop 1
	v_mul_u32_u24_e32 v22, 0x1600, v5
	v_mov_b32_e32 v23, v3
	v_lshl_add_u64 v[22:23], v[30:31], 0, v[22:23]
	s_waitcnt lgkmcnt(0)
	global_store_dwordx4 v[22:23], v[26:29], off sc0 sc1
	ds_read_b128 v[22:25], v17 offset:4224
	v_or_b32_e32 v5, s2, v10
	v_mul_u32_u24_e32 v26, 0x1600, v5
	v_mov_b32_e32 v27, v3
	v_lshl_add_u64 v[32:33], v[30:31], 0, v[26:27]
	ds_read_b128 v[26:29], v17 offset:5280
	v_or_b32_e32 v5, s2, v11
	s_waitcnt lgkmcnt(1)
	global_store_dwordx4 v[32:33], v[22:25], off sc0 sc1
	s_nop 1
	v_mul_u32_u24_e32 v22, 0x1600, v5
	v_mov_b32_e32 v23, v3
	v_lshl_add_u64 v[22:23], v[30:31], 0, v[22:23]
	s_waitcnt lgkmcnt(0)
	global_store_dwordx4 v[22:23], v[26:29], off sc0 sc1
	ds_read_b128 v[22:25], v17 offset:6336
	v_or_b32_e32 v5, s2, v12
	v_mul_u32_u24_e32 v26, 0x1600, v5
	v_mov_b32_e32 v27, v3
	v_lshl_add_u64 v[32:33], v[30:31], 0, v[26:27]
	ds_read_b128 v[26:29], v17 offset:7392
	v_or_b32_e32 v5, s2, v13
	s_waitcnt lgkmcnt(1)
	global_store_dwordx4 v[32:33], v[22:25], off sc0 sc1
	s_mov_b64 s[2:3], 0
	s_nop 0
	v_mul_u32_u24_e32 v22, 0x1600, v5
	v_mov_b32_e32 v23, v3
	v_lshl_add_u64 v[22:23], v[30:31], 0, v[22:23]
	s_waitcnt lgkmcnt(0)
	global_store_dwordx4 v[22:23], v[26:29], off sc0 sc1
	s_barrier
.LBB0_1212:
	s_andn2_b64 vcc, exec, s[2:3]
	s_cbranch_vccnz .LBB0_1214
	v_readlane_b32 s40, v251, 0
	s_mul_i32 s2, s37, 0xb00000
	v_readlane_b32 s42, v251, 2
	s_mul_hi_i32 s0, s37, 0xb00000
	v_readlane_b32 s41, v251, 1
	v_readlane_b32 s43, v251, 3
	s_add_u32 s40, s42, s2
	s_addc_u32 s41, s43, s0
	s_add_u32 s3, s84, s2
	s_addc_u32 s38, s85, s0
	s_add_i32 s0, s36, 0xffa8
	s_bfe_u32 s2, s0, 0x70001
	s_mulk_i32 s2, 0xbb
	s_bfe_u32 s39, s2, 0x5000b
	s_mul_i32 s2, s39, 22
	s_sub_i32 s2, s0, s2
	v_lshl_or_b32 v5, s39, 8, v1
	s_and_b32 s0, s2, 0xff
	v_mul_u32_u24_e32 v22, 0x2c00, v5
	v_mov_b32_e32 v23, v3
	v_lshl_add_u64 v[22:23], s[40:41], 0, v[22:23]
	s_lshl_b32 s0, s0, 9
	v_lshl_add_u64 v[22:23], v[22:23], 0, s[0:1]
	v_lshl_add_u64 v[82:83], v[22:23], 0, v[2:3]
	v_add_co_u32_e32 v26, vcc, s21, v82
	s_lshl_b32 s0, s39, 9
	s_nop 0
	v_addc_co_u32_e32 v27, vcc, 0, v83, vcc
	v_add_co_u32_e32 v30, vcc, s22, v82
	global_load_dwordx4 v[22:25], v[82:83], off nt
	s_nop 0
	global_load_dwordx4 v[26:29], v[26:27], off offset:2048 nt
	v_addc_co_u32_e32 v31, vcc, 0, v83, vcc
	v_add_co_u32_e32 v34, vcc, s13, v82
	s_add_u32 s40, s3, s0
	s_nop 0
	v_addc_co_u32_e32 v35, vcc, 0, v83, vcc
	v_add_co_u32_e32 v38, vcc, s16, v82
	global_load_dwordx4 v[30:33], v[30:31], off nt
	s_nop 0
	global_load_dwordx4 v[34:37], v[34:35], off offset:2048 nt
	v_addc_co_u32_e32 v39, vcc, 0, v83, vcc
	v_add_co_u32_e32 v42, vcc, s23, v82
	s_addc_u32 s41, s38, 0
	s_nop 0
	v_addc_co_u32_e32 v43, vcc, 0, v83, vcc
	v_add_co_u32_e32 v46, vcc, s24, v82
	global_load_dwordx4 v[38:41], v[38:39], off nt
	s_nop 0
	global_load_dwordx4 v[42:45], v[42:43], off offset:2048 nt
	v_addc_co_u32_e32 v47, vcc, 0, v83, vcc
	v_add_co_u32_e32 v50, vcc, s25, v82
	s_lshl_b32 s0, s2, 8
	s_nop 0
	v_addc_co_u32_e32 v51, vcc, 0, v83, vcc
	v_add_co_u32_e32 v54, vcc, s26, v82
	global_load_dwordx4 v[46:49], v[46:47], off nt
	s_nop 0
	global_load_dwordx4 v[50:53], v[50:51], off offset:2048 nt
	v_addc_co_u32_e32 v55, vcc, 0, v83, vcc
	v_add_co_u32_e32 v58, vcc, s27, v82
	v_mov_b32_e32 v5, v3
	s_nop 0
	v_addc_co_u32_e32 v59, vcc, 0, v83, vcc
	v_add_co_u32_e32 v62, vcc, s28, v82
	global_load_dwordx4 v[54:57], v[54:55], off nt
	s_nop 0
	global_load_dwordx4 v[58:61], v[58:59], off offset:2048 nt
	v_addc_co_u32_e32 v63, vcc, 0, v83, vcc
	v_add_co_u32_e32 v66, vcc, s29, v82
	s_and_b32 s0, s0, 0x3f00
	s_nop 0
	v_addc_co_u32_e32 v67, vcc, 0, v83, vcc
	v_add_co_u32_e32 v70, vcc, s30, v82
	global_load_dwordx4 v[62:65], v[62:63], off nt
	s_nop 0
	global_load_dwordx4 v[66:69], v[66:67], off offset:2048 nt
	v_addc_co_u32_e32 v71, vcc, 0, v83, vcc
	v_add_co_u32_e32 v74, vcc, s31, v82
	v_readlane_b32 s44, v251, 4
	s_nop 0
	v_addc_co_u32_e32 v75, vcc, 0, v83, vcc
	v_add_co_u32_e32 v78, vcc, s33, v82
	global_load_dwordx4 v[70:73], v[70:71], off nt
	s_nop 0
	global_load_dwordx4 v[74:77], v[74:75], off offset:2048 nt
	v_addc_co_u32_e32 v79, vcc, 0, v83, vcc
	v_add_co_u32_e32 v82, vcc, s34, v82
	global_load_dwordx4 v[78:81], v[78:79], off nt
	s_nop 0
	v_addc_co_u32_e32 v83, vcc, 0, v83, vcc
	global_load_dwordx4 v[82:85], v[82:83], off offset:2048 nt
	v_readlane_b32 s45, v251, 5
	v_readlane_b32 s46, v251, 6
	v_readlane_b32 s47, v251, 7
	s_waitcnt vmcnt(15)
; #define LAS __attribute__((address_space(3)))
; #define LDS_WAIT() asm volatile("s_waitcnt lgkmcnt(0)" ::: "memory")
; template <bool BF, class RowMap>
; __device__ __forceinline__ void cvt_block(const float* W, int K, int N, f16* WT, const RowMap& rm, int item, int tid, LAS unsigned char* S) {
;     ...
;     const int g = lane >> 4, i16 = lane & 15, q_ = i16 >> 2, p_ = i16 & 3;
;     LAS unsigned char* T = S;
;     u32x4 wv[8];
; #pragma unroll
;     for (int st = 0; st < 8; ++st) {
;         const int ch = 4 * st + g;
;         const LAS unsigned char* ap = S + (8 * ch + q_) * CVB_RS + (16 * wave + 4 * p_) * 2;
;         const s16x4 lo = __builtin_amdgcn_ds_read_tr16_b64_v4i16((LAS s16x4*)ap);
;         const s16x4 hi = __builtin_amdgcn_ds_read_tr16_b64_v4i16((LAS s16x4*)(ap + 4 * CVB_RS));
;         const u32x2 l2 = __builtin_bit_cast(u32x2, lo), h2 = __builtin_bit_cast(u32x2, hi); wv[st].x = l2.x; wv[st].y = l2.y; wv[st].z = h2.x; wv[st].w = h2.y;
;     }
;     __syncthreads();
; #pragma unroll
;     for (int st = 0; st < 8; ++st) *(LAS u32x4*)(T + (16 * wave + i16) * CVT_TS + 16 * (4 * st + g)) = wv[st];
;     LDS_WAIT();
; #pragma unroll
;     for (int j = 0; j < 8; ++j) { const int nr = 16 * wave + 2 * j + (lane >> 5), ch = lane & 31;
;         const u32x4 w = *(const LAS u32x4*)(T + nr * CVT_TS + 16 * ch);
;         *(u32x4*)(WT + (size_t)rm(n0 + nr) * K + k0 + 8 * ch) = w; }
;     __syncthreads();
	v_cvt_pk_bf16_f32 v22, v22, v23
	v_cvt_pk_bf16_f32 v23, v24, v25
	s_waitcnt vmcnt(14)
	v_cvt_pk_bf16_f32 v24, v26, v27
	v_cvt_pk_bf16_f32 v25, v28, v29
	ds_write2_b64 v14, v[22:23], v[24:25] offset1:66
	s_waitcnt vmcnt(13)
	v_cvt_pk_bf16_f32 v22, v30, v31
	v_cvt_pk_bf16_f32 v23, v32, v33
	s_waitcnt vmcnt(12)
	v_cvt_pk_bf16_f32 v24, v34, v35
	v_cvt_pk_bf16_f32 v25, v36, v37
	ds_write2_b64 v14, v[22:23], v[24:25] offset0:132 offset1:198
	s_waitcnt vmcnt(11)
	v_cvt_pk_bf16_f32 v22, v38, v39
	v_cvt_pk_bf16_f32 v23, v40, v41
	s_waitcnt vmcnt(10)
	v_cvt_pk_bf16_f32 v24, v42, v43
	v_cvt_pk_bf16_f32 v25, v44, v45
	ds_write2_b64 v18, v[22:23], v[24:25] offset0:8 offset1:74
	s_waitcnt vmcnt(9)
	v_cvt_pk_bf16_f32 v22, v46, v47
	v_cvt_pk_bf16_f32 v23, v48, v49
	s_waitcnt vmcnt(8)
	v_cvt_pk_bf16_f32 v24, v50, v51
	v_cvt_pk_bf16_f32 v25, v52, v53
	ds_write2_b64 v18, v[22:23], v[24:25] offset0:140 offset1:206
	s_waitcnt vmcnt(7)
	v_cvt_pk_bf16_f32 v22, v54, v55
	v_cvt_pk_bf16_f32 v23, v56, v57
	s_waitcnt vmcnt(6)
	v_cvt_pk_bf16_f32 v24, v58, v59
	v_cvt_pk_bf16_f32 v25, v60, v61
	ds_write2_b64 v19, v[22:23], v[24:25] offset0:16 offset1:82
	s_waitcnt vmcnt(5)
	v_cvt_pk_bf16_f32 v22, v62, v63
	v_cvt_pk_bf16_f32 v23, v64, v65
	s_waitcnt vmcnt(4)
	v_cvt_pk_bf16_f32 v24, v66, v67
	v_cvt_pk_bf16_f32 v25, v68, v69
	ds_write2_b64 v19, v[22:23], v[24:25] offset0:148 offset1:214
	s_waitcnt vmcnt(3)
	v_cvt_pk_bf16_f32 v22, v70, v71
	v_cvt_pk_bf16_f32 v23, v72, v73
	s_waitcnt vmcnt(2)
	v_cvt_pk_bf16_f32 v24, v74, v75
	v_cvt_pk_bf16_f32 v25, v76, v77
	ds_write2_b64 v20, v[22:23], v[24:25] offset0:24 offset1:90
	s_waitcnt vmcnt(1)
	v_cvt_pk_bf16_f32 v22, v78, v79
	v_cvt_pk_bf16_f32 v23, v80, v81
	s_waitcnt vmcnt(0)
	v_cvt_pk_bf16_f32 v24, v82, v83
	v_cvt_pk_bf16_f32 v25, v84, v85
	ds_write2_b64 v20, v[22:23], v[24:25] offset0:156 offset1:222
	s_waitcnt lgkmcnt(0)
	s_barrier
	ds_read_b64_tr_b16 v[22:23], v15
	ds_read_b64_tr_b16 v[24:25], v15 offset:1056
	ds_read_b64_tr_b16 v[26:27], v15 offset:8448
	ds_read_b64_tr_b16 v[28:29], v15 offset:9504
	ds_read_b64_tr_b16 v[30:31], v15 offset:16896
	ds_read_b64_tr_b16 v[32:33], v15 offset:17952
	ds_read_b64_tr_b16 v[34:35], v15 offset:25344
	ds_read_b64_tr_b16 v[36:37], v15 offset:26400
	ds_read_b64_tr_b16 v[38:39], v15 offset:33792
	ds_read_b64_tr_b16 v[40:41], v15 offset:34848
	ds_read_b64_tr_b16 v[42:43], v15 offset:42240
	ds_read_b64_tr_b16 v[44:45], v15 offset:43296
	ds_read_b64_tr_b16 v[46:47], v15 offset:50688
	ds_read_b64_tr_b16 v[48:49], v15 offset:51744
	ds_read_b64_tr_b16 v[50:51], v15 offset:59136
	ds_read_b64_tr_b16 v[52:53], v15 offset:60192
	s_waitcnt lgkmcnt(0)
	s_barrier
	ds_write_b128 v16, v[22:25]
	ds_write_b128 v16, v[26:29] offset:64
	ds_write_b128 v16, v[30:33] offset:128
	ds_write_b128 v16, v[34:37] offset:192
	ds_write_b128 v16, v[38:41] offset:256
	ds_write_b128 v16, v[42:45] offset:320
	ds_write_b128 v16, v[46:49] offset:384
	ds_write_b128 v16, v[50:53] offset:448
	s_waitcnt lgkmcnt(0)
	v_lshl_add_u64 v[30:31], s[40:41], 0, v[4:5]
	v_or_b32_e32 v5, s0, v6
	ds_read_b128 v[22:25], v17
	v_lshlrev_b32_e32 v5, 11, v5
	v_or_b32_e32 v26, 0x40000, v5
	v_mov_b32_e32 v27, v3
	v_lshl_add_u64 v[32:33], v[30:31], 0, v[26:27]
	ds_read_b128 v[26:29], v17 offset:1056
	s_waitcnt lgkmcnt(1)
	global_store_dwordx4 v[32:33], v[22:25], off sc0 sc1
	s_nop 1
	v_or_b32_e32 v22, 0x41000, v5
	v_mov_b32_e32 v23, v3
	v_lshl_add_u64 v[22:23], v[30:31], 0, v[22:23]
	s_waitcnt lgkmcnt(0)
	global_store_dwordx4 v[22:23], v[26:29], off sc0 sc1
	ds_read_b128 v[22:25], v17 offset:2112
	s_nop 0
	v_or_b32_e32 v26, 0x42000, v5
	v_mov_b32_e32 v27, v3
	v_lshl_add_u64 v[32:33], v[30:31], 0, v[26:27]
	ds_read_b128 v[26:29], v17 offset:3168
	s_waitcnt lgkmcnt(1)
	global_store_dwordx4 v[32:33], v[22:25], off sc0 sc1
	s_nop 1
	v_or_b32_e32 v22, 0x43000, v5
	v_mov_b32_e32 v23, v3
	v_lshl_add_u64 v[22:23], v[30:31], 0, v[22:23]
	s_waitcnt lgkmcnt(0)
	global_store_dwordx4 v[22:23], v[26:29], off sc0 sc1
	ds_read_b128 v[22:25], v17 offset:4224
	s_nop 0
	v_or_b32_e32 v26, 0x44000, v5
	v_mov_b32_e32 v27, v3
	v_lshl_add_u64 v[32:33], v[30:31], 0, v[26:27]
	ds_read_b128 v[26:29], v17 offset:5280
	s_waitcnt lgkmcnt(1)
	global_store_dwordx4 v[32:33], v[22:25], off sc0 sc1
	s_nop 1
	v_or_b32_e32 v22, 0x45000, v5
	v_mov_b32_e32 v23, v3
	v_lshl_add_u64 v[22:23], v[30:31], 0, v[22:23]
	s_waitcnt lgkmcnt(0)
	global_store_dwordx4 v[22:23], v[26:29], off sc0 sc1
	ds_read_b128 v[22:25], v17 offset:6336
	s_nop 0
	v_or_b32_e32 v26, 0x46000, v5
	v_mov_b32_e32 v27, v3
	v_lshl_add_u64 v[32:33], v[30:31], 0, v[26:27]
	ds_read_b128 v[26:29], v17 offset:7392
	s_waitcnt lgkmcnt(1)
	global_store_dwordx4 v[32:33], v[22:25], off sc0 sc1
	s_nop 1
	v_or_b32_e32 v22, 0x47000, v5
	v_mov_b32_e32 v23, v3
	v_lshl_add_u64 v[22:23], v[30:31], 0, v[22:23]
	s_waitcnt lgkmcnt(0)
	global_store_dwordx4 v[22:23], v[26:29], off sc0 sc1
	s_barrier

; #define LAS __attribute__((address_space(3)))
; template <bool BF> __device__ __forceinline__ unsigned pk16(float lo, float hi) { return BF ? pkb(lo, hi) : pkh(lo, hi); }
; template <bool BF, class RowMap>
; __device__ __forceinline__ void cvt_block(const float* W, int K, int N, f16* WT, const RowMap& rm, int item, int tid, LAS unsigned char* S) {
;     const int lane = tid & 63, wave = tid >> 6;
;     const int nblk = N / 128, kb = item / nblk, nb = item % nblk, k0 = 256 * kb, n0 = 128 * nb;
;     const float* src = W + (size_t)(k0 + 32 * wave + (lane >> 5)) * N + n0 + 4 * (lane & 31);
;     f32x4 v[16];
; #pragma unroll
;     for (int i = 0; i < 16; ++i) v[i] = *(const f32x4*)(src + (size_t)(2 * i) * N);
; #pragma unroll
;     for (int i = 0; i < 16; ++i) { u32x2 w; w.x = pk16<BF>(v[i][0], v[i][1]); w.y = pk16<BF>(v[i][2], v[i][3]);
;         *(LAS u32x2*)(S + (32 * wave + 2 * i + (lane >> 5)) * CVB_RS + 8 * (lane & 31)) = w; }
;     __syncthreads();
; __device__ __forceinline__ void cvt_moe(const float* w1, const float* w3, const float* w2, f16* W13, f16* W2T, int tid, LAS unsigned char* S) {
;     ...
;         if (r < I13) { cvt_block<MOE_BF16>(w1 + (size_t)e * DM * DE, DM, DE, W13 + (size_t)e * 2 * DE * DM, MapGLU{0}, r, tid, S); continue; } r -= I13;
.LBB0_1215:
	s_andn2_b64 vcc, exec, s[2:3]
	s_cbranch_vccnz .LBB0_1208
	s_mul_hi_i32 s2, s37, 0xb00000
	s_mul_i32 s37, s37, 0xb00000
	v_readlane_b32 s40, v251, 0
	v_readlane_b32 s41, v251, 1
	s_add_u32 s38, s40, s37
	s_addc_u32 s39, s41, s2
	s_add_u32 s0, s84, s37
	s_addc_u32 s37, s85, s2
	s_mul_i32 s2, s36, 0xba3
	s_lshr_b32 s3, s2, 31
	s_lshr_b32 s2, s2, 16
	s_add_i32 s2, s2, s3
	s_sext_i32_i16 s3, s2
	s_mul_i32 s2, s2, 22
	s_sub_i32 s2, s36, s2
	s_sext_i32_i16 s36, s2
	s_lshl_b32 s2, s3, 8
	v_or_b32_e32 v5, s2, v1
	v_mul_i32_i24_e32 v22, 0x2c00, v5
	s_lshl_b32 s40, s36, 7
	v_ashrrev_i32_e32 v23, 31, v22
	v_lshl_add_u64 v[22:23], s[38:39], 0, v[22:23]
	s_ashr_i32 s41, s40, 31
	v_lshl_add_u64 v[22:23], s[40:41], 2, v[22:23]
	v_lshl_add_u64 v[82:83], v[22:23], 0, v[2:3]
	v_add_co_u32_e32 v26, vcc, s21, v82
	s_ashr_i32 s3, s2, 31
	s_nop 0
	v_addc_co_u32_e32 v27, vcc, 0, v83, vcc
	v_add_co_u32_e32 v30, vcc, s22, v82
	global_load_dwordx4 v[22:25], v[82:83], off nt
	s_nop 0
	global_load_dwordx4 v[26:29], v[26:27], off offset:2048 nt
	v_addc_co_u32_e32 v31, vcc, 0, v83, vcc
	v_add_co_u32_e32 v34, vcc, s13, v82
	s_lshl_b64 s[2:3], s[2:3], 1
	s_nop 0
	v_addc_co_u32_e32 v35, vcc, 0, v83, vcc
	v_add_co_u32_e32 v38, vcc, s16, v82
	global_load_dwordx4 v[30:33], v[30:31], off nt
	s_nop 0
	global_load_dwordx4 v[34:37], v[34:35], off offset:2048 nt
	v_addc_co_u32_e32 v39, vcc, 0, v83, vcc
	v_add_co_u32_e32 v42, vcc, s23, v82
	s_add_u32 s2, s0, s2
	s_nop 0
	v_addc_co_u32_e32 v43, vcc, 0, v83, vcc
	v_add_co_u32_e32 v46, vcc, s24, v82
	global_load_dwordx4 v[38:41], v[38:39], off nt
	s_nop 0
	global_load_dwordx4 v[42:45], v[42:43], off offset:2048 nt
	v_addc_co_u32_e32 v47, vcc, 0, v83, vcc
	v_add_co_u32_e32 v50, vcc, s25, v82
	s_addc_u32 s3, s37, s3
	s_nop 0
	v_addc_co_u32_e32 v51, vcc, 0, v83, vcc
	v_add_co_u32_e32 v54, vcc, s26, v82
	global_load_dwordx4 v[46:49], v[46:47], off nt
	s_nop 0
	global_load_dwordx4 v[50:53], v[50:51], off offset:2048 nt
	v_addc_co_u32_e32 v55, vcc, 0, v83, vcc
	v_add_co_u32_e32 v58, vcc, s27, v82
	s_lshl_b32 s0, s36, 8
	s_nop 0
	v_addc_co_u32_e32 v59, vcc, 0, v83, vcc
	v_add_co_u32_e32 v62, vcc, s28, v82
	global_load_dwordx4 v[54:57], v[54:55], off nt
	s_nop 0
	global_load_dwordx4 v[58:61], v[58:59], off offset:2048 nt
	v_addc_co_u32_e32 v63, vcc, 0, v83, vcc
	v_add_co_u32_e32 v66, vcc, s29, v82
	v_mov_b32_e32 v5, v3
	s_nop 0
	v_addc_co_u32_e32 v67, vcc, 0, v83, vcc
	v_add_co_u32_e32 v70, vcc, s30, v82
	global_load_dwordx4 v[62:65], v[62:63], off nt
	s_nop 0
	global_load_dwordx4 v[66:69], v[66:67], off offset:2048 nt
	v_addc_co_u32_e32 v71, vcc, 0, v83, vcc
	v_add_co_u32_e32 v74, vcc, s31, v82
	v_readlane_b32 s42, v251, 2
	s_nop 0
	v_addc_co_u32_e32 v75, vcc, 0, v83, vcc
	v_add_co_u32_e32 v78, vcc, s33, v82
	global_load_dwordx4 v[70:73], v[70:71], off nt
	s_nop 0
	global_load_dwordx4 v[74:77], v[74:75], off offset:2048 nt
	v_addc_co_u32_e32 v79, vcc, 0, v83, vcc
	v_add_co_u32_e32 v82, vcc, s34, v82
	global_load_dwordx4 v[78:81], v[78:79], off nt
	s_nop 0
	v_addc_co_u32_e32 v83, vcc, 0, v83, vcc
	global_load_dwordx4 v[82:85], v[82:83], off offset:2048 nt
	v_readlane_b32 s43, v251, 3
	v_readlane_b32 s44, v251, 4
	v_readlane_b32 s45, v251, 5
	v_readlane_b32 s46, v251, 6
	v_readlane_b32 s47, v251, 7
	s_waitcnt vmcnt(15)
	v_cvt_pk_bf16_f32 v22, v22, v23
	v_cvt_pk_bf16_f32 v23, v24, v25
	s_waitcnt vmcnt(14)
	v_cvt_pk_bf16_f32 v24, v26, v27
	v_cvt_pk_bf16_f32 v25, v28, v29
	ds_write2_b64 v14, v[22:23], v[24:25] offset1:66
	s_waitcnt vmcnt(13)
	v_cvt_pk_bf16_f32 v22, v30, v31
	v_cvt_pk_bf16_f32 v23, v32, v33
	s_waitcnt vmcnt(12)
	v_cvt_pk_bf16_f32 v24, v34, v35
	v_cvt_pk_bf16_f32 v25, v36, v37
	ds_write2_b64 v14, v[22:23], v[24:25] offset0:132 offset1:198
	s_waitcnt vmcnt(11)
	v_cvt_pk_bf16_f32 v22, v38, v39
	v_cvt_pk_bf16_f32 v23, v40, v41
	s_waitcnt vmcnt(10)
	v_cvt_pk_bf16_f32 v24, v42, v43
	v_cvt_pk_bf16_f32 v25, v44, v45
	ds_write2_b64 v18, v[22:23], v[24:25] offset0:8 offset1:74
	s_waitcnt vmcnt(9)
	v_cvt_pk_bf16_f32 v22, v46, v47
	v_cvt_pk_bf16_f32 v23, v48, v49
	s_waitcnt vmcnt(8)
	v_cvt_pk_bf16_f32 v24, v50, v51
	v_cvt_pk_bf16_f32 v25, v52, v53
	ds_write2_b64 v18, v[22:23], v[24:25] offset0:140 offset1:206
	s_waitcnt vmcnt(7)
	v_cvt_pk_bf16_f32 v22, v54, v55
	v_cvt_pk_bf16_f32 v23, v56, v57
	s_waitcnt vmcnt(6)
	v_cvt_pk_bf16_f32 v24, v58, v59
	v_cvt_pk_bf16_f32 v25, v60, v61
	ds_write2_b64 v19, v[22:23], v[24:25] offset0:16 offset1:82
	s_waitcnt vmcnt(5)
	v_cvt_pk_bf16_f32 v22, v62, v63
	v_cvt_pk_bf16_f32 v23, v64, v65
	s_waitcnt vmcnt(4)
	v_cvt_pk_bf16_f32 v24, v66, v67
	v_cvt_pk_bf16_f32 v25, v68, v69
	ds_write2_b64 v19, v[22:23], v[24:25] offset0:148 offset1:214
	s_waitcnt vmcnt(3)
	v_cvt_pk_bf16_f32 v22, v70, v71
	v_cvt_pk_bf16_f32 v23, v72, v73
	s_waitcnt vmcnt(2)
	v_cvt_pk_bf16_f32 v24, v74, v75
	v_cvt_pk_bf16_f32 v25, v76, v77
	ds_write2_b64 v20, v[22:23], v[24:25] offset0:24 offset1:90
	s_waitcnt vmcnt(1)
	v_cvt_pk_bf16_f32 v22, v78, v79
	v_cvt_pk_bf16_f32 v23, v80, v81
	s_waitcnt vmcnt(0)
	v_cvt_pk_bf16_f32 v24, v82, v83
	v_cvt_pk_bf16_f32 v25, v84, v85
	ds_write2_b64 v20, v[22:23], v[24:25] offset0:156 offset1:222
	s_waitcnt lgkmcnt(0)
	s_barrier
; #define LAS __attribute__((address_space(3)))
; #define LDS_WAIT() asm volatile("s_waitcnt lgkmcnt(0)" ::: "memory")
; template <bool BF, class RowMap>
; __device__ __forceinline__ void cvt_block(const float* W, int K, int N, f16* WT, const RowMap& rm, int item, int tid, LAS unsigned char* S) {
;     ...
;     const int g = lane >> 4, i16 = lane & 15, q_ = i16 >> 2, p_ = i16 & 3;
;     LAS unsigned char* T = S;
;     u32x4 wv[8];
; #pragma unroll
;     for (int st = 0; st < 8; ++st) {
;         const int ch = 4 * st + g;
;         const LAS unsigned char* ap = S + (8 * ch + q_) * CVB_RS + (16 * wave + 4 * p_) * 2;
;         const s16x4 lo = __builtin_amdgcn_ds_read_tr16_b64_v4i16((LAS s16x4*)ap);
;         const s16x4 hi = __builtin_amdgcn_ds_read_tr16_b64_v4i16((LAS s16x4*)(ap + 4 * CVB_RS));
;         const u32x2 l2 = __builtin_bit_cast(u32x2, lo), h2 = __builtin_bit_cast(u32x2, hi); wv[st].x = l2.x; wv[st].y = l2.y; wv[st].z = h2.x; wv[st].w = h2.y;
;     }
;     __syncthreads();
; #pragma unroll
;     for (int st = 0; st < 8; ++st) *(LAS u32x4*)(T + (16 * wave + i16) * CVT_TS + 16 * (4 * st + g)) = wv[st];
;     LDS_WAIT();
; #pragma unroll
;     for (int j = 0; j < 8; ++j) { const int nr = 16 * wave + 2 * j + (lane >> 5), ch = lane & 31;
;         const u32x4 w = *(const LAS u32x4*)(T + nr * CVT_TS + 16 * ch);
;         *(u32x4*)(WT + (size_t)rm(n0 + nr) * K + k0 + 8 * ch) = w; }
;     __syncthreads();
	ds_read_b64_tr_b16 v[22:23], v15
	ds_read_b64_tr_b16 v[24:25], v15 offset:1056
	ds_read_b64_tr_b16 v[26:27], v15 offset:8448
	ds_read_b64_tr_b16 v[28:29], v15 offset:9504
	ds_read_b64_tr_b16 v[30:31], v15 offset:16896
	ds_read_b64_tr_b16 v[32:33], v15 offset:17952
	ds_read_b64_tr_b16 v[34:35], v15 offset:25344
	ds_read_b64_tr_b16 v[36:37], v15 offset:26400
	ds_read_b64_tr_b16 v[38:39], v15 offset:33792
	ds_read_b64_tr_b16 v[40:41], v15 offset:34848
	ds_read_b64_tr_b16 v[42:43], v15 offset:42240
	ds_read_b64_tr_b16 v[44:45], v15 offset:43296
	ds_read_b64_tr_b16 v[46:47], v15 offset:50688
	ds_read_b64_tr_b16 v[48:49], v15 offset:51744
	ds_read_b64_tr_b16 v[50:51], v15 offset:59136
	ds_read_b64_tr_b16 v[52:53], v15 offset:60192
	s_waitcnt lgkmcnt(0)
	s_barrier
	ds_write_b128 v16, v[22:25]
	ds_write_b128 v16, v[26:29] offset:64
	ds_write_b128 v16, v[30:33] offset:128
	ds_write_b128 v16, v[34:37] offset:192
	ds_write_b128 v16, v[38:41] offset:256
	ds_write_b128 v16, v[42:45] offset:320
	ds_write_b128 v16, v[46:49] offset:384
	ds_write_b128 v16, v[50:53] offset:448
	s_waitcnt lgkmcnt(0)
	ds_read_b128 v[22:25], v17
	v_or_b32_e32 v26, s0, v6
	v_ashrrev_i32_e32 v27, 31, v26
	v_lshl_add_u64 v[30:31], s[2:3], 0, v[4:5]
	v_lshlrev_b64 v[26:27], 11, v[26:27]
	v_lshl_add_u64 v[32:33], v[30:31], 0, v[26:27]
	ds_read_b128 v[26:29], v17 offset:1056
	s_waitcnt lgkmcnt(1)
	global_store_dwordx4 v[32:33], v[22:25], off sc0 sc1
	s_nop 1
	v_or_b32_e32 v22, s0, v7
	v_ashrrev_i32_e32 v23, 31, v22
	v_lshlrev_b64 v[22:23], 11, v[22:23]
	v_lshl_add_u64 v[22:23], v[30:31], 0, v[22:23]
	s_waitcnt lgkmcnt(0)
	global_store_dwordx4 v[22:23], v[26:29], off sc0 sc1
	ds_read_b128 v[22:25], v17 offset:2112
	s_nop 0
	v_or_b32_e32 v26, s0, v8
	v_ashrrev_i32_e32 v27, 31, v26
	v_lshlrev_b64 v[26:27], 11, v[26:27]
	v_lshl_add_u64 v[32:33], v[30:31], 0, v[26:27]
	ds_read_b128 v[26:29], v17 offset:3168
	s_waitcnt lgkmcnt(1)
	global_store_dwordx4 v[32:33], v[22:25], off sc0 sc1
	s_nop 1
	v_or_b32_e32 v22, s0, v9
	v_ashrrev_i32_e32 v23, 31, v22
	v_lshlrev_b64 v[22:23], 11, v[22:23]
	v_lshl_add_u64 v[22:23], v[30:31], 0, v[22:23]
	s_waitcnt lgkmcnt(0)
	global_store_dwordx4 v[22:23], v[26:29], off sc0 sc1
	ds_read_b128 v[22:25], v17 offset:4224
	s_nop 0
	v_or_b32_e32 v26, s0, v10
	v_ashrrev_i32_e32 v27, 31, v26
	v_lshlrev_b64 v[26:27], 11, v[26:27]
	v_lshl_add_u64 v[32:33], v[30:31], 0, v[26:27]
	ds_read_b128 v[26:29], v17 offset:5280
	s_waitcnt lgkmcnt(1)
	global_store_dwordx4 v[32:33], v[22:25], off sc0 sc1
	s_nop 1
	v_or_b32_e32 v22, s0, v11
	v_ashrrev_i32_e32 v23, 31, v22
	v_lshlrev_b64 v[22:23], 11, v[22:23]
	v_lshl_add_u64 v[22:23], v[30:31], 0, v[22:23]
	s_waitcnt lgkmcnt(0)
	global_store_dwordx4 v[22:23], v[26:29], off sc0 sc1
	ds_read_b128 v[22:25], v17 offset:6336
	s_nop 0
	v_or_b32_e32 v26, s0, v12
	v_ashrrev_i32_e32 v27, 31, v26
	v_lshlrev_b64 v[26:27], 11, v[26:27]
	v_lshl_add_u64 v[32:33], v[30:31], 0, v[26:27]
	ds_read_b128 v[26:29], v17 offset:7392
	s_waitcnt lgkmcnt(1)
	global_store_dwordx4 v[32:33], v[22:25], off sc0 sc1
	s_nop 1
	v_or_b32_e32 v22, s0, v13
	v_ashrrev_i32_e32 v23, 31, v22
	v_lshlrev_b64 v[22:23], 11, v[22:23]
	v_lshl_add_u64 v[22:23], v[30:31], 0, v[22:23]
	s_waitcnt lgkmcnt(0)
	global_store_dwordx4 v[22:23], v[26:29], off sc0 sc1
	s_barrier
	s_branch .LBB0_1208

; __device__ __forceinline__ void conv_phase(const f16* Z1, f16* Y, const float* scw, const float* cfw, const float* cfb, const float* lng, const float* lnb, LAS unsigned char* lds) {
;     ...
;             const f16x8 gb = *(const f16x8*)(zb + (size_t)t * gm::ZP1N + 1024 + c8);
;             { u32x4 w; w.x = pkh((float)gb[0] * cacc[0], (float)gb[1] * cacc[1]); w.y = pkh((float)gb[2] * cacc[2], (float)gb[3] * cacc[3]);
;               w.z = pkh((float)gb[4] * cacc[4], (float)gb[5] * cacc[5]); w.w = pkh((float)gb[6] * cacc[6], (float)gb[7] * cacc[7]); *(u32x4*)(yr + c8) = w; }
;         }
;         __syncthreads();
.LBB0_1349:
	s_mul_hi_i32 s1, s0, 0xc00
	s_add_u32 s0, s92, s86
	s_addc_u32 s1, s93, s1
	global_load_dwordx4 v[26:29], v4, s[0:1] offset:2048
	s_add_i32 s75, s75, s96
	s_add_i32 s85, s85, s68
	v_lshl_add_u64 v[30:31], s[2:3], 0, v[4:5]
	s_cmpk_lt_i32 s75, 0x400
	s_waitcnt vmcnt(0)
	v_cvt_f32_f16_e32 v16, v26
	v_cvt_f32_f16_sdwa v17, v26 dst_sel:DWORD dst_unused:UNUSED_PAD src0_sel:WORD_1
	v_cvt_f32_f16_e32 v26, v27
	v_cvt_f32_f16_sdwa v27, v27 dst_sel:DWORD dst_unused:UNUSED_PAD src0_sel:WORD_1
	v_cvt_f32_f16_e32 v32, v28
	v_cvt_f32_f16_sdwa v33, v28 dst_sel:DWORD dst_unused:UNUSED_PAD src0_sel:WORD_1
	v_cvt_f32_f16_e32 v28, v29
	v_cvt_f32_f16_sdwa v29, v29 dst_sel:DWORD dst_unused:UNUSED_PAD src0_sel:WORD_1
	v_pk_mul_f32 v[16:17], v[18:19], v[16:17]
	v_pk_mul_f32 v[18:19], v[20:21], v[26:27]
	v_pk_mul_f32 v[20:21], v[22:23], v[32:33]
	v_pk_mul_f32 v[22:23], v[24:25], v[28:29]
	v_cvt_pk_f16_f32 v16, v16, v17
	v_cvt_pk_f16_f32 v17, v18, v19
	v_cvt_pk_f16_f32 v18, v20, v21
	v_cvt_pk_f16_f32 v19, v22, v23
	global_store_dwordx4 v[30:31], v[16:19], off sc0 sc1
	s_barrier
	s_cbranch_scc0 .LBB0_1407

; __device__ __forceinline__ void conv_phase(const f16* Z1, f16* Y, const float* scw, const float* cfw, const float* cfb, const float* lng, const float* lnb, LAS unsigned char* lds) {
;     ...
;         for (int q = 0; q < 4; ++q) { const int tt = wave * 4 + q, t = t0 + tt, c8 = lane * 8;
;             const f32x4 x0 = *(const LAS f32x4*)(U + tt * 512 + c8), x1 = *(const LAS f32x4*)(U + tt * 512 + c8 + 4);
;             float x[8] = {x0[0], x0[1], x0[2], x0[3], x1[0], x1[1], x1[2], x1[3]};
;             float s = 0.f;
; #pragma unroll
;             for (int j = 0; j < 8; ++j) s += x[j];
;             const float mean = wave_sum(s) * (1.f / 512.f); float s2 = 0.f;
; #pragma unroll
;             for (int j = 0; j < 8; ++j) { x[j] -= mean; s2 += x[j] * x[j]; }
;             const float rstd = __builtin_amdgcn_rsqf(wave_sum(s2) * (1.f / 512.f) + EPS);
;             const f32x4 g0 = *(const f32x4*)(lng + c8), g1 = *(const f32x4*)(lng + c8 + 4), b0 = *(const f32x4*)(lnb + c8), b1 = *(const f32x4*)(lnb + c8 + 4);
;             const float gg[8] = {g0[0], g0[1], g0[2], g0[3], g1[0], g1[1], g1[2], g1[3]}, bb[8] = {b0[0], b0[1], b0[2], b0[3], b1[0], b1[1], b1[2], b1[3]};
;             float yd[8];
; #pragma unroll
;             for (int j = 0; j < 8; ++j) yd[j] = silu_f(x[j] * rstd * gg[j] + bb[j]);
;             f16* yr = Y + ((size_t)b * SEQ + t) * DM;
;             { u32x4 w; w.x = pkh(yd[0], yd[1]); w.y = pkh(yd[2], yd[3]); w.z = pkh(yd[4], yd[5]); w.w = pkh(yd[6], yd[7]); *(u32x4*)(yr + 512 + c8) = w; }
;             float cacc[8];
; #pragma unroll
;             for (int j = 0; j < 8; ++j) cacc[j] = 0.f;
; #pragma unroll
;             for (int k = 0; k < 3; ++k) { const int ts = t + k - 1;
;                 if (ts >= 0 && ts < SEQ) { const f16x8 in8 = *(const f16x8*)(zb + (size_t)ts * gm::ZP1N + c8);
;                     const f32x4 w0 = *(const f32x4*)(scw + k * 512 + c8), w1 = *(const f32x4*)(scw + k * 512 + c8 + 4);
;                     const float ww[8] = {w0[0], w0[1], w0[2], w0[3], w1[0], w1[1], w1[2], w1[3]};
; #pragma unroll
;                     for (int j = 0; j < 8; ++j) cacc[j] += ww[j] * (float)in8[j]; } }
;             const f16x8 gb = *(const f16x8*)(zb + (size_t)t * gm::ZP1N + 1024 + c8);
;             { u32x4 w; w.x = pkh((float)gb[0] * cacc[0], (float)gb[1] * cacc[1]); w.y = pkh((float)gb[2] * cacc[2], (float)gb[3] * cacc[3]);
.LBB0_1389:
	s_mul_hi_i32 s1, s0, 0xc00
	s_add_u32 s0, s92, s86
	s_addc_u32 s1, s93, s1
	global_load_dwordx4 v[26:29], v4, s[0:1] offset:2048
	v_lshl_add_u64 v[30:31], s[2:3], 0, v[4:5]
	v_add_u32_e32 v38, s76, v77
	v_mov_b32_e32 v42, v5
	v_mov_b32_e32 v43, v5
	s_add_i32 s0, s80, s71
	s_ashr_i32 s1, s0, 31
	s_lshl_b64 s[2:3], s[0:1], 11
	v_mov_b32_e32 v141, v5
	v_mov_b32_e32 v146, v5
	s_add_u32 s2, s40, s2
	s_addc_u32 s3, s41, s3
	s_cmpk_gt_u32 s0, 0x800
	s_mul_i32 s86, s0, 0xc00
	s_waitcnt vmcnt(0)
	v_cvt_f32_f16_e32 v32, v26
	v_cvt_f32_f16_sdwa v33, v26 dst_sel:DWORD dst_unused:UNUSED_PAD src0_sel:WORD_1
	v_cvt_f32_f16_e32 v26, v27
	v_cvt_f32_f16_sdwa v27, v27 dst_sel:DWORD dst_unused:UNUSED_PAD src0_sel:WORD_1
	v_cvt_f32_f16_e32 v34, v28
	v_cvt_f32_f16_sdwa v35, v28 dst_sel:DWORD dst_unused:UNUSED_PAD src0_sel:WORD_1
	v_cvt_f32_f16_e32 v28, v29
	v_cvt_f32_f16_sdwa v29, v29 dst_sel:DWORD dst_unused:UNUSED_PAD src0_sel:WORD_1
	v_pk_mul_f32 v[20:21], v[20:21], v[32:33]
	v_pk_mul_f32 v[22:23], v[22:23], v[26:27]
	v_pk_mul_f32 v[24:25], v[24:25], v[34:35]
	v_pk_mul_f32 v[26:27], v[18:19], v[28:29]
	v_cvt_pk_f16_f32 v18, v20, v21
	v_cvt_pk_f16_f32 v19, v22, v23
	v_cvt_pk_f16_f32 v20, v24, v25
	v_cvt_pk_f16_f32 v21, v26, v27
	global_store_dwordx4 v[30:31], v[18:21], off sc0 sc1
	global_load_dwordx4 v[18:21], v[10:11], off
	s_nop 0
	global_load_dwordx4 v[22:25], v[8:9], off
	global_load_dwordx4 v[26:29], v[8:9], off offset:16
	global_load_dwordx4 v[30:33], v[10:11], off offset:16
	ds_read_b128 v[34:37], v38
	ds_read_b128 v[38:41], v38 offset:16
	s_waitcnt lgkmcnt(1)
	v_add_f32_e32 v44, 0, v34
	v_add_f32_e32 v44, v35, v44
	v_add_f32_e32 v44, v36, v44
	v_add_f32_e32 v44, v37, v44
	s_waitcnt lgkmcnt(0)
	v_add_f32_e32 v44, v38, v44
	v_add_f32_e32 v44, v39, v44
	v_add_f32_e32 v44, v40, v44
	v_add_f32_e32 v44, v41, v44
	s_nop 1
	v_add_f32_dpp v44, v44, v44 quad_perm:[1,0,3,2] row_mask:0xf bank_mask:0xf bound_ctrl:1
	s_nop 1
	v_add_f32_dpp v44, v44, v44 quad_perm:[2,3,0,1] row_mask:0xf bank_mask:0xf bound_ctrl:1
	s_nop 1
	v_add_f32_dpp v44, v44, v44 row_half_mirror row_mask:0xf bank_mask:0xf bound_ctrl:1
	s_nop 1
	v_add_f32_dpp v44, v44, v44 row_mirror row_mask:0xf bank_mask:0xf bound_ctrl:1
	s_nop 1
	v_mov_b32_dpp v42, v44 row_bcast:15 row_mask:0xa bank_mask:0xf
	v_add_f32_e32 v42, v44, v42
	s_nop 1
	v_mov_b32_dpp v43, v42 row_bcast:31 row_mask:0xc bank_mask:0xf
	v_add_f32_e32 v42, v42, v43
	s_nop 0
	v_readlane_b32 s1, v42, 63
	s_nop 1
	v_mul_f32_e32 v42, s1, v140
	v_pk_add_f32 v[34:35], v[34:35], v[42:43] op_sel_hi:[1,0] neg_lo:[0,1] neg_hi:[0,1]
	v_pk_add_f32 v[36:37], v[36:37], v[42:43] op_sel_hi:[1,0] neg_lo:[0,1] neg_hi:[0,1]
	v_pk_mul_f32 v[144:145], v[34:35], v[34:35]
	v_pk_mul_f32 v[142:143], v[36:37], v[36:37]
	v_add_f32_e32 v144, v144, v145
	v_pk_add_f32 v[38:39], v[38:39], v[42:43] op_sel_hi:[1,0] neg_lo:[0,1] neg_hi:[0,1]
	v_add_f32_e32 v142, v142, v144
	v_pk_mul_f32 v[44:45], v[38:39], v[38:39]
	v_add_f32_e32 v142, v143, v142
	v_pk_add_f32 v[40:41], v[40:41], v[42:43] op_sel_hi:[1,0] neg_lo:[0,1] neg_hi:[0,1]
	v_add_f32_e32 v44, v44, v142
	v_pk_mul_f32 v[42:43], v[40:41], v[40:41]
	v_add_f32_e32 v44, v45, v44
	v_add_f32_e32 v42, v42, v44
	v_add_f32_e32 v42, v43, v42
	s_nop 1
	v_add_f32_dpp v42, v42, v42 quad_perm:[1,0,3,2] row_mask:0xf bank_mask:0xf bound_ctrl:1
	s_nop 1
	v_add_f32_dpp v42, v42, v42 quad_perm:[2,3,0,1] row_mask:0xf bank_mask:0xf bound_ctrl:1
	s_nop 1
	v_add_f32_dpp v42, v42, v42 row_half_mirror row_mask:0xf bank_mask:0xf bound_ctrl:1
	s_nop 1
	v_add_f32_dpp v42, v42, v42 row_mirror row_mask:0xf bank_mask:0xf bound_ctrl:1
	s_nop 1
	v_mov_b32_dpp v141, v42 row_bcast:15 row_mask:0xa bank_mask:0xf
	v_add_f32_e32 v42, v42, v141
	s_nop 1
	v_mov_b32_dpp v146, v42 row_bcast:31 row_mask:0xc bank_mask:0xf
	v_add_f32_e32 v42, v42, v146
	s_nop 0
	v_readlane_b32 s1, v42, 63
	s_nop 1
	v_fma_f32 v42, s1, v140, v139
	v_rsq_f32_e32 v42, v42
	s_nop 0
	v_pk_mul_f32 v[34:35], v[34:35], v[42:43] op_sel_hi:[1,0]
	v_pk_mul_f32 v[36:37], v[36:37], v[42:43] op_sel_hi:[1,0]
	v_pk_mul_f32 v[38:39], v[38:39], v[42:43] op_sel_hi:[1,0]
	v_pk_mul_f32 v[40:41], v[40:41], v[42:43] op_sel_hi:[1,0]
	s_waitcnt vmcnt(2)
	v_pk_fma_f32 v[18:19], v[22:23], v[34:35], v[18:19]
	v_pk_fma_f32 v[20:21], v[24:25], v[36:37], v[20:21]
	s_waitcnt vmcnt(0)
	v_pk_fma_f32 v[22:23], v[26:27], v[38:39], v[30:31]
	v_pk_fma_f32 v[24:25], v[28:29], v[40:41], v[32:33]
	v_mul_f32_e32 v26, 0xbfb8aa3b, v18
	v_mul_f32_e32 v27, 0xbfb8aa3b, v19
	v_mul_f32_e32 v28, 0xbfb8aa3b, v20
	v_mul_f32_e32 v29, 0xbfb8aa3b, v21
	v_mul_f32_e32 v30, 0xbfb8aa3b, v22
	v_mul_f32_e32 v31, 0xbfb8aa3b, v23
	v_mul_f32_e32 v32, 0xbfb8aa3b, v24
	v_mul_f32_e32 v33, 0xbfb8aa3b, v25
	v_exp_f32_e32 v26, v26
	v_exp_f32_e32 v27, v27
	v_exp_f32_e32 v28, v28
	v_exp_f32_e32 v29, v29
	v_exp_f32_e32 v30, v30
	v_exp_f32_e32 v31, v31
	v_exp_f32_e32 v32, v32
	v_exp_f32_e32 v33, v33
	v_add_f32_e32 v26, 1.0, v26
	v_add_f32_e32 v27, 1.0, v27
	v_add_f32_e32 v28, 1.0, v28
	v_add_f32_e32 v29, 1.0, v29
	v_add_f32_e32 v30, 1.0, v30
	v_add_f32_e32 v31, 1.0, v31
	v_add_f32_e32 v32, 1.0, v32
	v_add_f32_e32 v33, 1.0, v33
	v_rcp_f32_e32 v26, v26
	v_rcp_f32_e32 v27, v27
	v_rcp_f32_e32 v28, v28
	v_rcp_f32_e32 v29, v29
	v_rcp_f32_e32 v30, v30
	v_rcp_f32_e32 v31, v31
	v_rcp_f32_e32 v32, v32
	v_rcp_f32_e32 v33, v33
	v_pk_mul_f32 v[18:19], v[18:19], v[26:27]
	v_pk_mul_f32 v[20:21], v[20:21], v[28:29]
	v_pk_mul_f32 v[22:23], v[22:23], v[30:31]
	v_pk_mul_f32 v[24:25], v[24:25], v[32:33]
	v_cvt_pk_f16_f32 v18, v18, v19
	v_cvt_pk_f16_f32 v19, v20, v21
	v_cvt_pk_f16_f32 v20, v22, v23
	v_cvt_pk_f16_f32 v21, v24, v25
	global_store_dwordx4 v4, v[18:21], s[2:3] offset:1024
	s_cbranch_scc1 .LBB0_1391
	s_nop 0
	v_lshl_add_u64 v[18:19], v[16:17], 0, s[86:87]
	global_load_dwordx4 v[18:21], v[18:19], off offset:-3072
	s_nop 0
	global_load_dwordx4 v[22:25], v[12:13], off offset:16
	global_load_dwordx4 v[26:29], v[12:13], off
	s_waitcnt vmcnt(2)
	v_cvt_f32_f16_e32 v30, v18
	v_cvt_f32_f16_e32 v32, v19
	v_cvt_f32_f16_e32 v34, v20
	v_cvt_f32_f16_e32 v36, v21
	v_cvt_f32_f16_sdwa v37, v21 dst_sel:DWORD dst_unused:UNUSED_PAD src0_sel:WORD_1
	v_cvt_f32_f16_sdwa v35, v20 dst_sel:DWORD dst_unused:UNUSED_PAD src0_sel:WORD_1
	v_cvt_f32_f16_sdwa v33, v19 dst_sel:DWORD dst_unused:UNUSED_PAD src0_sel:WORD_1
	v_cvt_f32_f16_sdwa v31, v18 dst_sel:DWORD dst_unused:UNUSED_PAD src0_sel:WORD_1
	s_waitcnt vmcnt(1)
	v_pk_fma_f32 v[18:19], v[24:25], v[36:37], 0 op_sel_hi:[1,1,0]
	v_pk_fma_f32 v[24:25], v[22:23], v[34:35], 0 op_sel_hi:[1,1,0]
	s_waitcnt vmcnt(0)
	v_pk_fma_f32 v[22:23], v[28:29], v[32:33], 0 op_sel_hi:[1,1,0]
	v_pk_fma_f32 v[20:21], v[26:27], v[30:31], 0 op_sel_hi:[1,1,0]
	s_cmpk_gt_u32 s0, 0x7ff
	s_cbranch_scc0 .LBB0_1392
	s_branch .LBB0_1393

; __device__ __forceinline__ void conv_phase(const f16* Z1, f16* Y, const float* scw, const float* cfw, const float* cfb, const float* lng, const float* lnb, LAS unsigned char* lds) {
;     ...
;         for (int q = 0; q < 4; ++q) { const int tt = wave * 4 + q, t = t0 + tt, c8 = lane * 8;
;             const f32x4 x0 = *(const LAS f32x4*)(U + tt * 512 + c8), x1 = *(const LAS f32x4*)(U + tt * 512 + c8 + 4);
;             float x[8] = {x0[0], x0[1], x0[2], x0[3], x1[0], x1[1], x1[2], x1[3]};
;             float s = 0.f;
; #pragma unroll
;             for (int j = 0; j < 8; ++j) s += x[j];
;             const float mean = wave_sum(s) * (1.f / 512.f); float s2 = 0.f;
; #pragma unroll
;             for (int j = 0; j < 8; ++j) { x[j] -= mean; s2 += x[j] * x[j]; }
;             const float rstd = __builtin_amdgcn_rsqf(wave_sum(s2) * (1.f / 512.f) + EPS);
;             const f32x4 g0 = *(const f32x4*)(lng + c8), g1 = *(const f32x4*)(lng + c8 + 4), b0 = *(const f32x4*)(lnb + c8), b1 = *(const f32x4*)(lnb + c8 + 4);
;             const float gg[8] = {g0[0], g0[1], g0[2], g0[3], g1[0], g1[1], g1[2], g1[3]}, bb[8] = {b0[0], b0[1], b0[2], b0[3], b1[0], b1[1], b1[2], b1[3]};
;             float yd[8];
; #pragma unroll
;             for (int j = 0; j < 8; ++j) yd[j] = silu_f(x[j] * rstd * gg[j] + bb[j]);
;             f16* yr = Y + ((size_t)b * SEQ + t) * DM;
;             { u32x4 w; w.x = pkh(yd[0], yd[1]); w.y = pkh(yd[2], yd[3]); w.z = pkh(yd[4], yd[5]); w.w = pkh(yd[6], yd[7]); *(u32x4*)(yr + 512 + c8) = w; }
;             float cacc[8];
; #pragma unroll
;             for (int j = 0; j < 8; ++j) cacc[j] = 0.f;
; #pragma unroll
;             for (int k = 0; k < 3; ++k) { const int ts = t + k - 1;
;                 if (ts >= 0 && ts < SEQ) { const f16x8 in8 = *(const f16x8*)(zb + (size_t)ts * gm::ZP1N + c8);
;                     const f32x4 w0 = *(const f32x4*)(scw + k * 512 + c8), w1 = *(const f32x4*)(scw + k * 512 + c8 + 4);
;                     const float ww[8] = {w0[0], w0[1], w0[2], w0[3], w1[0], w1[1], w1[2], w1[3]};
; #pragma unroll
;                     for (int j = 0; j < 8; ++j) cacc[j] += ww[j] * (float)in8[j]; } }
;             const f16x8 gb = *(const f16x8*)(zb + (size_t)t * gm::ZP1N + 1024 + c8);
;             { u32x4 w; w.x = pkh((float)gb[0] * cacc[0], (float)gb[1] * cacc[1]); w.y = pkh((float)gb[2] * cacc[2], (float)gb[3] * cacc[3]);
.LBB0_1395:
	s_mul_hi_i32 s1, s0, 0xc00
	s_add_u32 s0, s92, s86
	s_addc_u32 s1, s93, s1
	global_load_dwordx4 v[26:29], v4, s[0:1] offset:2048
	v_lshl_add_u64 v[30:31], s[2:3], 0, v[4:5]
	v_add_u32_e32 v38, s88, v77
	v_mov_b32_e32 v42, v5
	v_mov_b32_e32 v43, v5
	s_add_i32 s0, s80, s77
	s_ashr_i32 s1, s0, 31
	s_lshl_b64 s[2:3], s[0:1], 11
	v_mov_b32_e32 v141, v5
	v_mov_b32_e32 v146, v5
	s_add_u32 s2, s40, s2
	s_addc_u32 s3, s41, s3
	s_cmpk_gt_u32 s0, 0x800
	s_mul_i32 s86, s0, 0xc00
	s_waitcnt vmcnt(0)
	v_cvt_f32_f16_e32 v32, v26
	v_cvt_f32_f16_sdwa v33, v26 dst_sel:DWORD dst_unused:UNUSED_PAD src0_sel:WORD_1
	v_cvt_f32_f16_e32 v26, v27
	v_cvt_f32_f16_sdwa v27, v27 dst_sel:DWORD dst_unused:UNUSED_PAD src0_sel:WORD_1
	v_cvt_f32_f16_e32 v34, v28
	v_cvt_f32_f16_sdwa v35, v28 dst_sel:DWORD dst_unused:UNUSED_PAD src0_sel:WORD_1
	v_cvt_f32_f16_e32 v28, v29
	v_cvt_f32_f16_sdwa v29, v29 dst_sel:DWORD dst_unused:UNUSED_PAD src0_sel:WORD_1
	v_pk_mul_f32 v[20:21], v[20:21], v[32:33]
	v_pk_mul_f32 v[22:23], v[22:23], v[26:27]
	v_pk_mul_f32 v[24:25], v[24:25], v[34:35]
	v_pk_mul_f32 v[26:27], v[18:19], v[28:29]
	v_cvt_pk_f16_f32 v18, v20, v21
	v_cvt_pk_f16_f32 v19, v22, v23
	v_cvt_pk_f16_f32 v20, v24, v25
	v_cvt_pk_f16_f32 v21, v26, v27
	global_store_dwordx4 v[30:31], v[18:21], off sc0 sc1
	global_load_dwordx4 v[18:21], v[10:11], off
	s_nop 0
	global_load_dwordx4 v[22:25], v[8:9], off
	global_load_dwordx4 v[26:29], v[8:9], off offset:16
	global_load_dwordx4 v[30:33], v[10:11], off offset:16
	ds_read_b128 v[34:37], v38
	ds_read_b128 v[38:41], v38 offset:16
	s_waitcnt lgkmcnt(1)
	v_add_f32_e32 v44, 0, v34
	v_add_f32_e32 v44, v35, v44
	v_add_f32_e32 v44, v36, v44
	v_add_f32_e32 v44, v37, v44
	s_waitcnt lgkmcnt(0)
	v_add_f32_e32 v44, v38, v44
	v_add_f32_e32 v44, v39, v44
	v_add_f32_e32 v44, v40, v44
	v_add_f32_e32 v44, v41, v44
	s_nop 1
	v_add_f32_dpp v44, v44, v44 quad_perm:[1,0,3,2] row_mask:0xf bank_mask:0xf bound_ctrl:1
	s_nop 1
	v_add_f32_dpp v44, v44, v44 quad_perm:[2,3,0,1] row_mask:0xf bank_mask:0xf bound_ctrl:1
	s_nop 1
	v_add_f32_dpp v44, v44, v44 row_half_mirror row_mask:0xf bank_mask:0xf bound_ctrl:1
	s_nop 1
	v_add_f32_dpp v44, v44, v44 row_mirror row_mask:0xf bank_mask:0xf bound_ctrl:1
	s_nop 1
	v_mov_b32_dpp v42, v44 row_bcast:15 row_mask:0xa bank_mask:0xf
	v_add_f32_e32 v42, v44, v42
	s_nop 1
	v_mov_b32_dpp v43, v42 row_bcast:31 row_mask:0xc bank_mask:0xf
	v_add_f32_e32 v42, v42, v43
	s_nop 0
	v_readlane_b32 s1, v42, 63
	s_nop 1
	v_mul_f32_e32 v42, s1, v140
	v_pk_add_f32 v[34:35], v[34:35], v[42:43] op_sel_hi:[1,0] neg_lo:[0,1] neg_hi:[0,1]
	v_pk_add_f32 v[36:37], v[36:37], v[42:43] op_sel_hi:[1,0] neg_lo:[0,1] neg_hi:[0,1]
	v_pk_mul_f32 v[144:145], v[34:35], v[34:35]
	v_pk_mul_f32 v[142:143], v[36:37], v[36:37]
	v_add_f32_e32 v144, v144, v145
	v_pk_add_f32 v[38:39], v[38:39], v[42:43] op_sel_hi:[1,0] neg_lo:[0,1] neg_hi:[0,1]
	v_add_f32_e32 v142, v142, v144
	v_pk_mul_f32 v[44:45], v[38:39], v[38:39]
	v_add_f32_e32 v142, v143, v142
	v_pk_add_f32 v[40:41], v[40:41], v[42:43] op_sel_hi:[1,0] neg_lo:[0,1] neg_hi:[0,1]
	v_add_f32_e32 v44, v44, v142
	v_pk_mul_f32 v[42:43], v[40:41], v[40:41]
	v_add_f32_e32 v44, v45, v44
	v_add_f32_e32 v42, v42, v44
	v_add_f32_e32 v42, v43, v42
	s_nop 1
	v_add_f32_dpp v42, v42, v42 quad_perm:[1,0,3,2] row_mask:0xf bank_mask:0xf bound_ctrl:1
	s_nop 1
	v_add_f32_dpp v42, v42, v42 quad_perm:[2,3,0,1] row_mask:0xf bank_mask:0xf bound_ctrl:1
	s_nop 1
	v_add_f32_dpp v42, v42, v42 row_half_mirror row_mask:0xf bank_mask:0xf bound_ctrl:1
	s_nop 1
	v_add_f32_dpp v42, v42, v42 row_mirror row_mask:0xf bank_mask:0xf bound_ctrl:1
	s_nop 1
	v_mov_b32_dpp v141, v42 row_bcast:15 row_mask:0xa bank_mask:0xf
	v_add_f32_e32 v42, v42, v141
	s_nop 1
	v_mov_b32_dpp v146, v42 row_bcast:31 row_mask:0xc bank_mask:0xf
	v_add_f32_e32 v42, v42, v146
	s_nop 0
	v_readlane_b32 s1, v42, 63
	s_nop 1
	v_fma_f32 v42, s1, v140, v139
	v_rsq_f32_e32 v42, v42
	s_nop 0
	v_pk_mul_f32 v[34:35], v[34:35], v[42:43] op_sel_hi:[1,0]
	v_pk_mul_f32 v[36:37], v[36:37], v[42:43] op_sel_hi:[1,0]
	v_pk_mul_f32 v[38:39], v[38:39], v[42:43] op_sel_hi:[1,0]
	v_pk_mul_f32 v[40:41], v[40:41], v[42:43] op_sel_hi:[1,0]
	s_waitcnt vmcnt(2)
	v_pk_fma_f32 v[18:19], v[22:23], v[34:35], v[18:19]
	v_pk_fma_f32 v[20:21], v[24:25], v[36:37], v[20:21]
	s_waitcnt vmcnt(0)
	v_pk_fma_f32 v[22:23], v[26:27], v[38:39], v[30:31]
	v_pk_fma_f32 v[24:25], v[28:29], v[40:41], v[32:33]
	v_mul_f32_e32 v26, 0xbfb8aa3b, v18
	v_mul_f32_e32 v27, 0xbfb8aa3b, v19
	v_mul_f32_e32 v28, 0xbfb8aa3b, v20
	v_mul_f32_e32 v29, 0xbfb8aa3b, v21
	v_mul_f32_e32 v30, 0xbfb8aa3b, v22
	v_mul_f32_e32 v31, 0xbfb8aa3b, v23
	v_mul_f32_e32 v32, 0xbfb8aa3b, v24
	v_mul_f32_e32 v33, 0xbfb8aa3b, v25
	v_exp_f32_e32 v26, v26
	v_exp_f32_e32 v27, v27
	v_exp_f32_e32 v28, v28
	v_exp_f32_e32 v29, v29
	v_exp_f32_e32 v30, v30
	v_exp_f32_e32 v31, v31
	v_exp_f32_e32 v32, v32
	v_exp_f32_e32 v33, v33
	v_add_f32_e32 v26, 1.0, v26
	v_add_f32_e32 v27, 1.0, v27
	v_add_f32_e32 v28, 1.0, v28
	v_add_f32_e32 v29, 1.0, v29
	v_add_f32_e32 v30, 1.0, v30
	v_add_f32_e32 v31, 1.0, v31
	v_add_f32_e32 v32, 1.0, v32
	v_add_f32_e32 v33, 1.0, v33
	v_rcp_f32_e32 v26, v26
	v_rcp_f32_e32 v27, v27
	v_rcp_f32_e32 v28, v28
	v_rcp_f32_e32 v29, v29
	v_rcp_f32_e32 v30, v30
	v_rcp_f32_e32 v31, v31
	v_rcp_f32_e32 v32, v32
	v_rcp_f32_e32 v33, v33
	v_pk_mul_f32 v[18:19], v[18:19], v[26:27]
	v_pk_mul_f32 v[20:21], v[20:21], v[28:29]
	v_pk_mul_f32 v[22:23], v[22:23], v[30:31]
	v_pk_mul_f32 v[24:25], v[24:25], v[32:33]
	v_cvt_pk_f16_f32 v18, v18, v19
	v_cvt_pk_f16_f32 v19, v20, v21
	v_cvt_pk_f16_f32 v20, v22, v23
	v_cvt_pk_f16_f32 v21, v24, v25
	global_store_dwordx4 v4, v[18:21], s[2:3] offset:1024
	s_cbranch_scc1 .LBB0_1397
	s_nop 0
	v_lshl_add_u64 v[18:19], v[16:17], 0, s[86:87]
	global_load_dwordx4 v[18:21], v[18:19], off offset:-3072
	s_nop 0
	global_load_dwordx4 v[22:25], v[12:13], off offset:16
	global_load_dwordx4 v[26:29], v[12:13], off
	s_waitcnt vmcnt(2)
	v_cvt_f32_f16_e32 v30, v18
	v_cvt_f32_f16_e32 v32, v19
	v_cvt_f32_f16_e32 v34, v20
	v_cvt_f32_f16_e32 v36, v21
	v_cvt_f32_f16_sdwa v37, v21 dst_sel:DWORD dst_unused:UNUSED_PAD src0_sel:WORD_1
	v_cvt_f32_f16_sdwa v35, v20 dst_sel:DWORD dst_unused:UNUSED_PAD src0_sel:WORD_1
	v_cvt_f32_f16_sdwa v33, v19 dst_sel:DWORD dst_unused:UNUSED_PAD src0_sel:WORD_1
	v_cvt_f32_f16_sdwa v31, v18 dst_sel:DWORD dst_unused:UNUSED_PAD src0_sel:WORD_1
	s_waitcnt vmcnt(1)
	v_pk_fma_f32 v[18:19], v[24:25], v[36:37], 0 op_sel_hi:[1,1,0]
	v_pk_fma_f32 v[24:25], v[22:23], v[34:35], 0 op_sel_hi:[1,1,0]
	s_waitcnt vmcnt(0)
	v_pk_fma_f32 v[22:23], v[28:29], v[32:33], 0 op_sel_hi:[1,1,0]
	v_pk_fma_f32 v[20:21], v[26:27], v[30:31], 0 op_sel_hi:[1,1,0]
	s_cmpk_lt_u32 s0, 0x800
	s_cselect_b64 s[38:39], -1, 0
	s_cmpk_gt_u32 s0, 0x7ff
	s_cbranch_scc0 .LBB0_1398
	s_branch .LBB0_1399

; __device__ __forceinline__ void conv_phase(const f16* Z1, f16* Y, const float* scw, const float* cfw, const float* cfb, const float* lng, const float* lnb, LAS unsigned char* lds) {
;     ...
;         for (int q = 0; q < 4; ++q) { const int tt = wave * 4 + q, t = t0 + tt, c8 = lane * 8;
;             const f32x4 x0 = *(const LAS f32x4*)(U + tt * 512 + c8), x1 = *(const LAS f32x4*)(U + tt * 512 + c8 + 4);
;             float x[8] = {x0[0], x0[1], x0[2], x0[3], x1[0], x1[1], x1[2], x1[3]};
;             float s = 0.f;
; #pragma unroll
;             for (int j = 0; j < 8; ++j) s += x[j];
;             const float mean = wave_sum(s) * (1.f / 512.f); float s2 = 0.f;
; #pragma unroll
;             for (int j = 0; j < 8; ++j) { x[j] -= mean; s2 += x[j] * x[j]; }
;             const float rstd = __builtin_amdgcn_rsqf(wave_sum(s2) * (1.f / 512.f) + EPS);
;             const f32x4 g0 = *(const f32x4*)(lng + c8), g1 = *(const f32x4*)(lng + c8 + 4), b0 = *(const f32x4*)(lnb + c8), b1 = *(const f32x4*)(lnb + c8 + 4);
;             const float gg[8] = {g0[0], g0[1], g0[2], g0[3], g1[0], g1[1], g1[2], g1[3]}, bb[8] = {b0[0], b0[1], b0[2], b0[3], b1[0], b1[1], b1[2], b1[3]};
;             float yd[8];
; #pragma unroll
;             for (int j = 0; j < 8; ++j) yd[j] = silu_f(x[j] * rstd * gg[j] + bb[j]);
;             f16* yr = Y + ((size_t)b * SEQ + t) * DM;
;             { u32x4 w; w.x = pkh(yd[0], yd[1]); w.y = pkh(yd[2], yd[3]); w.z = pkh(yd[4], yd[5]); w.w = pkh(yd[6], yd[7]); *(u32x4*)(yr + 512 + c8) = w; }
;             float cacc[8];
; #pragma unroll
;             for (int j = 0; j < 8; ++j) cacc[j] = 0.f;
; #pragma unroll
;             for (int k = 0; k < 3; ++k) { const int ts = t + k - 1;
;                 if (ts >= 0 && ts < SEQ) { const f16x8 in8 = *(const f16x8*)(zb + (size_t)ts * gm::ZP1N + c8);
;                     const f32x4 w0 = *(const f32x4*)(scw + k * 512 + c8), w1 = *(const f32x4*)(scw + k * 512 + c8 + 4);
;                     const float ww[8] = {w0[0], w0[1], w0[2], w0[3], w1[0], w1[1], w1[2], w1[3]};
; #pragma unroll
;                     for (int j = 0; j < 8; ++j) cacc[j] += ww[j] * (float)in8[j]; } }
;             const f16x8 gb = *(const f16x8*)(zb + (size_t)t * gm::ZP1N + 1024 + c8);
;             { u32x4 w; w.x = pkh((float)gb[0] * cacc[0], (float)gb[1] * cacc[1]); w.y = pkh((float)gb[2] * cacc[2], (float)gb[3] * cacc[3]);
.LBB0_1401:
	s_mul_hi_i32 s1, s0, 0xc00
	s_add_u32 s0, s92, s86
	s_addc_u32 s1, s93, s1
	global_load_dwordx4 v[26:29], v4, s[0:1] offset:2048
	v_lshl_add_u64 v[30:31], s[2:3], 0, v[4:5]
	v_add_u32_e32 v38, s84, v77
	v_mov_b32_e32 v42, v5
	v_mov_b32_e32 v43, v5
	s_add_i32 s0, s80, s89
	s_ashr_i32 s1, s0, 31
	s_lshl_b64 s[2:3], s[0:1], 11
	v_mov_b32_e32 v141, v5
	v_mov_b32_e32 v146, v5
	s_add_u32 s2, s40, s2
	s_addc_u32 s3, s41, s3
	s_cmpk_gt_u32 s0, 0x800
	s_mul_i32 s86, s0, 0xc00
	s_waitcnt vmcnt(0)
	v_cvt_f32_f16_e32 v32, v26
	v_cvt_f32_f16_sdwa v33, v26 dst_sel:DWORD dst_unused:UNUSED_PAD src0_sel:WORD_1
	v_cvt_f32_f16_e32 v26, v27
	v_cvt_f32_f16_sdwa v27, v27 dst_sel:DWORD dst_unused:UNUSED_PAD src0_sel:WORD_1
	v_cvt_f32_f16_e32 v34, v28
	v_cvt_f32_f16_sdwa v35, v28 dst_sel:DWORD dst_unused:UNUSED_PAD src0_sel:WORD_1
	v_cvt_f32_f16_e32 v28, v29
	v_cvt_f32_f16_sdwa v29, v29 dst_sel:DWORD dst_unused:UNUSED_PAD src0_sel:WORD_1
	v_pk_mul_f32 v[20:21], v[20:21], v[32:33]
	v_pk_mul_f32 v[22:23], v[22:23], v[26:27]
	v_pk_mul_f32 v[24:25], v[24:25], v[34:35]
	v_pk_mul_f32 v[26:27], v[18:19], v[28:29]
	v_cvt_pk_f16_f32 v18, v20, v21
	v_cvt_pk_f16_f32 v19, v22, v23
	v_cvt_pk_f16_f32 v20, v24, v25
	v_cvt_pk_f16_f32 v21, v26, v27
	global_store_dwordx4 v[30:31], v[18:21], off sc0 sc1
	global_load_dwordx4 v[18:21], v[10:11], off
	s_nop 0
	global_load_dwordx4 v[22:25], v[8:9], off
	global_load_dwordx4 v[26:29], v[8:9], off offset:16
	global_load_dwordx4 v[30:33], v[10:11], off offset:16
	ds_read_b128 v[34:37], v38
	ds_read_b128 v[38:41], v38 offset:16
	s_waitcnt lgkmcnt(1)
	v_add_f32_e32 v44, 0, v34
	v_add_f32_e32 v44, v35, v44
	v_add_f32_e32 v44, v36, v44
	v_add_f32_e32 v44, v37, v44
	s_waitcnt lgkmcnt(0)
	v_add_f32_e32 v44, v38, v44
	v_add_f32_e32 v44, v39, v44
	v_add_f32_e32 v44, v40, v44
	v_add_f32_e32 v44, v41, v44
	s_nop 1
	v_add_f32_dpp v44, v44, v44 quad_perm:[1,0,3,2] row_mask:0xf bank_mask:0xf bound_ctrl:1
	s_nop 1
	v_add_f32_dpp v44, v44, v44 quad_perm:[2,3,0,1] row_mask:0xf bank_mask:0xf bound_ctrl:1
	s_nop 1
	v_add_f32_dpp v44, v44, v44 row_half_mirror row_mask:0xf bank_mask:0xf bound_ctrl:1
	s_nop 1
	v_add_f32_dpp v44, v44, v44 row_mirror row_mask:0xf bank_mask:0xf bound_ctrl:1
	s_nop 1
	v_mov_b32_dpp v42, v44 row_bcast:15 row_mask:0xa bank_mask:0xf
	v_add_f32_e32 v42, v44, v42
	s_nop 1
	v_mov_b32_dpp v43, v42 row_bcast:31 row_mask:0xc bank_mask:0xf
	v_add_f32_e32 v42, v42, v43
	s_nop 0
	v_readlane_b32 s1, v42, 63
	s_nop 1
	v_mul_f32_e32 v42, s1, v140
	v_pk_add_f32 v[34:35], v[34:35], v[42:43] op_sel_hi:[1,0] neg_lo:[0,1] neg_hi:[0,1]
	v_pk_add_f32 v[36:37], v[36:37], v[42:43] op_sel_hi:[1,0] neg_lo:[0,1] neg_hi:[0,1]
	v_pk_mul_f32 v[144:145], v[34:35], v[34:35]
	v_pk_mul_f32 v[142:143], v[36:37], v[36:37]
	v_add_f32_e32 v144, v144, v145
	v_pk_add_f32 v[38:39], v[38:39], v[42:43] op_sel_hi:[1,0] neg_lo:[0,1] neg_hi:[0,1]
	v_add_f32_e32 v142, v142, v144
	v_pk_mul_f32 v[44:45], v[38:39], v[38:39]
	v_add_f32_e32 v142, v143, v142
	v_pk_add_f32 v[40:41], v[40:41], v[42:43] op_sel_hi:[1,0] neg_lo:[0,1] neg_hi:[0,1]
	v_add_f32_e32 v44, v44, v142
	v_pk_mul_f32 v[42:43], v[40:41], v[40:41]
	v_add_f32_e32 v44, v45, v44
	v_add_f32_e32 v42, v42, v44
	v_add_f32_e32 v42, v43, v42
	s_nop 1
	v_add_f32_dpp v42, v42, v42 quad_perm:[1,0,3,2] row_mask:0xf bank_mask:0xf bound_ctrl:1
	s_nop 1
	v_add_f32_dpp v42, v42, v42 quad_perm:[2,3,0,1] row_mask:0xf bank_mask:0xf bound_ctrl:1
	s_nop 1
	v_add_f32_dpp v42, v42, v42 row_half_mirror row_mask:0xf bank_mask:0xf bound_ctrl:1
	s_nop 1
	v_add_f32_dpp v42, v42, v42 row_mirror row_mask:0xf bank_mask:0xf bound_ctrl:1
	s_nop 1
	v_mov_b32_dpp v141, v42 row_bcast:15 row_mask:0xa bank_mask:0xf
	v_add_f32_e32 v42, v42, v141
	s_nop 1
	v_mov_b32_dpp v146, v42 row_bcast:31 row_mask:0xc bank_mask:0xf
	v_add_f32_e32 v42, v42, v146
	s_nop 0
	v_readlane_b32 s1, v42, 63
	s_nop 1
	v_fma_f32 v42, s1, v140, v139
	v_rsq_f32_e32 v42, v42
	s_nop 0
	v_pk_mul_f32 v[34:35], v[34:35], v[42:43] op_sel_hi:[1,0]
	v_pk_mul_f32 v[36:37], v[36:37], v[42:43] op_sel_hi:[1,0]
	v_pk_mul_f32 v[38:39], v[38:39], v[42:43] op_sel_hi:[1,0]
	v_pk_mul_f32 v[40:41], v[40:41], v[42:43] op_sel_hi:[1,0]
	s_waitcnt vmcnt(2)
	v_pk_fma_f32 v[18:19], v[22:23], v[34:35], v[18:19]
	v_pk_fma_f32 v[20:21], v[24:25], v[36:37], v[20:21]
	s_waitcnt vmcnt(0)
	v_pk_fma_f32 v[22:23], v[26:27], v[38:39], v[30:31]
	v_pk_fma_f32 v[24:25], v[28:29], v[40:41], v[32:33]
	v_mul_f32_e32 v26, 0xbfb8aa3b, v18
	v_mul_f32_e32 v27, 0xbfb8aa3b, v19
	v_mul_f32_e32 v28, 0xbfb8aa3b, v20
	v_mul_f32_e32 v29, 0xbfb8aa3b, v21
	v_mul_f32_e32 v30, 0xbfb8aa3b, v22
	v_mul_f32_e32 v31, 0xbfb8aa3b, v23
	v_mul_f32_e32 v32, 0xbfb8aa3b, v24
	v_mul_f32_e32 v33, 0xbfb8aa3b, v25
	v_exp_f32_e32 v26, v26
	v_exp_f32_e32 v27, v27
	v_exp_f32_e32 v28, v28
	v_exp_f32_e32 v29, v29
	v_exp_f32_e32 v30, v30
	v_exp_f32_e32 v31, v31
	v_exp_f32_e32 v32, v32
	v_exp_f32_e32 v33, v33
	v_add_f32_e32 v26, 1.0, v26
	v_add_f32_e32 v27, 1.0, v27
	v_add_f32_e32 v28, 1.0, v28
	v_add_f32_e32 v29, 1.0, v29
	v_add_f32_e32 v30, 1.0, v30
	v_add_f32_e32 v31, 1.0, v31
	v_add_f32_e32 v32, 1.0, v32
	v_add_f32_e32 v33, 1.0, v33
	v_rcp_f32_e32 v26, v26
	v_rcp_f32_e32 v27, v27
	v_rcp_f32_e32 v28, v28
	v_rcp_f32_e32 v29, v29
	v_rcp_f32_e32 v30, v30
	v_rcp_f32_e32 v31, v31
	v_rcp_f32_e32 v32, v32
	v_rcp_f32_e32 v33, v33
	v_pk_mul_f32 v[18:19], v[18:19], v[26:27]
	v_pk_mul_f32 v[20:21], v[20:21], v[28:29]
	v_pk_mul_f32 v[22:23], v[22:23], v[30:31]
	v_pk_mul_f32 v[24:25], v[24:25], v[32:33]
	v_cvt_pk_f16_f32 v18, v18, v19
	v_cvt_pk_f16_f32 v19, v20, v21
	v_cvt_pk_f16_f32 v20, v22, v23
	v_cvt_pk_f16_f32 v21, v24, v25
	global_store_dwordx4 v4, v[18:21], s[2:3] offset:1024
	s_cbranch_scc1 .LBB0_1403
	s_nop 0
	v_lshl_add_u64 v[18:19], v[16:17], 0, s[86:87]
	global_load_dwordx4 v[18:21], v[18:19], off offset:-3072
	s_nop 0
	global_load_dwordx4 v[22:25], v[12:13], off offset:16
	global_load_dwordx4 v[26:29], v[12:13], off
	s_waitcnt vmcnt(2)
	v_cvt_f32_f16_e32 v30, v18
	v_cvt_f32_f16_e32 v32, v19
	v_cvt_f32_f16_e32 v34, v20
	v_cvt_f32_f16_e32 v36, v21
	v_cvt_f32_f16_sdwa v37, v21 dst_sel:DWORD dst_unused:UNUSED_PAD src0_sel:WORD_1
	v_cvt_f32_f16_sdwa v35, v20 dst_sel:DWORD dst_unused:UNUSED_PAD src0_sel:WORD_1
	v_cvt_f32_f16_sdwa v33, v19 dst_sel:DWORD dst_unused:UNUSED_PAD src0_sel:WORD_1
	v_cvt_f32_f16_sdwa v31, v18 dst_sel:DWORD dst_unused:UNUSED_PAD src0_sel:WORD_1
	s_waitcnt vmcnt(1)
	v_pk_fma_f32 v[24:25], v[24:25], v[36:37], 0 op_sel_hi:[1,1,0]
	v_pk_fma_f32 v[22:23], v[22:23], v[34:35], 0 op_sel_hi:[1,1,0]
	s_waitcnt vmcnt(0)
	v_pk_fma_f32 v[20:21], v[28:29], v[32:33], 0 op_sel_hi:[1,1,0]
	v_pk_fma_f32 v[18:19], v[26:27], v[30:31], 0 op_sel_hi:[1,1,0]
	s_cmpk_gt_u32 s0, 0x7ff
	s_cbranch_scc0 .LBB0_1404
	s_branch .LBB0_1405

;     __device__ __forceinline__ void operator()() { if (cnt == turn) run_all(tid_); ++cnt; }
;     __device__ __forceinline__ void operator()(const Acc& acc, const Unit& u, int wr, int wc, int fr, int fq) const {
;         const int col0 = u.pn * BM + wc * 32 + 8 * fq; const int b = (u.pm * BM) / SEQ;
;         f32x4 gv[2][2];
; #pragma unroll
;         for (int bj = 0; bj < 2; ++bj)
; #pragma unroll
;             for (int n = 0; n < 2; ++n) gv[bj][n] = *(const f32x4*)(gate + (size_t)b * gstride + col0 + bj * HALF + 4 * n);
; #pragma unroll
;         for (int ai = 0; ai < 2; ++ai)
; #pragma unroll
;             for (int m = 0; m < 4; ++m) { const size_t off = (size_t)(u.pm * BM + ai * HALF + wr * 64 + m * 16 + fr) * DM + col0;
; #pragma unroll
;                 for (int bj = 0; bj < 2; ++bj) { f32x4 b0, b1;
;                     if constexpr (BASE16) { const f16x8 bv = *(const f16x8*)((const f16*)base + off + bj * HALF);
;                         b0 = (f32x4){(float)bv[0], (float)bv[1], (float)bv[2], (float)bv[3]}; b1 = (f32x4){(float)bv[4], (float)bv[5], (float)bv[6], (float)bv[7]}; }
;                     else { b0 = *(const f32x4*)((const float*)base + off + bj * HALF); b1 = *(const f32x4*)((const float*)base + off + bj * HALF + 4); }
;                     const f32x4 v0 = b0 + gv[bj][0] * acc[ai][bj][m][0], v1 = b1 + gv[bj][1] * acc[ai][bj][m][1];
;                     u32x4 w; w.x = pkh(v0[0], v0[1]); w.y = pkh(v0[2], v0[3]); w.z = pkh(v1[0], v1[1]); w.w = pkh(v1[2], v1[3]);
;                     *(u32x4*)(out + off + bj * HALF) = w; }
.LBB0_1483:
	v_lshl_add_u32 v164, s2, 8, v1
	v_lshl_or_b32 v162, s3, 8, v167
	v_ashrrev_i32_e32 v165, 31, v164
	s_ashr_i32 s3, s2, 31
	v_ashrrev_i32_e32 v163, 31, v162
	v_lshlrev_b64 v[122:123], 10, v[164:165]
	s_lshr_b32 s3, s3, 29
	v_lshl_add_u64 v[122:123], v[122:123], 0, v[162:163]
	v_lshlrev_b64 v[130:131], 1, v[122:123]
	s_add_i32 s2, s2, s3
	v_lshl_add_u64 v[176:177], s[66:67], 0, v[130:131]
	s_ashr_i32 s2, s2, 3
	global_load_dwordx4 v[172:175], v[176:177], off
	s_mul_hi_i32 s3, s2, 0x6000
	s_mulk_i32 s2, 0x6000
	s_add_u32 s2, s38, s2
	s_addc_u32 s3, s39, s3
	v_lshl_add_u64 v[134:135], v[162:163], 2, s[2:3]
	global_load_dwordx4 v[126:129], v[134:135], off
	global_load_dwordx4 v[122:125], v[134:135], off offset:16
	v_lshl_add_u64 v[178:179], s[8:9], 0, v[130:131]
	global_load_dwordx4 v[130:133], v[134:135], off offset:528
	s_nop 0
	global_load_dwordx4 v[134:137], v[134:135], off offset:512
	s_andn2_b64 vcc, exec, s[4:5]
	s_mov_b64 s[2:3], -1
	s_waitcnt vmcnt(0)
	v_cvt_f32_f16_e32 v180, v172
	v_cvt_f32_f16_sdwa v181, v172 dst_sel:DWORD dst_unused:UNUSED_PAD src0_sel:WORD_1
	v_cvt_f32_f16_e32 v172, v173
	v_cvt_f32_f16_sdwa v173, v173 dst_sel:DWORD dst_unused:UNUSED_PAD src0_sel:WORD_1
	v_cvt_f32_f16_e32 v182, v174
	v_cvt_f32_f16_e32 v184, v175
	v_cvt_f32_f16_sdwa v185, v175 dst_sel:DWORD dst_unused:UNUSED_PAD src0_sel:WORD_1
	v_cvt_f32_f16_sdwa v183, v174 dst_sel:DWORD dst_unused:UNUSED_PAD src0_sel:WORD_1
	v_pk_fma_f32 v[144:145], v[144:145], v[128:129], v[172:173]
	v_pk_fma_f32 v[142:143], v[142:143], v[126:127], v[180:181]
	v_pk_fma_f32 v[172:173], v[140:141], v[124:125], v[184:185]
	v_pk_fma_f32 v[140:141], v[138:139], v[122:123], v[182:183]
	v_cvt_pk_f16_f32 v138, v142, v143
	v_cvt_pk_f16_f32 v139, v144, v145
	v_cvt_pk_f16_f32 v140, v140, v141
	v_cvt_pk_f16_f32 v141, v172, v173
	global_store_dwordx4 v[178:179], v[138:141], off sc0 sc1
	global_load_dwordx4 v[138:141], v[176:177], off offset:256
	v_or_b32_e32 v142, 16, v164
	v_ashrrev_i32_e32 v143, 31, v142
	v_lshlrev_b64 v[142:143], 10, v[142:143]
	v_lshl_add_u64 v[142:143], v[142:143], 0, v[162:163]
	v_lshlrev_b64 v[142:143], 1, v[142:143]
	v_lshl_add_u64 v[144:145], s[66:67], 0, v[142:143]
	s_waitcnt vmcnt(0)
	v_cvt_f32_f16_e32 v172, v138
	v_cvt_f32_f16_sdwa v173, v138 dst_sel:DWORD dst_unused:UNUSED_PAD src0_sel:WORD_1
	v_cvt_f32_f16_e32 v138, v139
	v_cvt_f32_f16_sdwa v139, v139 dst_sel:DWORD dst_unused:UNUSED_PAD src0_sel:WORD_1
	v_cvt_f32_f16_e32 v174, v140
	v_cvt_f32_f16_e32 v176, v141
	v_cvt_f32_f16_sdwa v177, v141 dst_sel:DWORD dst_unused:UNUSED_PAD src0_sel:WORD_1
	v_cvt_f32_f16_sdwa v175, v140 dst_sel:DWORD dst_unused:UNUSED_PAD src0_sel:WORD_1
	v_pk_fma_f32 v[120:121], v[120:121], v[136:137], v[138:139]
	v_pk_fma_f32 v[118:119], v[118:119], v[134:135], v[172:173]
	v_pk_fma_f32 v[138:139], v[116:117], v[132:133], v[176:177]
	v_pk_fma_f32 v[116:117], v[114:115], v[130:131], v[174:175]
	v_cvt_pk_f16_f32 v114, v118, v119
	v_cvt_pk_f16_f32 v115, v120, v121
	v_cvt_pk_f16_f32 v116, v116, v117
	v_cvt_pk_f16_f32 v117, v138, v139
	global_store_dwordx4 v[178:179], v[114:117], off offset:256 sc0 sc1
	global_load_dwordx4 v[114:117], v[144:145], off
	v_lshl_add_u64 v[118:119], s[8:9], 0, v[142:143]
	s_waitcnt vmcnt(0)
	v_cvt_f32_f16_e32 v120, v114
	v_cvt_f32_f16_sdwa v121, v114 dst_sel:DWORD dst_unused:UNUSED_PAD src0_sel:WORD_1
	v_cvt_f32_f16_e32 v114, v115
	v_cvt_f32_f16_sdwa v115, v115 dst_sel:DWORD dst_unused:UNUSED_PAD src0_sel:WORD_1
	v_cvt_f32_f16_e32 v138, v116
	v_cvt_f32_f16_e32 v140, v117
	v_cvt_f32_f16_sdwa v141, v117 dst_sel:DWORD dst_unused:UNUSED_PAD src0_sel:WORD_1
	v_cvt_f32_f16_sdwa v139, v116 dst_sel:DWORD dst_unused:UNUSED_PAD src0_sel:WORD_1
	v_pk_fma_f32 v[112:113], v[112:113], v[128:129], v[114:115]
	v_pk_fma_f32 v[110:111], v[110:111], v[126:127], v[120:121]
	v_pk_fma_f32 v[114:115], v[108:109], v[124:125], v[140:141]
	v_pk_fma_f32 v[108:109], v[106:107], v[122:123], v[138:139]
	v_cvt_pk_f16_f32 v106, v110, v111
	v_cvt_pk_f16_f32 v107, v112, v113
	v_cvt_pk_f16_f32 v108, v108, v109
	v_cvt_pk_f16_f32 v109, v114, v115
	global_store_dwordx4 v[118:119], v[106:109], off sc0 sc1
	global_load_dwordx4 v[106:109], v[144:145], off offset:256
	v_or_b32_e32 v110, 32, v164
	v_ashrrev_i32_e32 v111, 31, v110
	v_lshlrev_b64 v[110:111], 10, v[110:111]
	v_lshl_add_u64 v[110:111], v[110:111], 0, v[162:163]
	v_lshlrev_b64 v[110:111], 1, v[110:111]
	v_lshl_add_u64 v[112:113], s[66:67], 0, v[110:111]
	s_waitcnt vmcnt(0)
	v_cvt_f32_f16_e32 v114, v106
	v_cvt_f32_f16_sdwa v115, v106 dst_sel:DWORD dst_unused:UNUSED_PAD src0_sel:WORD_1
	v_cvt_f32_f16_e32 v106, v107
	v_cvt_f32_f16_sdwa v107, v107 dst_sel:DWORD dst_unused:UNUSED_PAD src0_sel:WORD_1
	v_cvt_f32_f16_e32 v116, v108
	v_cvt_f32_f16_e32 v120, v109
	v_cvt_f32_f16_sdwa v121, v109 dst_sel:DWORD dst_unused:UNUSED_PAD src0_sel:WORD_1
	v_cvt_f32_f16_sdwa v117, v108 dst_sel:DWORD dst_unused:UNUSED_PAD src0_sel:WORD_1
	v_pk_fma_f32 v[104:105], v[104:105], v[136:137], v[106:107]
	v_pk_fma_f32 v[102:103], v[102:103], v[134:135], v[114:115]
	v_pk_fma_f32 v[106:107], v[100:101], v[132:133], v[120:121]
	v_pk_fma_f32 v[100:101], v[98:99], v[130:131], v[116:117]
	v_cvt_pk_f16_f32 v98, v102, v103
	v_cvt_pk_f16_f32 v99, v104, v105
	v_cvt_pk_f16_f32 v100, v100, v101
	v_cvt_pk_f16_f32 v101, v106, v107
	global_store_dwordx4 v[118:119], v[98:101], off offset:256 sc0 sc1
	global_load_dwordx4 v[98:101], v[112:113], off
	v_lshl_add_u64 v[102:103], s[8:9], 0, v[110:111]
	s_waitcnt vmcnt(0)
;     __device__ __forceinline__ void operator()(const Acc& acc, const Unit& u, int wr, int wc, int fr, int fq) const {
;     ...
;         for (int ai = 0; ai < 2; ++ai)
; #pragma unroll
;             for (int m = 0; m < 4; ++m) { const size_t off = (size_t)(u.pm * BM + ai * HALF + wr * 64 + m * 16 + fr) * DM + col0;
; #pragma unroll
;                 for (int bj = 0; bj < 2; ++bj) { f32x4 b0, b1;
;                     if constexpr (BASE16) { const f16x8 bv = *(const f16x8*)((const f16*)base + off + bj * HALF);
;                         b0 = (f32x4){(float)bv[0], (float)bv[1], (float)bv[2], (float)bv[3]}; b1 = (f32x4){(float)bv[4], (float)bv[5], (float)bv[6], (float)bv[7]}; }
;                     else { b0 = *(const f32x4*)((const float*)base + off + bj * HALF); b1 = *(const f32x4*)((const float*)base + off + bj * HALF + 4); }
;                     const f32x4 v0 = b0 + gv[bj][0] * acc[ai][bj][m][0], v1 = b1 + gv[bj][1] * acc[ai][bj][m][1];
;                     u32x4 w; w.x = pkh(v0[0], v0[1]); w.y = pkh(v0[2], v0[3]); w.z = pkh(v1[0], v1[1]); w.w = pkh(v1[2], v1[3]);
;                     *(u32x4*)(out + off + bj * HALF) = w; }
	v_cvt_f32_f16_e32 v104, v98
	v_cvt_f32_f16_sdwa v105, v98 dst_sel:DWORD dst_unused:UNUSED_PAD src0_sel:WORD_1
	v_cvt_f32_f16_e32 v98, v99
	v_cvt_f32_f16_sdwa v99, v99 dst_sel:DWORD dst_unused:UNUSED_PAD src0_sel:WORD_1
	v_cvt_f32_f16_e32 v106, v100
	v_cvt_f32_f16_e32 v108, v101
	v_cvt_f32_f16_sdwa v109, v101 dst_sel:DWORD dst_unused:UNUSED_PAD src0_sel:WORD_1
	v_cvt_f32_f16_sdwa v107, v100 dst_sel:DWORD dst_unused:UNUSED_PAD src0_sel:WORD_1
	v_pk_fma_f32 v[96:97], v[96:97], v[128:129], v[98:99]
	v_pk_fma_f32 v[94:95], v[94:95], v[126:127], v[104:105]
	v_pk_fma_f32 v[98:99], v[92:93], v[124:125], v[108:109]
	v_pk_fma_f32 v[92:93], v[90:91], v[122:123], v[106:107]
	v_cvt_pk_f16_f32 v90, v94, v95
	v_cvt_pk_f16_f32 v91, v96, v97
	v_cvt_pk_f16_f32 v92, v92, v93
	v_cvt_pk_f16_f32 v93, v98, v99
	global_store_dwordx4 v[102:103], v[90:93], off sc0 sc1
	global_load_dwordx4 v[90:93], v[112:113], off offset:256
	v_or_b32_e32 v94, 48, v164
	v_ashrrev_i32_e32 v95, 31, v94
	v_lshlrev_b64 v[94:95], 10, v[94:95]
	v_lshl_add_u64 v[94:95], v[94:95], 0, v[162:163]
	v_lshlrev_b64 v[94:95], 1, v[94:95]
	v_lshl_add_u64 v[96:97], s[66:67], 0, v[94:95]
	s_waitcnt vmcnt(0)
	v_cvt_f32_f16_e32 v98, v90
	v_cvt_f32_f16_sdwa v99, v90 dst_sel:DWORD dst_unused:UNUSED_PAD src0_sel:WORD_1
	v_cvt_f32_f16_e32 v90, v91
	v_cvt_f32_f16_sdwa v91, v91 dst_sel:DWORD dst_unused:UNUSED_PAD src0_sel:WORD_1
	v_cvt_f32_f16_e32 v100, v92
	v_cvt_f32_f16_e32 v104, v93
	v_cvt_f32_f16_sdwa v105, v93 dst_sel:DWORD dst_unused:UNUSED_PAD src0_sel:WORD_1
	v_cvt_f32_f16_sdwa v101, v92 dst_sel:DWORD dst_unused:UNUSED_PAD src0_sel:WORD_1
	v_pk_fma_f32 v[88:89], v[88:89], v[136:137], v[90:91]
	v_pk_fma_f32 v[86:87], v[86:87], v[134:135], v[98:99]
	v_pk_fma_f32 v[90:91], v[84:85], v[132:133], v[104:105]
	v_pk_fma_f32 v[84:85], v[82:83], v[130:131], v[100:101]
	v_cvt_pk_f16_f32 v82, v86, v87
	v_cvt_pk_f16_f32 v83, v88, v89
	v_cvt_pk_f16_f32 v84, v84, v85
	v_cvt_pk_f16_f32 v85, v90, v91
	global_store_dwordx4 v[102:103], v[82:85], off offset:256 sc0 sc1
	global_load_dwordx4 v[82:85], v[96:97], off
	v_lshl_add_u64 v[86:87], s[8:9], 0, v[94:95]
	s_waitcnt vmcnt(0)
	v_cvt_f32_f16_e32 v88, v82
	v_cvt_f32_f16_sdwa v89, v82 dst_sel:DWORD dst_unused:UNUSED_PAD src0_sel:WORD_1
	v_cvt_f32_f16_e32 v82, v83
	v_cvt_f32_f16_sdwa v83, v83 dst_sel:DWORD dst_unused:UNUSED_PAD src0_sel:WORD_1
	v_cvt_f32_f16_e32 v90, v84
	v_cvt_f32_f16_e32 v92, v85
	v_cvt_f32_f16_sdwa v93, v85 dst_sel:DWORD dst_unused:UNUSED_PAD src0_sel:WORD_1
	v_cvt_f32_f16_sdwa v91, v84 dst_sel:DWORD dst_unused:UNUSED_PAD src0_sel:WORD_1
	v_pk_fma_f32 v[80:81], v[80:81], v[128:129], v[82:83]
	v_pk_fma_f32 v[78:79], v[78:79], v[126:127], v[88:89]
	v_pk_fma_f32 v[82:83], v[76:77], v[124:125], v[92:93]
	v_pk_fma_f32 v[76:77], v[74:75], v[122:123], v[90:91]
	v_cvt_pk_f16_f32 v74, v78, v79
	v_cvt_pk_f16_f32 v75, v80, v81
	v_cvt_pk_f16_f32 v76, v76, v77
	v_cvt_pk_f16_f32 v77, v82, v83
	global_store_dwordx4 v[86:87], v[74:77], off sc0 sc1
	global_load_dwordx4 v[74:77], v[96:97], off offset:256
	v_add_u32_e32 v78, 0x80, v164
	v_ashrrev_i32_e32 v79, 31, v78
	v_lshlrev_b64 v[78:79], 10, v[78:79]
	v_lshl_add_u64 v[78:79], v[78:79], 0, v[162:163]
	v_lshlrev_b64 v[78:79], 1, v[78:79]
	v_lshl_add_u64 v[80:81], s[66:67], 0, v[78:79]
	s_waitcnt vmcnt(0)
	v_cvt_f32_f16_e32 v82, v74
	v_cvt_f32_f16_sdwa v83, v74 dst_sel:DWORD dst_unused:UNUSED_PAD src0_sel:WORD_1
	v_cvt_f32_f16_e32 v74, v75
	v_cvt_f32_f16_sdwa v75, v75 dst_sel:DWORD dst_unused:UNUSED_PAD src0_sel:WORD_1
	v_cvt_f32_f16_e32 v84, v76
	v_cvt_f32_f16_e32 v88, v77
	v_cvt_f32_f16_sdwa v89, v77 dst_sel:DWORD dst_unused:UNUSED_PAD src0_sel:WORD_1
	v_cvt_f32_f16_sdwa v85, v76 dst_sel:DWORD dst_unused:UNUSED_PAD src0_sel:WORD_1
	v_pk_fma_f32 v[72:73], v[72:73], v[136:137], v[74:75]
	v_pk_fma_f32 v[70:71], v[70:71], v[134:135], v[82:83]
	v_pk_fma_f32 v[74:75], v[68:69], v[132:133], v[88:89]
	v_pk_fma_f32 v[68:69], v[66:67], v[130:131], v[84:85]
	v_cvt_pk_f16_f32 v66, v70, v71
	v_cvt_pk_f16_f32 v67, v72, v73
	v_cvt_pk_f16_f32 v68, v68, v69
	v_cvt_pk_f16_f32 v69, v74, v75
	global_store_dwordx4 v[86:87], v[66:69], off offset:256 sc0 sc1
	global_load_dwordx4 v[66:69], v[80:81], off
	v_lshl_add_u64 v[70:71], s[8:9], 0, v[78:79]
	s_waitcnt vmcnt(0)
	v_cvt_f32_f16_e32 v72, v66
	v_cvt_f32_f16_sdwa v73, v66 dst_sel:DWORD dst_unused:UNUSED_PAD src0_sel:WORD_1
	v_cvt_f32_f16_e32 v66, v67
	v_cvt_f32_f16_sdwa v67, v67 dst_sel:DWORD dst_unused:UNUSED_PAD src0_sel:WORD_1
	v_cvt_f32_f16_e32 v74, v68
	v_cvt_f32_f16_e32 v76, v69
	v_cvt_f32_f16_sdwa v77, v69 dst_sel:DWORD dst_unused:UNUSED_PAD src0_sel:WORD_1
	v_cvt_f32_f16_sdwa v75, v68 dst_sel:DWORD dst_unused:UNUSED_PAD src0_sel:WORD_1
	v_pk_fma_f32 v[64:65], v[64:65], v[128:129], v[66:67]
	v_pk_fma_f32 v[62:63], v[62:63], v[126:127], v[72:73]
	v_pk_fma_f32 v[66:67], v[60:61], v[124:125], v[76:77]
	v_pk_fma_f32 v[60:61], v[58:59], v[122:123], v[74:75]
	v_cvt_pk_f16_f32 v58, v62, v63
	v_cvt_pk_f16_f32 v59, v64, v65
	v_cvt_pk_f16_f32 v60, v60, v61
	v_cvt_pk_f16_f32 v61, v66, v67
	global_store_dwordx4 v[70:71], v[58:61], off sc0 sc1
	global_load_dwordx4 v[58:61], v[80:81], off offset:256
	v_add_u32_e32 v62, 0x90, v164
	v_ashrrev_i32_e32 v63, 31, v62
	v_lshlrev_b64 v[62:63], 10, v[62:63]
	v_lshl_add_u64 v[62:63], v[62:63], 0, v[162:163]
	v_lshlrev_b64 v[62:63], 1, v[62:63]
	v_lshl_add_u64 v[64:65], s[66:67], 0, v[62:63]
	s_waitcnt vmcnt(0)
;     __device__ __forceinline__ void operator()(const Acc& acc, const Unit& u, int wr, int wc, int fr, int fq) const {
;     ...
;             for (int m = 0; m < 4; ++m) { const size_t off = (size_t)(u.pm * BM + ai * HALF + wr * 64 + m * 16 + fr) * DM + col0;
; #pragma unroll
;                 for (int bj = 0; bj < 2; ++bj) { f32x4 b0, b1;
;                     if constexpr (BASE16) { const f16x8 bv = *(const f16x8*)((const f16*)base + off + bj * HALF);
;                         b0 = (f32x4){(float)bv[0], (float)bv[1], (float)bv[2], (float)bv[3]}; b1 = (f32x4){(float)bv[4], (float)bv[5], (float)bv[6], (float)bv[7]}; }
;                     else { b0 = *(const f32x4*)((const float*)base + off + bj * HALF); b1 = *(const f32x4*)((const float*)base + off + bj * HALF + 4); }
;                     const f32x4 v0 = b0 + gv[bj][0] * acc[ai][bj][m][0], v1 = b1 + gv[bj][1] * acc[ai][bj][m][1];
;                     u32x4 w; w.x = pkh(v0[0], v0[1]); w.y = pkh(v0[2], v0[3]); w.z = pkh(v1[0], v1[1]); w.w = pkh(v1[2], v1[3]);
;                     *(u32x4*)(out + off + bj * HALF) = w; }
;                 if (m & 1) asm volatile("" ::: "memory"); }
	v_cvt_f32_f16_e32 v66, v58
	v_cvt_f32_f16_sdwa v67, v58 dst_sel:DWORD dst_unused:UNUSED_PAD src0_sel:WORD_1
	v_cvt_f32_f16_e32 v58, v59
	v_cvt_f32_f16_sdwa v59, v59 dst_sel:DWORD dst_unused:UNUSED_PAD src0_sel:WORD_1
	v_cvt_f32_f16_e32 v68, v60
	v_cvt_f32_f16_e32 v72, v61
	v_cvt_f32_f16_sdwa v73, v61 dst_sel:DWORD dst_unused:UNUSED_PAD src0_sel:WORD_1
	v_cvt_f32_f16_sdwa v69, v60 dst_sel:DWORD dst_unused:UNUSED_PAD src0_sel:WORD_1
	v_pk_fma_f32 v[56:57], v[56:57], v[136:137], v[58:59]
	v_pk_fma_f32 v[54:55], v[54:55], v[134:135], v[66:67]
	v_pk_fma_f32 v[58:59], v[52:53], v[132:133], v[72:73]
	v_pk_fma_f32 v[52:53], v[50:51], v[130:131], v[68:69]
	v_cvt_pk_f16_f32 v50, v54, v55
	v_cvt_pk_f16_f32 v51, v56, v57
	v_cvt_pk_f16_f32 v52, v52, v53
	v_cvt_pk_f16_f32 v53, v58, v59
	global_store_dwordx4 v[70:71], v[50:53], off offset:256 sc0 sc1
	global_load_dwordx4 v[50:53], v[64:65], off
	v_lshl_add_u64 v[54:55], s[8:9], 0, v[62:63]
	s_waitcnt vmcnt(0)
	v_cvt_f32_f16_e32 v56, v50
	v_cvt_f32_f16_sdwa v57, v50 dst_sel:DWORD dst_unused:UNUSED_PAD src0_sel:WORD_1
	v_cvt_f32_f16_e32 v50, v51
	v_cvt_f32_f16_sdwa v51, v51 dst_sel:DWORD dst_unused:UNUSED_PAD src0_sel:WORD_1
	v_cvt_f32_f16_e32 v58, v52
	v_cvt_f32_f16_e32 v60, v53
	v_cvt_f32_f16_sdwa v61, v53 dst_sel:DWORD dst_unused:UNUSED_PAD src0_sel:WORD_1
	v_cvt_f32_f16_sdwa v59, v52 dst_sel:DWORD dst_unused:UNUSED_PAD src0_sel:WORD_1
	v_pk_fma_f32 v[48:49], v[48:49], v[128:129], v[50:51]
	v_pk_fma_f32 v[46:47], v[46:47], v[126:127], v[56:57]
	v_pk_fma_f32 v[50:51], v[44:45], v[124:125], v[60:61]
	v_pk_fma_f32 v[44:45], v[42:43], v[122:123], v[58:59]
	v_cvt_pk_f16_f32 v42, v46, v47
	v_cvt_pk_f16_f32 v43, v48, v49
	v_cvt_pk_f16_f32 v44, v44, v45
	v_cvt_pk_f16_f32 v45, v50, v51
	global_store_dwordx4 v[54:55], v[42:45], off sc0 sc1
	global_load_dwordx4 v[42:45], v[64:65], off offset:256
	v_add_u32_e32 v46, 0xa0, v164
	v_ashrrev_i32_e32 v47, 31, v46
	v_lshlrev_b64 v[46:47], 10, v[46:47]
	v_lshl_add_u64 v[46:47], v[46:47], 0, v[162:163]
	v_lshlrev_b64 v[46:47], 1, v[46:47]
	v_lshl_add_u64 v[48:49], s[66:67], 0, v[46:47]
	s_waitcnt vmcnt(0)
	v_cvt_f32_f16_e32 v50, v42
	v_cvt_f32_f16_sdwa v51, v42 dst_sel:DWORD dst_unused:UNUSED_PAD src0_sel:WORD_1
	v_cvt_f32_f16_e32 v42, v43
	v_cvt_f32_f16_sdwa v43, v43 dst_sel:DWORD dst_unused:UNUSED_PAD src0_sel:WORD_1
	v_cvt_f32_f16_e32 v52, v44
	v_cvt_f32_f16_e32 v56, v45
	v_cvt_f32_f16_sdwa v57, v45 dst_sel:DWORD dst_unused:UNUSED_PAD src0_sel:WORD_1
	v_cvt_f32_f16_sdwa v53, v44 dst_sel:DWORD dst_unused:UNUSED_PAD src0_sel:WORD_1
	v_pk_fma_f32 v[40:41], v[40:41], v[136:137], v[42:43]
	v_pk_fma_f32 v[38:39], v[38:39], v[134:135], v[50:51]
	v_pk_fma_f32 v[42:43], v[36:37], v[132:133], v[56:57]
	v_pk_fma_f32 v[36:37], v[34:35], v[130:131], v[52:53]
	v_cvt_pk_f16_f32 v34, v38, v39
	v_cvt_pk_f16_f32 v35, v40, v41
	v_cvt_pk_f16_f32 v36, v36, v37
	v_cvt_pk_f16_f32 v37, v42, v43
	global_store_dwordx4 v[54:55], v[34:37], off offset:256 sc0 sc1
	global_load_dwordx4 v[34:37], v[48:49], off
	v_lshl_add_u64 v[38:39], s[8:9], 0, v[46:47]
	s_waitcnt vmcnt(0)
	v_cvt_f32_f16_e32 v40, v34
	v_cvt_f32_f16_sdwa v41, v34 dst_sel:DWORD dst_unused:UNUSED_PAD src0_sel:WORD_1
	v_cvt_f32_f16_e32 v34, v35
	v_cvt_f32_f16_sdwa v35, v35 dst_sel:DWORD dst_unused:UNUSED_PAD src0_sel:WORD_1
	v_cvt_f32_f16_e32 v42, v36
	v_cvt_f32_f16_e32 v44, v37
	v_cvt_f32_f16_sdwa v45, v37 dst_sel:DWORD dst_unused:UNUSED_PAD src0_sel:WORD_1
	v_cvt_f32_f16_sdwa v43, v36 dst_sel:DWORD dst_unused:UNUSED_PAD src0_sel:WORD_1
	v_pk_fma_f32 v[32:33], v[32:33], v[128:129], v[34:35]
	v_pk_fma_f32 v[30:31], v[30:31], v[126:127], v[40:41]
	v_pk_fma_f32 v[34:35], v[28:29], v[124:125], v[44:45]
	v_pk_fma_f32 v[28:29], v[26:27], v[122:123], v[42:43]
	v_cvt_pk_f16_f32 v26, v30, v31
	v_cvt_pk_f16_f32 v27, v32, v33
	v_cvt_pk_f16_f32 v28, v28, v29
	v_cvt_pk_f16_f32 v29, v34, v35
	global_store_dwordx4 v[38:39], v[26:29], off sc0 sc1
	global_load_dwordx4 v[26:29], v[48:49], off offset:256
	v_add_u32_e32 v30, 0xb0, v164
	v_ashrrev_i32_e32 v31, 31, v30
	v_lshlrev_b64 v[30:31], 10, v[30:31]
	v_lshl_add_u64 v[30:31], v[30:31], 0, v[162:163]
	v_lshlrev_b64 v[30:31], 1, v[30:31]
	v_lshl_add_u64 v[32:33], s[66:67], 0, v[30:31]
	s_waitcnt vmcnt(0)
	v_cvt_f32_f16_e32 v34, v26
	v_cvt_f32_f16_sdwa v35, v26 dst_sel:DWORD dst_unused:UNUSED_PAD src0_sel:WORD_1
	v_cvt_f32_f16_e32 v26, v27
	v_cvt_f32_f16_sdwa v27, v27 dst_sel:DWORD dst_unused:UNUSED_PAD src0_sel:WORD_1
	v_cvt_f32_f16_e32 v36, v28
	v_cvt_f32_f16_e32 v40, v29
	v_cvt_f32_f16_sdwa v41, v29 dst_sel:DWORD dst_unused:UNUSED_PAD src0_sel:WORD_1
	v_cvt_f32_f16_sdwa v37, v28 dst_sel:DWORD dst_unused:UNUSED_PAD src0_sel:WORD_1
	v_pk_fma_f32 v[24:25], v[24:25], v[136:137], v[26:27]
	v_pk_fma_f32 v[22:23], v[22:23], v[134:135], v[34:35]
	v_pk_fma_f32 v[26:27], v[20:21], v[132:133], v[40:41]
	v_pk_fma_f32 v[20:21], v[18:19], v[130:131], v[36:37]
	v_cvt_pk_f16_f32 v18, v22, v23
	v_cvt_pk_f16_f32 v19, v24, v25
	v_cvt_pk_f16_f32 v20, v20, v21
	v_cvt_pk_f16_f32 v21, v26, v27
	global_store_dwordx4 v[38:39], v[18:21], off offset:256 sc0 sc1
	global_load_dwordx4 v[18:21], v[32:33], off
	v_lshl_add_u64 v[22:23], s[8:9], 0, v[30:31]
	s_waitcnt vmcnt(0)
	v_cvt_f32_f16_e32 v24, v18
	v_cvt_f32_f16_sdwa v25, v18 dst_sel:DWORD dst_unused:UNUSED_PAD src0_sel:WORD_1
	v_cvt_f32_f16_e32 v18, v19
	v_cvt_f32_f16_sdwa v19, v19 dst_sel:DWORD dst_unused:UNUSED_PAD src0_sel:WORD_1
	v_cvt_f32_f16_e32 v26, v20
	v_cvt_f32_f16_e32 v28, v21
	v_cvt_f32_f16_sdwa v29, v21 dst_sel:DWORD dst_unused:UNUSED_PAD src0_sel:WORD_1
	v_cvt_f32_f16_sdwa v27, v20 dst_sel:DWORD dst_unused:UNUSED_PAD src0_sel:WORD_1
	v_pk_fma_f32 v[16:17], v[16:17], v[128:129], v[18:19]
	v_pk_fma_f32 v[14:15], v[14:15], v[126:127], v[24:25]
	v_pk_fma_f32 v[18:19], v[12:13], v[124:125], v[28:29]
	v_pk_fma_f32 v[12:13], v[10:11], v[122:123], v[26:27]
	v_cvt_pk_f16_f32 v10, v14, v15
	v_cvt_pk_f16_f32 v11, v16, v17
	v_cvt_pk_f16_f32 v12, v12, v13
	v_cvt_pk_f16_f32 v13, v18, v19
	global_store_dwordx4 v[22:23], v[10:13], off sc0 sc1
	global_load_dwordx4 v[10:13], v[32:33], off offset:256
	s_waitcnt vmcnt(0)
	v_cvt_f32_f16_e32 v14, v10
	v_cvt_f32_f16_sdwa v15, v10 dst_sel:DWORD dst_unused:UNUSED_PAD src0_sel:WORD_1
	v_cvt_f32_f16_e32 v10, v11
	v_cvt_f32_f16_sdwa v11, v11 dst_sel:DWORD dst_unused:UNUSED_PAD src0_sel:WORD_1
	v_cvt_f32_f16_e32 v16, v12
	v_cvt_f32_f16_e32 v18, v13
	v_cvt_f32_f16_sdwa v19, v13 dst_sel:DWORD dst_unused:UNUSED_PAD src0_sel:WORD_1
	v_cvt_f32_f16_sdwa v17, v12 dst_sel:DWORD dst_unused:UNUSED_PAD src0_sel:WORD_1
	v_pk_fma_f32 v[8:9], v[8:9], v[136:137], v[10:11]
	v_pk_fma_f32 v[6:7], v[6:7], v[134:135], v[14:15]
	v_pk_fma_f32 v[10:11], v[4:5], v[132:133], v[18:19]
	v_pk_fma_f32 v[4:5], v[2:3], v[130:131], v[16:17]
	v_cvt_pk_f16_f32 v2, v6, v7
	v_cvt_pk_f16_f32 v3, v8, v9
	v_cvt_pk_f16_f32 v4, v4, v5
	v_cvt_pk_f16_f32 v5, v10, v11
	global_store_dwordx4 v[22:23], v[2:5], off offset:256 sc0 sc1
	s_cbranch_vccnz .LBB0_1472
	s_andn2_b64 vcc, exec, s[6:7]
	s_cbranch_vccnz .LBB0_1471
	s_barrier
	s_branch .LBB0_1471
